# v27: v10 + static-priority lever: per-segment s_setprio flips of all GEMM mainloops replaced by s_nop 0, one static s_setprio 1 for waves 4-7 for the whole launch; scan state waves at prio 3
# baseline (speedup 1.0000x reference)
.LBB0_285:
	s_cmp_lt_i32 s72, 2
	s_cselect_b64 s[12:13], -1, 0
	s_and_b64 s[4:5], s[12:13], s[4:5]
	s_andn2_b64 vcc, exec, s[4:5]
	s_lshr_b32 s82, s97, 6
	s_cmp_lt_u32 s82, 4
	s_cbranch_scc1 .Lprio_done
	s_setprio 1
.Lprio_done:
	s_cbranch_vccnz .LBB0_354
	s_load_dwordx2 s[4:5], s[74:75], 0x0
	s_load_dwordx2 s[6:7], s[74:75], 0x10
	v_mov_b32_e32 v1, v0
	s_movk_i32 s0, 0x600
	s_nop 0
	v_cmp_gt_i32_e32 vcc, s0, v1
	s_and_saveexec_b64 s[8:9], vcc
	s_cbranch_execz .LBB0_289
	s_load_dwordx2 s[10:11], s[74:75], 0x30
	s_waitcnt lgkmcnt(0)
	s_add_u32 s14, s54, 0x100000
	s_addc_u32 s15, s55, 0
	v_lshl_add_u32 v2, v1, 4, 0
	v_lshlrev_b32_e32 v3, 2, v1
	s_mov_b64 s[16:17], 0
	s_movk_i32 s3, 0x2000
	s_movk_i32 s18, 0x3ff

.LBB0_422:
	s_add_u32 s24, s6, 0x100
	s_addc_u32 s25, s7, 0
	s_add_u32 s0, s49, s6
	ds_read_b128 v[164:167], v156
	ds_read_b128 v[168:171], v156 offset:1024
	ds_read_b128 v[172:175], v156 offset:2048
	ds_read_b128 v[176:179], v156 offset:3072
	s_addc_u32 s1, s50, s7
	s_cmpk_eq_i32 s6, 0xf00
	s_cselect_b64 vcc, -1, 0
	s_and_b64 s[26:27], vcc, exec
	s_cselect_b32 s28, 0, s24
	s_cselect_b32 s29, 0, s25
	s_cselect_b32 s26, s48, s0
	s_cselect_b32 s27, s21, s1
	s_add_u32 s28, s10, s28
	v_cndmask_b32_e32 v136, v163, v159, vcc
	v_cndmask_b32_e32 v145, v144, v160, vcc
	v_cndmask_b32_e32 v230, v142, v161, vcc
	v_cndmask_b32_e32 v147, v146, v162, vcc
	s_addc_u32 s29, s11, s29
	v_lshl_add_u64 v[214:215], v[148:149], 0, s[6:7]
	s_add_i32 m0, s19, 0xc000
	ds_read_b128 v[180:183], v157
	ds_read_b128 v[184:187], v157 offset:1024
	ds_read_b128 v[190:193], v157 offset:2048
	ds_read_b128 v[194:197], v157 offset:3072
	ds_read_b128 v[198:201], v157 offset:4096
	ds_read_b128 v[202:205], v157 offset:5120
	ds_read_b128 v[206:209], v157 offset:6144
	ds_read_b128 v[210:213], v157 offset:7168
	global_load_lds_dwordx4 v[214:215], off
	v_lshl_add_u64 v[214:215], v[150:151], 0, s[6:7]
	s_add_i32 m0, s19, 0xe000
	s_nop 0
	global_load_lds_dwordx4 v[214:215], off
	s_waitcnt lgkmcnt(8)
	s_barrier
	s_waitcnt lgkmcnt(0)
	s_nop 0
	s_waitcnt lgkmcnt(0)
	v_mfma_f32_16x16x32_bf16 v[126:129], v[164:167], v[180:183], v[126:129]
	v_mfma_f32_16x16x32_bf16 v[122:125], v[172:175], v[180:183], v[122:125]
	v_mfma_f32_16x16x32_bf16 v[118:121], v[164:167], v[190:193], v[118:121]
	v_mfma_f32_16x16x32_bf16 v[114:117], v[172:175], v[190:193], v[114:117]
	v_mfma_f32_16x16x32_bf16 v[110:113], v[164:167], v[198:201], v[110:113]
	v_mfma_f32_16x16x32_bf16 v[106:109], v[172:175], v[198:201], v[106:109]
	v_mfma_f32_16x16x32_bf16 v[102:105], v[164:167], v[206:209], v[102:105]
	v_mfma_f32_16x16x32_bf16 v[98:101], v[172:175], v[206:209], v[98:101]
	v_mfma_f32_16x16x32_bf16 v[126:129], v[168:171], v[184:187], v[126:129]
	v_mfma_f32_16x16x32_bf16 v[122:125], v[176:179], v[184:187], v[122:125]
	v_mfma_f32_16x16x32_bf16 v[118:121], v[168:171], v[194:197], v[118:121]
	v_mfma_f32_16x16x32_bf16 v[114:117], v[176:179], v[194:197], v[114:117]
	v_mfma_f32_16x16x32_bf16 v[110:113], v[168:171], v[202:205], v[110:113]
	v_mfma_f32_16x16x32_bf16 v[106:109], v[176:179], v[202:205], v[106:109]
	v_mfma_f32_16x16x32_bf16 v[102:105], v[168:171], v[210:213], v[102:105]
	v_mfma_f32_16x16x32_bf16 v[98:101], v[176:179], v[210:213], v[98:101]
	s_nop 0
	s_barrier
	s_add_i32 s0, s43, s35
	v_lshl_add_u64 v[232:233], s[26:27], 0, v[132:133]
	s_mov_b32 m0, s0
	ds_read_b128 v[214:217], v158
	ds_read_b128 v[218:221], v158 offset:1024
	ds_read_b128 v[222:225], v158 offset:2048
	ds_read_b128 v[226:229], v158 offset:3072
	global_load_lds_dwordx4 v[232:233], off
	v_lshl_add_u64 v[234:235], s[26:27], 0, v[134:135]
	s_add_i32 m0, s0, 0x2000
	s_nop 0
	global_load_lds_dwordx4 v[234:235], off
	s_barrier
	s_waitcnt lgkmcnt(0)
	s_nop 0
	s_waitcnt lgkmcnt(0)
	v_mfma_f32_16x16x32_bf16 v[90:93], v[214:217], v[180:183], v[90:93]
	v_mfma_f32_16x16x32_bf16 v[82:85], v[222:225], v[180:183], v[82:85]
	v_mfma_f32_16x16x32_bf16 v[74:77], v[214:217], v[190:193], v[74:77]
	v_mfma_f32_16x16x32_bf16 v[62:65], v[222:225], v[190:193], v[62:65]
	v_mfma_f32_16x16x32_bf16 v[46:49], v[214:217], v[198:201], v[46:49]
	v_mfma_f32_16x16x32_bf16 v[38:41], v[222:225], v[198:201], v[38:41]
	v_mfma_f32_16x16x32_bf16 v[30:33], v[214:217], v[206:209], v[30:33]
	v_mfma_f32_16x16x32_bf16 v[22:25], v[222:225], v[206:209], v[22:25]
	v_mfma_f32_16x16x32_bf16 v[90:93], v[218:221], v[184:187], v[90:93]
	v_mfma_f32_16x16x32_bf16 v[82:85], v[226:229], v[184:187], v[82:85]
	v_mfma_f32_16x16x32_bf16 v[74:77], v[218:221], v[194:197], v[74:77]
	v_mfma_f32_16x16x32_bf16 v[62:65], v[226:229], v[194:197], v[62:65]
	v_mfma_f32_16x16x32_bf16 v[46:49], v[218:221], v[202:205], v[46:49]
	v_mfma_f32_16x16x32_bf16 v[38:41], v[226:229], v[202:205], v[38:41]
	v_mfma_f32_16x16x32_bf16 v[30:33], v[218:221], v[210:213], v[30:33]
	v_mfma_f32_16x16x32_bf16 v[22:25], v[226:229], v[210:213], v[22:25]
	s_nop 0
	s_mov_b32 m0, s19
	s_barrier
	ds_read_b128 v[180:183], v157 offset:16384
	ds_read_b128 v[184:187], v157 offset:17408
	ds_read_b128 v[190:193], v157 offset:18432
	ds_read_b128 v[194:197], v157 offset:19456
	ds_read_b128 v[198:201], v157 offset:20480
	ds_read_b128 v[202:205], v157 offset:21504
	ds_read_b128 v[206:209], v157 offset:22528
	ds_read_b128 v[210:213], v157 offset:23552
	global_load_lds_dwordx4 v136, s[28:29]
	s_mov_b32 m0, s36
	v_mov_b32_e32 v231, v137
	global_load_lds_dwordx4 v230, s[28:29]
	s_barrier
	s_waitcnt lgkmcnt(0)
	v_lshl_add_u64 v[236:237], s[28:29], 0, v[136:137]
	v_lshl_add_u64 v[230:231], s[28:29], 0, v[230:231]
	s_nop 0
	s_waitcnt lgkmcnt(0)
	v_mfma_f32_16x16x32_bf16 v[94:97], v[164:167], v[180:183], v[94:97]
	v_mfma_f32_16x16x32_bf16 v[86:89], v[172:175], v[180:183], v[86:89]
	v_mfma_f32_16x16x32_bf16 v[78:81], v[164:167], v[190:193], v[78:81]
	v_mfma_f32_16x16x32_bf16 v[70:73], v[172:175], v[190:193], v[70:73]
	v_mfma_f32_16x16x32_bf16 v[42:45], v[164:167], v[198:201], v[42:45]
	v_mfma_f32_16x16x32_bf16 v[34:37], v[172:175], v[198:201], v[34:37]
	v_mfma_f32_16x16x32_bf16 v[26:29], v[164:167], v[206:209], v[26:29]
	v_mfma_f32_16x16x32_bf16 v[18:21], v[172:175], v[206:209], v[18:21]
	v_mfma_f32_16x16x32_bf16 v[94:97], v[168:171], v[184:187], v[94:97]
	v_mfma_f32_16x16x32_bf16 v[86:89], v[176:179], v[184:187], v[86:89]
	v_mfma_f32_16x16x32_bf16 v[78:81], v[168:171], v[194:197], v[78:81]
	v_mfma_f32_16x16x32_bf16 v[70:73], v[176:179], v[194:197], v[70:73]
	v_mfma_f32_16x16x32_bf16 v[42:45], v[168:171], v[202:205], v[42:45]
	v_mfma_f32_16x16x32_bf16 v[34:37], v[176:179], v[202:205], v[34:37]
	v_mfma_f32_16x16x32_bf16 v[26:29], v[168:171], v[210:213], v[26:29]
	v_mfma_f32_16x16x32_bf16 v[18:21], v[176:179], v[210:213], v[18:21]
	s_nop 0
	s_barrier
	s_add_u32 s6, s26, 0x80000
	s_addc_u32 s7, s27, 0
	s_add_i32 s0, s44, s35
	v_lshl_add_u64 v[164:165], s[6:7], 0, v[132:133]
	s_mov_b32 m0, s0
	s_nop 0
	global_load_lds_dwordx4 v[164:165], off
	v_lshl_add_u64 v[164:165], s[6:7], 0, v[134:135]
	s_add_i32 m0, s0, 0x2000
	s_nop 0
	global_load_lds_dwordx4 v[164:165], off
	s_waitcnt vmcnt(6)
	s_barrier
	s_nop 0
	v_mfma_f32_16x16x32_bf16 v[14:17], v[214:217], v[180:183], v[14:17]
	v_mfma_f32_16x16x32_bf16 v[10:13], v[222:225], v[180:183], v[10:13]
	v_mfma_f32_16x16x32_bf16 v[6:9], v[214:217], v[190:193], v[6:9]
	v_mfma_f32_16x16x32_bf16 v[2:5], v[222:225], v[190:193], v[2:5]
	v_mfma_f32_16x16x32_bf16 v[54:57], v[214:217], v[198:201], v[54:57]
	v_mfma_f32_16x16x32_bf16 v[66:69], v[222:225], v[198:201], v[66:69]
	v_mfma_f32_16x16x32_bf16 v[50:53], v[214:217], v[206:209], v[50:53]
	v_mfma_f32_16x16x32_bf16 v[58:61], v[222:225], v[206:209], v[58:61]
	v_mfma_f32_16x16x32_bf16 v[14:17], v[218:221], v[184:187], v[14:17]
	v_mfma_f32_16x16x32_bf16 v[10:13], v[226:229], v[184:187], v[10:13]
	v_mfma_f32_16x16x32_bf16 v[6:9], v[218:221], v[194:197], v[6:9]
	v_mfma_f32_16x16x32_bf16 v[2:5], v[226:229], v[194:197], v[2:5]
	v_mfma_f32_16x16x32_bf16 v[54:57], v[218:221], v[202:205], v[54:57]
	v_mfma_f32_16x16x32_bf16 v[66:69], v[226:229], v[202:205], v[66:69]
	v_mfma_f32_16x16x32_bf16 v[50:53], v[218:221], v[210:213], v[50:53]
	v_mfma_f32_16x16x32_bf16 v[58:61], v[226:229], v[210:213], v[58:61]
	s_nop 0
	s_add_i32 s0, 0, 0x18000
	v_add_u32_e32 v136, s0, v154
	s_barrier
	ds_read_b128 v[164:167], v136
	ds_read_b128 v[168:171], v136 offset:1024
	ds_read_b128 v[172:175], v136 offset:2048
	ds_read_b128 v[176:179], v136 offset:3072
	s_mov_b32 m0, s37
	ds_read_b128 v[180:183], v157 offset:32768
	ds_read_b128 v[184:187], v157 offset:33792
	ds_read_b128 v[190:193], v157 offset:34816
	ds_read_b128 v[194:197], v157 offset:35840
	ds_read_b128 v[198:201], v157 offset:36864
	ds_read_b128 v[202:205], v157 offset:37888
	ds_read_b128 v[206:209], v157 offset:38912
	ds_read_b128 v[210:213], v157 offset:39936
	global_load_lds_dwordx4 v145, s[28:29]
	s_mov_b32 m0, s38
	s_nop 0
	global_load_lds_dwordx4 v147, s[28:29]
	s_waitcnt lgkmcnt(8)
	s_barrier
	s_waitcnt lgkmcnt(0)
	s_nop 0
	s_waitcnt lgkmcnt(0)
	v_mfma_f32_16x16x32_bf16 v[126:129], v[164:167], v[180:183], v[126:129]
	v_mfma_f32_16x16x32_bf16 v[122:125], v[172:175], v[180:183], v[122:125]
	v_mfma_f32_16x16x32_bf16 v[118:121], v[164:167], v[190:193], v[118:121]
	v_mfma_f32_16x16x32_bf16 v[114:117], v[172:175], v[190:193], v[114:117]
	v_mfma_f32_16x16x32_bf16 v[110:113], v[164:167], v[198:201], v[110:113]
	v_mfma_f32_16x16x32_bf16 v[106:109], v[172:175], v[198:201], v[106:109]
	v_mfma_f32_16x16x32_bf16 v[102:105], v[164:167], v[206:209], v[102:105]
	v_mfma_f32_16x16x32_bf16 v[98:101], v[172:175], v[206:209], v[98:101]
	v_mfma_f32_16x16x32_bf16 v[126:129], v[168:171], v[184:187], v[126:129]
	v_mfma_f32_16x16x32_bf16 v[122:125], v[176:179], v[184:187], v[122:125]
	v_mfma_f32_16x16x32_bf16 v[118:121], v[168:171], v[194:197], v[118:121]
	v_mfma_f32_16x16x32_bf16 v[114:117], v[176:179], v[194:197], v[114:117]
	v_mfma_f32_16x16x32_bf16 v[110:113], v[168:171], v[202:205], v[110:113]
	v_mfma_f32_16x16x32_bf16 v[106:109], v[176:179], v[202:205], v[106:109]
	v_mfma_f32_16x16x32_bf16 v[102:105], v[168:171], v[210:213], v[102:105]
	v_mfma_f32_16x16x32_bf16 v[98:101], v[176:179], v[210:213], v[98:101]
	s_nop 0
	s_barrier
	s_add_i32 s1, 0, 0x1c000
	s_add_i32 s0, s0, s35
	v_add_u32_e32 v136, s1, v154
	v_lshl_add_u64 v[232:233], v[232:233], 0, s[14:15]
	s_mov_b32 m0, s0
	ds_read_b128 v[214:217], v136
	ds_read_b128 v[218:221], v136 offset:1024
	ds_read_b128 v[222:225], v136 offset:2048
	ds_read_b128 v[226:229], v136 offset:3072
	global_load_lds_dwordx4 v[232:233], off
	v_lshl_add_u64 v[232:233], v[234:235], 0, s[14:15]
	s_add_i32 m0, s0, 0x2000
	s_nop 0
	global_load_lds_dwordx4 v[232:233], off
	s_barrier
	s_waitcnt lgkmcnt(0)
	s_nop 0
	s_waitcnt lgkmcnt(0)
	v_mfma_f32_16x16x32_bf16 v[90:93], v[214:217], v[180:183], v[90:93]
	v_mfma_f32_16x16x32_bf16 v[82:85], v[222:225], v[180:183], v[82:85]
	v_mfma_f32_16x16x32_bf16 v[74:77], v[214:217], v[190:193], v[74:77]
	v_mfma_f32_16x16x32_bf16 v[62:65], v[222:225], v[190:193], v[62:65]
	v_mfma_f32_16x16x32_bf16 v[46:49], v[214:217], v[198:201], v[46:49]
	v_mfma_f32_16x16x32_bf16 v[38:41], v[222:225], v[198:201], v[38:41]
	v_mfma_f32_16x16x32_bf16 v[30:33], v[214:217], v[206:209], v[30:33]
	v_mfma_f32_16x16x32_bf16 v[22:25], v[222:225], v[206:209], v[22:25]
	v_mfma_f32_16x16x32_bf16 v[90:93], v[218:221], v[184:187], v[90:93]
	v_mfma_f32_16x16x32_bf16 v[82:85], v[226:229], v[184:187], v[82:85]
	v_mfma_f32_16x16x32_bf16 v[74:77], v[218:221], v[194:197], v[74:77]
	v_mfma_f32_16x16x32_bf16 v[62:65], v[226:229], v[194:197], v[62:65]
	v_mfma_f32_16x16x32_bf16 v[46:49], v[218:221], v[202:205], v[46:49]
	v_mfma_f32_16x16x32_bf16 v[38:41], v[226:229], v[202:205], v[38:41]
	v_mfma_f32_16x16x32_bf16 v[30:33], v[218:221], v[210:213], v[30:33]
	v_mfma_f32_16x16x32_bf16 v[22:25], v[226:229], v[210:213], v[22:25]
	s_nop 0
	s_mov_b32 m0, s40
	v_lshl_add_u64 v[232:233], v[236:237], 0, s[14:15]
	s_barrier
	ds_read_b128 v[180:183], v157 offset:49152
	ds_read_b128 v[184:187], v157 offset:50176
	ds_read_b128 v[190:193], v157 offset:51200
	ds_read_b128 v[194:197], v157 offset:52224
	ds_read_b128 v[198:201], v157 offset:53248
	ds_read_b128 v[202:205], v157 offset:54272
	ds_read_b128 v[206:209], v157 offset:55296
	ds_read_b128 v[210:213], v157 offset:56320
	global_load_lds_dwordx4 v[232:233], off
	v_lshl_add_u64 v[230:231], v[230:231], 0, s[14:15]
	s_mov_b32 m0, s41
	s_nop 0
	global_load_lds_dwordx4 v[230:231], off
	s_barrier
	s_waitcnt lgkmcnt(0)
	s_nop 0
	s_waitcnt lgkmcnt(0)
	v_mfma_f32_16x16x32_bf16 v[94:97], v[164:167], v[180:183], v[94:97]
	v_mfma_f32_16x16x32_bf16 v[86:89], v[172:175], v[180:183], v[86:89]
	v_mfma_f32_16x16x32_bf16 v[78:81], v[164:167], v[190:193], v[78:81]
	v_mfma_f32_16x16x32_bf16 v[70:73], v[172:175], v[190:193], v[70:73]
	v_mfma_f32_16x16x32_bf16 v[42:45], v[164:167], v[198:201], v[42:45]
	v_mfma_f32_16x16x32_bf16 v[34:37], v[172:175], v[198:201], v[34:37]
	v_mfma_f32_16x16x32_bf16 v[26:29], v[164:167], v[206:209], v[26:29]
	v_mfma_f32_16x16x32_bf16 v[18:21], v[172:175], v[206:209], v[18:21]
	v_mfma_f32_16x16x32_bf16 v[94:97], v[168:171], v[184:187], v[94:97]
	v_mfma_f32_16x16x32_bf16 v[86:89], v[176:179], v[184:187], v[86:89]
	v_mfma_f32_16x16x32_bf16 v[78:81], v[168:171], v[194:197], v[78:81]
	v_mfma_f32_16x16x32_bf16 v[70:73], v[176:179], v[194:197], v[70:73]
	v_mfma_f32_16x16x32_bf16 v[42:45], v[168:171], v[202:205], v[42:45]
	v_mfma_f32_16x16x32_bf16 v[34:37], v[176:179], v[202:205], v[34:37]
	v_mfma_f32_16x16x32_bf16 v[26:29], v[168:171], v[210:213], v[26:29]
	v_mfma_f32_16x16x32_bf16 v[18:21], v[176:179], v[210:213], v[18:21]
	s_nop 0
	s_barrier
	s_add_u32 s6, s26, 0x80080
	s_addc_u32 s7, s27, 0
	s_add_i32 s0, s1, s35
	v_lshl_add_u64 v[164:165], s[6:7], 0, v[132:133]
	s_mov_b32 m0, s0
	s_nop 0
	global_load_lds_dwordx4 v[164:165], off
	v_lshl_add_u64 v[164:165], s[6:7], 0, v[134:135]
	s_add_i32 m0, s0, 0x2000
	s_nop 0
	global_load_lds_dwordx4 v[164:165], off
	s_waitcnt vmcnt(6)
	s_barrier
	s_nop 0
	v_mfma_f32_16x16x32_bf16 v[14:17], v[214:217], v[180:183], v[14:17]
	v_mfma_f32_16x16x32_bf16 v[10:13], v[222:225], v[180:183], v[10:13]
	v_mfma_f32_16x16x32_bf16 v[6:9], v[214:217], v[190:193], v[6:9]
	v_mfma_f32_16x16x32_bf16 v[2:5], v[222:225], v[190:193], v[2:5]
	v_mfma_f32_16x16x32_bf16 v[54:57], v[214:217], v[198:201], v[54:57]
	v_mfma_f32_16x16x32_bf16 v[66:69], v[222:225], v[198:201], v[66:69]
	v_mfma_f32_16x16x32_bf16 v[50:53], v[214:217], v[206:209], v[50:53]
	v_mfma_f32_16x16x32_bf16 v[58:61], v[222:225], v[206:209], v[58:61]
	v_mfma_f32_16x16x32_bf16 v[14:17], v[218:221], v[184:187], v[14:17]
	v_mfma_f32_16x16x32_bf16 v[10:13], v[226:229], v[184:187], v[10:13]
	v_mfma_f32_16x16x32_bf16 v[6:9], v[218:221], v[194:197], v[6:9]
	v_mfma_f32_16x16x32_bf16 v[2:5], v[226:229], v[194:197], v[2:5]
	v_mfma_f32_16x16x32_bf16 v[54:57], v[218:221], v[202:205], v[54:57]
	v_mfma_f32_16x16x32_bf16 v[66:69], v[226:229], v[202:205], v[66:69]
	v_mfma_f32_16x16x32_bf16 v[50:53], v[218:221], v[210:213], v[50:53]
	v_mfma_f32_16x16x32_bf16 v[58:61], v[226:229], v[210:213], v[58:61]
	s_nop 0
	s_add_i32 s51, s51, 2
	s_cmp_gt_u32 s51, 29
	s_mov_b64 s[6:7], s[24:25]
	s_barrier
	s_cbranch_scc0 .LBB0_422
	v_add_u32_e32 v144, s18, v155
	v_ashrrev_i32_e32 v145, 31, v144
	v_add_u32_e32 v136, s46, v143
	v_lshl_add_u64 v[144:145], v[144:145], 1, s[12:13]
	v_cvt_pk_bf16_f32 v126, v126, v127
	v_cvt_pk_bf16_f32 v127, v128, v129
	v_cvt_pk_bf16_f32 v128, v122, v123
	v_cvt_pk_bf16_f32 v129, v124, v125
	v_mad_i64_i32 v[122:123], s[6:7], v136, s45, v[144:145]
	v_add_u32_e32 v124, 16, v136
	v_cvt_pk_bf16_f32 v26, v26, v27
	v_cvt_pk_bf16_f32 v27, v28, v29
	v_cvt_pk_bf16_f32 v28, v18, v19
	v_cvt_pk_bf16_f32 v29, v20, v21
	v_cvt_pk_bf16_f32 v18, v90, v91
	v_cvt_pk_bf16_f32 v19, v92, v93
	v_cvt_pk_bf16_f32 v20, v82, v83
	v_cvt_pk_bf16_f32 v21, v84, v85
	v_cvt_pk_bf16_f32 v118, v118, v119
	v_cvt_pk_bf16_f32 v119, v120, v121
	v_cvt_pk_bf16_f32 v120, v114, v115
	v_cvt_pk_bf16_f32 v121, v116, v117
	v_mad_i64_i32 v[114:115], s[6:7], v124, s45, v[144:145]
	v_add_u32_e32 v116, 32, v136
	v_cvt_pk_bf16_f32 v78, v78, v79
	v_cvt_pk_bf16_f32 v79, v80, v81
	v_cvt_pk_bf16_f32 v81, v72, v73
	v_add_u32_e32 v72, 0xa0, v136
	global_store_dwordx4 v[122:123], v[18:21], off offset:256
	v_add_u32_e32 v142, 0x80, v136
	v_cvt_pk_bf16_f32 v110, v110, v111
	v_cvt_pk_bf16_f32 v18, v74, v75
	v_cvt_pk_bf16_f32 v19, v76, v77
	v_cvt_pk_bf16_f32 v20, v62, v63
	v_cvt_pk_bf16_f32 v21, v64, v65
	v_cvt_pk_bf16_f32 v111, v112, v113
	v_cvt_pk_bf16_f32 v112, v106, v107
	v_cvt_pk_bf16_f32 v113, v108, v109
	v_mad_i64_i32 v[106:107], s[6:7], v116, s45, v[144:145]
	v_add_u32_e32 v108, 48, v136
	v_cvt_pk_bf16_f32 v94, v94, v95
	v_cvt_pk_bf16_f32 v95, v96, v97
	v_cvt_pk_bf16_f32 v97, v88, v89
	v_add_u32_e32 v88, 0x90, v136
	v_cvt_pk_bf16_f32 v42, v42, v43
	v_cvt_pk_bf16_f32 v43, v44, v45
	v_cvt_pk_bf16_f32 v44, v34, v35
	v_cvt_pk_bf16_f32 v45, v36, v37
	v_mad_i64_i32 v[34:35], s[6:7], v72, s45, v[144:145]
	v_add_u32_e32 v36, 0xb0, v136
	global_store_dwordx4 v[114:115], v[18:21], off offset:256
	v_cvt_pk_bf16_f32 v6, v6, v7
	v_cvt_pk_bf16_f32 v7, v8, v9
	v_cvt_pk_bf16_f32 v18, v46, v47
	v_cvt_pk_bf16_f32 v19, v48, v49
	v_cvt_pk_bf16_f32 v20, v38, v39
	v_cvt_pk_bf16_f32 v21, v40, v41
	v_cvt_pk_bf16_f32 v8, v2, v3
	v_cvt_pk_bf16_f32 v9, v4, v5
	v_cvt_pk_bf16_f32 v2, v54, v55
	v_cvt_pk_bf16_f32 v3, v56, v57
	v_cvt_pk_bf16_f32 v4, v66, v67
	v_cvt_pk_bf16_f32 v5, v68, v69
	v_cvt_pk_bf16_f32 v102, v102, v103
	v_cvt_pk_bf16_f32 v103, v104, v105
	v_cvt_pk_bf16_f32 v104, v98, v99
	v_cvt_pk_bf16_f32 v105, v100, v101
	v_mad_i64_i32 v[98:99], s[6:7], v108, s45, v[144:145]
	v_cvt_pk_bf16_f32 v96, v86, v87
	v_mad_i64_i32 v[86:87], s[6:7], v142, s45, v[144:145]
	v_cvt_pk_bf16_f32 v80, v70, v71
	v_mad_i64_i32 v[70:71], s[6:7], v88, s45, v[144:145]
	v_mad_i64_i32 v[36:37], s[6:7], v36, s45, v[144:145]
	global_store_dwordx4 v[106:107], v[18:21], off offset:256
	v_cvt_pk_bf16_f32 v14, v14, v15
	v_cvt_pk_bf16_f32 v15, v16, v17
	v_cvt_pk_bf16_f32 v18, v30, v31
	v_cvt_pk_bf16_f32 v19, v32, v33
	v_cvt_pk_bf16_f32 v20, v22, v23
	v_cvt_pk_bf16_f32 v21, v24, v25
	v_cvt_pk_bf16_f32 v16, v10, v11
	v_cvt_pk_bf16_f32 v17, v12, v13
	global_store_dwordx4 v[34:35], v[2:5], off offset:256
	s_and_b64 vcc, exec, s[4:5]
	v_mov_b32_e32 v142, v161
	v_cvt_pk_bf16_f32 v2, v50, v51
	v_cvt_pk_bf16_f32 v3, v52, v53
	v_cvt_pk_bf16_f32 v4, v58, v59
	v_cvt_pk_bf16_f32 v5, v60, v61
	v_mov_b32_e32 v163, v159
	v_mov_b32_e32 v146, v162
	v_mov_b32_e32 v144, v160
	s_mov_b32 s18, s20
	s_mov_b32 s46, s47
	s_mov_b64 s[24:25], s[22:23]
	global_store_dwordx4 v[122:123], v[126:129], off
	global_store_dwordx4 v[114:115], v[118:121], off
	global_store_dwordx4 v[106:107], v[110:113], off
	global_store_dwordx4 v[98:99], v[102:105], off
	global_store_dwordx4 v[86:87], v[94:97], off
	global_store_dwordx4 v[70:71], v[78:81], off
	global_store_dwordx4 v[34:35], v[42:45], off
	global_store_dwordx4 v[36:37], v[26:29], off
	global_store_dwordx4 v[98:99], v[18:21], off offset:256
	global_store_dwordx4 v[86:87], v[14:17], off offset:256
	global_store_dwordx4 v[70:71], v[6:9], off offset:256
	global_store_dwordx4 v[36:37], v[2:5], off offset:256
	s_cbranch_vccz .LBB0_413
	s_waitcnt vmcnt(0)
	s_cmpk_gt_u32 s3, 0xff
	s_cbranch_scc1 .LBB0_426
	s_barrier

.LBB0_709:
	s_add_u32 s0, s54, s6
	s_addc_u32 s1, s55, s7
	s_add_u32 s0, s0, 0x29400100
	ds_read_b128 v[140:143], v167
	ds_read_b128 v[158:161], v167 offset:1024
	ds_read_b128 v[174:177], v167 offset:2048
	ds_read_b128 v[178:181], v167 offset:3072
	s_addc_u32 s1, s1, 0
	s_add_u32 s58, s51, s6
	s_addc_u32 s59, s56, s7
	s_cmpk_eq_i32 s6, 0xf00
	s_cselect_b64 vcc, -1, 0
	s_and_b64 s[26:27], vcc, exec
	v_cndmask_b32_e32 v152, v131, v170, vcc
	s_cselect_b32 s29, s11, s1
	s_cselect_b32 s28, s10, s0
	v_cndmask_b32_e32 v133, v132, v171, vcc
	v_cndmask_b32_e32 v144, v130, v172, vcc
	v_cndmask_b32_e32 v135, v134, v173, vcc
	s_cselect_b32 s27, s21, s59
	s_cselect_b32 s26, s50, s58
	v_lshl_add_u64 v[186:187], v[138:139], 0, s[6:7]
	s_add_i32 m0, s25, 0xc000
	ds_read_b128 v[182:185], v168
	ds_read_b128 v[190:193], v168 offset:1024
	ds_read_b128 v[194:197], v168 offset:2048
	ds_read_b128 v[198:201], v168 offset:3072
	ds_read_b128 v[202:205], v168 offset:4096
	ds_read_b128 v[206:209], v168 offset:5120
	ds_read_b128 v[210:213], v168 offset:6144
	ds_read_b128 v[214:217], v168 offset:7168
	global_load_lds_dwordx4 v[186:187], off
	v_lshl_add_u64 v[186:187], v[136:137], 0, s[6:7]
	s_add_i32 m0, s25, 0xe000
	s_nop 0
	global_load_lds_dwordx4 v[186:187], off
	s_waitcnt lgkmcnt(8)
	s_barrier
	s_waitcnt lgkmcnt(0)
	s_nop 0
	s_waitcnt lgkmcnt(0)
	v_mfma_f32_16x16x32_bf16 v[126:129], v[140:143], v[182:185], v[126:129]
	v_mfma_f32_16x16x32_bf16 v[122:125], v[174:177], v[182:185], v[122:125]
	v_mfma_f32_16x16x32_bf16 v[114:117], v[140:143], v[194:197], v[114:117]
	v_mfma_f32_16x16x32_bf16 v[110:113], v[174:177], v[194:197], v[110:113]
	v_mfma_f32_16x16x32_bf16 v[102:105], v[140:143], v[202:205], v[102:105]
	v_mfma_f32_16x16x32_bf16 v[94:97], v[174:177], v[202:205], v[94:97]
	v_mfma_f32_16x16x32_bf16 v[86:89], v[140:143], v[210:213], v[86:89]
	v_mfma_f32_16x16x32_bf16 v[78:81], v[174:177], v[210:213], v[78:81]
	v_mfma_f32_16x16x32_bf16 v[126:129], v[158:161], v[190:193], v[126:129]
	v_mfma_f32_16x16x32_bf16 v[122:125], v[178:181], v[190:193], v[122:125]
	v_mfma_f32_16x16x32_bf16 v[114:117], v[158:161], v[198:201], v[114:117]
	v_mfma_f32_16x16x32_bf16 v[110:113], v[178:181], v[198:201], v[110:113]
	v_mfma_f32_16x16x32_bf16 v[102:105], v[158:161], v[206:209], v[102:105]
	v_mfma_f32_16x16x32_bf16 v[94:97], v[178:181], v[206:209], v[94:97]
	v_mfma_f32_16x16x32_bf16 v[86:89], v[158:161], v[214:217], v[86:89]
	v_mfma_f32_16x16x32_bf16 v[78:81], v[178:181], v[214:217], v[78:81]
	s_nop 0
	s_barrier
	s_add_i32 s0, s46, s34
	v_lshl_add_u64 v[186:187], s[26:27], 0, v[150:151]
	s_mov_b32 m0, s0
	ds_read_b128 v[218:221], v169
	ds_read_b128 v[222:225], v169 offset:1024
	ds_read_b128 v[226:229], v169 offset:2048
	ds_read_b128 v[230:233], v169 offset:3072
	global_load_lds_dwordx4 v[186:187], off
	v_lshl_add_u64 v[234:235], s[26:27], 0, v[148:149]
	s_add_i32 m0, s0, 0x2000
	s_nop 0
	global_load_lds_dwordx4 v[234:235], off
	s_barrier
	s_waitcnt lgkmcnt(0)
	s_nop 0
	s_waitcnt lgkmcnt(0)
	v_mfma_f32_16x16x32_bf16 v[118:121], v[218:221], v[182:185], v[118:121]
	v_mfma_f32_16x16x32_bf16 v[106:109], v[226:229], v[182:185], v[106:109]
	v_mfma_f32_16x16x32_bf16 v[98:101], v[218:221], v[194:197], v[98:101]
	v_mfma_f32_16x16x32_bf16 v[90:93], v[226:229], v[194:197], v[90:93]
	v_mfma_f32_16x16x32_bf16 v[82:85], v[218:221], v[202:205], v[82:85]
	v_mfma_f32_16x16x32_bf16 v[74:77], v[226:229], v[202:205], v[74:77]
	v_mfma_f32_16x16x32_bf16 v[70:73], v[218:221], v[210:213], v[70:73]
	v_mfma_f32_16x16x32_bf16 v[66:69], v[226:229], v[210:213], v[66:69]
	v_mfma_f32_16x16x32_bf16 v[118:121], v[222:225], v[190:193], v[118:121]
	v_mfma_f32_16x16x32_bf16 v[106:109], v[230:233], v[190:193], v[106:109]
	v_mfma_f32_16x16x32_bf16 v[98:101], v[222:225], v[198:201], v[98:101]
	v_mfma_f32_16x16x32_bf16 v[90:93], v[230:233], v[198:201], v[90:93]
	v_mfma_f32_16x16x32_bf16 v[82:85], v[222:225], v[206:209], v[82:85]
	v_mfma_f32_16x16x32_bf16 v[74:77], v[230:233], v[206:209], v[74:77]
	v_mfma_f32_16x16x32_bf16 v[70:73], v[222:225], v[214:217], v[70:73]
	v_mfma_f32_16x16x32_bf16 v[66:69], v[230:233], v[214:217], v[66:69]
	s_nop 0
	s_mov_b32 m0, s25
	s_barrier
	ds_read_b128 v[182:185], v168 offset:16384
	ds_read_b128 v[190:193], v168 offset:17408
	ds_read_b128 v[194:197], v168 offset:18432
	ds_read_b128 v[198:201], v168 offset:19456
	ds_read_b128 v[202:205], v168 offset:20480
	ds_read_b128 v[206:209], v168 offset:21504
	ds_read_b128 v[210:213], v168 offset:22528
	ds_read_b128 v[214:217], v168 offset:23552
	global_load_lds_dwordx4 v152, s[28:29]
	s_mov_b32 m0, s37
	v_mov_b32_e32 v145, v153
	global_load_lds_dwordx4 v144, s[28:29]
	s_barrier
	s_waitcnt lgkmcnt(0)
	v_lshl_add_u64 v[236:237], s[28:29], 0, v[152:153]
	v_lshl_add_u64 v[144:145], s[28:29], 0, v[144:145]
	s_nop 0
	s_waitcnt lgkmcnt(0)
	v_mfma_f32_16x16x32_bf16 v[62:65], v[140:143], v[182:185], v[62:65]
	v_mfma_f32_16x16x32_bf16 v[58:61], v[174:177], v[182:185], v[58:61]
	v_mfma_f32_16x16x32_bf16 v[46:49], v[140:143], v[194:197], v[46:49]
	v_mfma_f32_16x16x32_bf16 v[38:41], v[174:177], v[194:197], v[38:41]
	v_mfma_f32_16x16x32_bf16 v[22:25], v[140:143], v[202:205], v[22:25]
	v_mfma_f32_16x16x32_bf16 v[14:17], v[174:177], v[202:205], v[14:17]
	v_mfma_f32_16x16x32_bf16 v[6:9], v[140:143], v[210:213], v[6:9]
	v_mfma_f32_16x16x32_bf16 v[2:5], v[174:177], v[210:213], v[2:5]
	v_mfma_f32_16x16x32_bf16 v[62:65], v[158:161], v[190:193], v[62:65]
	v_mfma_f32_16x16x32_bf16 v[58:61], v[178:181], v[190:193], v[58:61]
	v_mfma_f32_16x16x32_bf16 v[46:49], v[158:161], v[198:201], v[46:49]
	v_mfma_f32_16x16x32_bf16 v[38:41], v[178:181], v[198:201], v[38:41]
	v_mfma_f32_16x16x32_bf16 v[22:25], v[158:161], v[206:209], v[22:25]
	v_mfma_f32_16x16x32_bf16 v[14:17], v[178:181], v[206:209], v[14:17]
	v_mfma_f32_16x16x32_bf16 v[6:9], v[158:161], v[214:217], v[6:9]
	v_mfma_f32_16x16x32_bf16 v[2:5], v[178:181], v[214:217], v[2:5]
	s_nop 0
	s_barrier
	s_add_u32 s58, s26, 0x80000
	s_addc_u32 s59, s27, 0
	s_add_i32 s0, s47, s34
	v_lshl_add_u64 v[140:141], s[58:59], 0, v[150:151]
	s_mov_b32 m0, s0
	s_nop 0
	global_load_lds_dwordx4 v[140:141], off
	v_lshl_add_u64 v[140:141], s[58:59], 0, v[148:149]
	s_add_i32 m0, s0, 0x2000
	s_nop 0
	global_load_lds_dwordx4 v[140:141], off
	s_waitcnt vmcnt(6)
	s_barrier
	s_nop 0
	v_mfma_f32_16x16x32_bf16 v[42:45], v[218:221], v[182:185], v[42:45]
	v_mfma_f32_16x16x32_bf16 v[34:37], v[226:229], v[182:185], v[34:37]
	v_mfma_f32_16x16x32_bf16 v[18:21], v[218:221], v[194:197], v[18:21]
	v_mfma_f32_16x16x32_bf16 v[10:13], v[226:229], v[194:197], v[10:13]
	v_mfma_f32_16x16x32_bf16 v[54:57], v[218:221], v[202:205], v[54:57]
	v_mfma_f32_16x16x32_bf16 v[50:53], v[226:229], v[202:205], v[50:53]
	v_mfma_f32_16x16x32_bf16 v[30:33], v[218:221], v[210:213], v[30:33]
	v_mfma_f32_16x16x32_bf16 v[26:29], v[226:229], v[210:213], v[26:29]
	v_mfma_f32_16x16x32_bf16 v[42:45], v[222:225], v[190:193], v[42:45]
	v_mfma_f32_16x16x32_bf16 v[34:37], v[230:233], v[190:193], v[34:37]
	v_mfma_f32_16x16x32_bf16 v[18:21], v[222:225], v[198:201], v[18:21]
	v_mfma_f32_16x16x32_bf16 v[10:13], v[230:233], v[198:201], v[10:13]
	v_mfma_f32_16x16x32_bf16 v[54:57], v[222:225], v[206:209], v[54:57]
	v_mfma_f32_16x16x32_bf16 v[50:53], v[230:233], v[206:209], v[50:53]
	v_mfma_f32_16x16x32_bf16 v[30:33], v[222:225], v[214:217], v[30:33]
	v_mfma_f32_16x16x32_bf16 v[26:29], v[230:233], v[214:217], v[26:29]
	s_nop 0
	s_add_i32 s0, 0, 0x18000
	v_add_u32_e32 v152, s0, v165
	s_barrier
	ds_read_b128 v[140:143], v152
	ds_read_b128 v[158:161], v152 offset:1024
	ds_read_b128 v[174:177], v152 offset:2048
	ds_read_b128 v[178:181], v152 offset:3072
	s_mov_b32 m0, s38
	ds_read_b128 v[182:185], v168 offset:32768
	ds_read_b128 v[190:193], v168 offset:33792
	ds_read_b128 v[194:197], v168 offset:34816
	ds_read_b128 v[198:201], v168 offset:35840
	ds_read_b128 v[202:205], v168 offset:36864
	ds_read_b128 v[206:209], v168 offset:37888
	ds_read_b128 v[210:213], v168 offset:38912
	ds_read_b128 v[214:217], v168 offset:39936
	global_load_lds_dwordx4 v133, s[28:29]
	s_mov_b32 m0, s39
	s_nop 0
	global_load_lds_dwordx4 v135, s[28:29]
	s_waitcnt lgkmcnt(8)
	s_barrier
	s_waitcnt lgkmcnt(0)
	s_nop 0
	s_waitcnt lgkmcnt(0)
	v_mfma_f32_16x16x32_bf16 v[126:129], v[140:143], v[182:185], v[126:129]
	v_mfma_f32_16x16x32_bf16 v[122:125], v[174:177], v[182:185], v[122:125]
	v_mfma_f32_16x16x32_bf16 v[114:117], v[140:143], v[194:197], v[114:117]
	v_mfma_f32_16x16x32_bf16 v[110:113], v[174:177], v[194:197], v[110:113]
	v_mfma_f32_16x16x32_bf16 v[102:105], v[140:143], v[202:205], v[102:105]
	v_mfma_f32_16x16x32_bf16 v[94:97], v[174:177], v[202:205], v[94:97]
	v_mfma_f32_16x16x32_bf16 v[86:89], v[140:143], v[210:213], v[86:89]
	v_mfma_f32_16x16x32_bf16 v[78:81], v[174:177], v[210:213], v[78:81]
	v_mfma_f32_16x16x32_bf16 v[126:129], v[158:161], v[190:193], v[126:129]
	v_mfma_f32_16x16x32_bf16 v[122:125], v[178:181], v[190:193], v[122:125]
	v_mfma_f32_16x16x32_bf16 v[114:117], v[158:161], v[198:201], v[114:117]
	v_mfma_f32_16x16x32_bf16 v[110:113], v[178:181], v[198:201], v[110:113]
	v_mfma_f32_16x16x32_bf16 v[102:105], v[158:161], v[206:209], v[102:105]
	v_mfma_f32_16x16x32_bf16 v[94:97], v[178:181], v[206:209], v[94:97]
	v_mfma_f32_16x16x32_bf16 v[86:89], v[158:161], v[214:217], v[86:89]
	v_mfma_f32_16x16x32_bf16 v[78:81], v[178:181], v[214:217], v[78:81]
	s_nop 0
	s_barrier
	s_add_i32 s1, 0, 0x1c000
	s_add_i32 s0, s0, s34
	v_add_u32_e32 v133, s1, v165
	v_lshl_add_u64 v[186:187], v[186:187], 0, s[14:15]
	s_mov_b32 m0, s0
	ds_read_b128 v[218:221], v133
	ds_read_b128 v[222:225], v133 offset:1024
	ds_read_b128 v[226:229], v133 offset:2048
	ds_read_b128 v[230:233], v133 offset:3072
	global_load_lds_dwordx4 v[186:187], off
	v_lshl_add_u64 v[186:187], v[234:235], 0, s[14:15]
	s_add_i32 m0, s0, 0x2000
	s_nop 0
	global_load_lds_dwordx4 v[186:187], off
	s_barrier
	s_waitcnt lgkmcnt(0)
	s_nop 0
	s_waitcnt lgkmcnt(0)
	v_mfma_f32_16x16x32_bf16 v[118:121], v[218:221], v[182:185], v[118:121]
	v_mfma_f32_16x16x32_bf16 v[106:109], v[226:229], v[182:185], v[106:109]
	v_mfma_f32_16x16x32_bf16 v[98:101], v[218:221], v[194:197], v[98:101]
	v_mfma_f32_16x16x32_bf16 v[90:93], v[226:229], v[194:197], v[90:93]
	v_mfma_f32_16x16x32_bf16 v[82:85], v[218:221], v[202:205], v[82:85]
	v_mfma_f32_16x16x32_bf16 v[74:77], v[226:229], v[202:205], v[74:77]
	v_mfma_f32_16x16x32_bf16 v[70:73], v[218:221], v[210:213], v[70:73]
	v_mfma_f32_16x16x32_bf16 v[66:69], v[226:229], v[210:213], v[66:69]
	v_mfma_f32_16x16x32_bf16 v[118:121], v[222:225], v[190:193], v[118:121]
	v_mfma_f32_16x16x32_bf16 v[106:109], v[230:233], v[190:193], v[106:109]
	v_mfma_f32_16x16x32_bf16 v[98:101], v[222:225], v[198:201], v[98:101]
	v_mfma_f32_16x16x32_bf16 v[90:93], v[230:233], v[198:201], v[90:93]
	v_mfma_f32_16x16x32_bf16 v[82:85], v[222:225], v[206:209], v[82:85]
	v_mfma_f32_16x16x32_bf16 v[74:77], v[230:233], v[206:209], v[74:77]
	v_mfma_f32_16x16x32_bf16 v[70:73], v[222:225], v[214:217], v[70:73]
	v_mfma_f32_16x16x32_bf16 v[66:69], v[230:233], v[214:217], v[66:69]
	s_nop 0
	s_mov_b32 m0, s43
	v_lshl_add_u64 v[186:187], v[236:237], 0, s[14:15]
	s_barrier
	ds_read_b128 v[182:185], v168 offset:49152
	ds_read_b128 v[190:193], v168 offset:50176
	ds_read_b128 v[194:197], v168 offset:51200
	ds_read_b128 v[198:201], v168 offset:52224
	ds_read_b128 v[202:205], v168 offset:53248
	ds_read_b128 v[206:209], v168 offset:54272
	ds_read_b128 v[210:213], v168 offset:55296
	ds_read_b128 v[214:217], v168 offset:56320
	global_load_lds_dwordx4 v[186:187], off
	v_lshl_add_u64 v[144:145], v[144:145], 0, s[14:15]
	s_mov_b32 m0, s44
	s_nop 0
	global_load_lds_dwordx4 v[144:145], off
	s_barrier
	s_waitcnt lgkmcnt(0)
	s_nop 0
	s_waitcnt lgkmcnt(0)
	v_mfma_f32_16x16x32_bf16 v[62:65], v[140:143], v[182:185], v[62:65]
	v_mfma_f32_16x16x32_bf16 v[58:61], v[174:177], v[182:185], v[58:61]
	v_mfma_f32_16x16x32_bf16 v[46:49], v[140:143], v[194:197], v[46:49]
	v_mfma_f32_16x16x32_bf16 v[38:41], v[174:177], v[194:197], v[38:41]
	v_mfma_f32_16x16x32_bf16 v[22:25], v[140:143], v[202:205], v[22:25]
	v_mfma_f32_16x16x32_bf16 v[14:17], v[174:177], v[202:205], v[14:17]
	v_mfma_f32_16x16x32_bf16 v[6:9], v[140:143], v[210:213], v[6:9]
	v_mfma_f32_16x16x32_bf16 v[2:5], v[174:177], v[210:213], v[2:5]
	v_mfma_f32_16x16x32_bf16 v[62:65], v[158:161], v[190:193], v[62:65]
	v_mfma_f32_16x16x32_bf16 v[58:61], v[178:181], v[190:193], v[58:61]
	v_mfma_f32_16x16x32_bf16 v[46:49], v[158:161], v[198:201], v[46:49]
	v_mfma_f32_16x16x32_bf16 v[38:41], v[178:181], v[198:201], v[38:41]
	v_mfma_f32_16x16x32_bf16 v[22:25], v[158:161], v[206:209], v[22:25]
	v_mfma_f32_16x16x32_bf16 v[14:17], v[178:181], v[206:209], v[14:17]
	v_mfma_f32_16x16x32_bf16 v[6:9], v[158:161], v[214:217], v[6:9]
	v_mfma_f32_16x16x32_bf16 v[2:5], v[178:181], v[214:217], v[2:5]
	s_nop 0
	s_barrier
	s_add_u32 s26, s26, 0x80080
	s_addc_u32 s27, s27, 0
	s_add_i32 s0, s1, s34
	v_lshl_add_u64 v[140:141], s[26:27], 0, v[150:151]
	s_mov_b32 m0, s0
	s_nop 0
	global_load_lds_dwordx4 v[140:141], off
	v_lshl_add_u64 v[140:141], s[26:27], 0, v[148:149]
	s_add_i32 m0, s0, 0x2000
	s_nop 0
	global_load_lds_dwordx4 v[140:141], off
	s_waitcnt vmcnt(6)
	s_barrier
	s_nop 0
	v_mfma_f32_16x16x32_bf16 v[42:45], v[218:221], v[182:185], v[42:45]
	v_mfma_f32_16x16x32_bf16 v[34:37], v[226:229], v[182:185], v[34:37]
	v_mfma_f32_16x16x32_bf16 v[18:21], v[218:221], v[194:197], v[18:21]
	v_mfma_f32_16x16x32_bf16 v[10:13], v[226:229], v[194:197], v[10:13]
	v_mfma_f32_16x16x32_bf16 v[54:57], v[218:221], v[202:205], v[54:57]
	v_mfma_f32_16x16x32_bf16 v[50:53], v[226:229], v[202:205], v[50:53]
	v_mfma_f32_16x16x32_bf16 v[30:33], v[218:221], v[210:213], v[30:33]
	v_mfma_f32_16x16x32_bf16 v[26:29], v[226:229], v[210:213], v[26:29]
	v_mfma_f32_16x16x32_bf16 v[42:45], v[222:225], v[190:193], v[42:45]
	v_mfma_f32_16x16x32_bf16 v[34:37], v[230:233], v[190:193], v[34:37]
	v_mfma_f32_16x16x32_bf16 v[18:21], v[222:225], v[198:201], v[18:21]
	v_mfma_f32_16x16x32_bf16 v[10:13], v[230:233], v[198:201], v[10:13]
	v_mfma_f32_16x16x32_bf16 v[54:57], v[222:225], v[206:209], v[54:57]
	v_mfma_f32_16x16x32_bf16 v[50:53], v[230:233], v[206:209], v[50:53]
	v_mfma_f32_16x16x32_bf16 v[30:33], v[222:225], v[214:217], v[30:33]
	v_mfma_f32_16x16x32_bf16 v[26:29], v[230:233], v[214:217], v[26:29]
	s_nop 0
	s_add_i32 s57, s57, 2
	s_add_u32 s6, s6, 0x100
	s_addc_u32 s7, s7, 0
	s_cmp_gt_u32 s57, 29
	s_barrier
	s_cbranch_scc0 .LBB0_709
	s_mov_b64 s[26:27], 0x6000
	s_cmpk_gt_i32 s49, 0x7fff
	s_mov_b64 s[6:7], s[18:19]
	s_cbranch_scc1 .LBB0_703
	s_ashr_i32 s0, s49, 31
	s_lshr_b32 s0, s0, 18
	s_add_i32 s0, s49, s0
	s_ashr_i32 s0, s0, 14
	s_mul_i32 s26, s0, 0x3000
	s_ashr_i32 s27, s26, 31
	s_mov_b64 s[6:7], s[12:13]
	s_branch .LBB0_703

.LBB0_913:
	s_add_u32 s0, s54, s6
	s_addc_u32 s1, s55, s7
	v_add_u32_e32 v141, s77, v150
	s_add_u32 s0, s0, 0x8c00100
	ds_read_b128 v[160:163], v141
	ds_read_b128 v[164:167], v141 offset:1024
	ds_read_b128 v[168:171], v141 offset:2048
	ds_read_b128 v[172:175], v141 offset:3072
	s_addc_u32 s1, s1, 0
	s_add_u32 s90, s87, s6
	s_addc_u32 s91, s88, s7
	s_cmpk_eq_i32 s6, 0xf00
	s_cselect_b64 vcc, -1, 0
	s_and_b64 s[38:39], vcc, exec
	v_cndmask_b32_e32 v134, v158, v154, vcc
	s_cselect_b32 s41, s11, s1
	s_cselect_b32 s40, s10, s0
	v_cndmask_b32_e32 v137, v136, v155, vcc
	v_cndmask_b32_e32 v226, v138, v156, vcc
	v_cndmask_b32_e32 v141, v140, v157, vcc
	s_cselect_b32 s39, s35, s91
	s_cselect_b32 s38, s86, s90
	v_lshl_add_u64 v[210:211], v[144:145], 0, s[6:7]
	s_add_i32 m0, s48, 0xc000
	ds_read_b128 v[176:179], v153
	ds_read_b128 v[180:183], v153 offset:1024
	ds_read_b128 v[184:187], v153 offset:2048
	ds_read_b128 v[190:193], v153 offset:3072
	ds_read_b128 v[194:197], v153 offset:4096
	ds_read_b128 v[198:201], v153 offset:5120
	ds_read_b128 v[202:205], v153 offset:6144
	ds_read_b128 v[206:209], v153 offset:7168
	global_load_lds_dwordx4 v[210:211], off
	v_lshl_add_u64 v[210:211], v[142:143], 0, s[6:7]
	s_add_i32 m0, s48, 0xe000
	s_nop 0
	global_load_lds_dwordx4 v[210:211], off
	s_waitcnt lgkmcnt(8)
	s_barrier
	s_waitcnt lgkmcnt(0)
	s_nop 0
	s_waitcnt lgkmcnt(0)
	v_mfma_f32_16x16x32_bf16 v[126:129], v[160:163], v[176:179], v[126:129]
	v_mfma_f32_16x16x32_bf16 v[122:125], v[168:171], v[176:179], v[122:125]
	v_mfma_f32_16x16x32_bf16 v[110:113], v[160:163], v[184:187], v[110:113]
	v_mfma_f32_16x16x32_bf16 v[106:109], v[168:171], v[184:187], v[106:109]
	v_mfma_f32_16x16x32_bf16 v[94:97], v[160:163], v[194:197], v[94:97]
	v_mfma_f32_16x16x32_bf16 v[90:93], v[168:171], v[194:197], v[90:93]
	v_mfma_f32_16x16x32_bf16 v[78:81], v[160:163], v[202:205], v[78:81]
	v_mfma_f32_16x16x32_bf16 v[74:77], v[168:171], v[202:205], v[74:77]
	v_mfma_f32_16x16x32_bf16 v[126:129], v[164:167], v[180:183], v[126:129]
	v_mfma_f32_16x16x32_bf16 v[122:125], v[172:175], v[180:183], v[122:125]
	v_mfma_f32_16x16x32_bf16 v[110:113], v[164:167], v[190:193], v[110:113]
	v_mfma_f32_16x16x32_bf16 v[106:109], v[172:175], v[190:193], v[106:109]
	v_mfma_f32_16x16x32_bf16 v[94:97], v[164:167], v[198:201], v[94:97]
	v_mfma_f32_16x16x32_bf16 v[90:93], v[172:175], v[198:201], v[90:93]
	v_mfma_f32_16x16x32_bf16 v[78:81], v[164:167], v[206:209], v[78:81]
	v_mfma_f32_16x16x32_bf16 v[74:77], v[172:175], v[206:209], v[74:77]
	s_nop 0
	s_barrier
	s_add_i32 s0, s77, s45
	v_add_u32_e32 v159, s78, v150
	v_lshl_add_u64 v[228:229], s[38:39], 0, v[132:133]
	s_mov_b32 m0, s0
	ds_read_b128 v[210:213], v159
	ds_read_b128 v[214:217], v159 offset:1024
	ds_read_b128 v[218:221], v159 offset:2048
	ds_read_b128 v[222:225], v159 offset:3072
	global_load_lds_dwordx4 v[228:229], off
	v_lshl_add_u64 v[230:231], s[38:39], 0, v[130:131]
	s_add_i32 m0, s0, 0x2000
	s_nop 0
	global_load_lds_dwordx4 v[230:231], off
	s_barrier
	s_waitcnt lgkmcnt(0)
	s_nop 0
	s_waitcnt lgkmcnt(0)
	v_mfma_f32_16x16x32_bf16 v[118:121], v[210:213], v[176:179], v[118:121]
	v_mfma_f32_16x16x32_bf16 v[114:117], v[218:221], v[176:179], v[114:117]
	v_mfma_f32_16x16x32_bf16 v[102:105], v[210:213], v[184:187], v[102:105]
	v_mfma_f32_16x16x32_bf16 v[98:101], v[218:221], v[184:187], v[98:101]
	v_mfma_f32_16x16x32_bf16 v[86:89], v[210:213], v[194:197], v[86:89]
	v_mfma_f32_16x16x32_bf16 v[82:85], v[218:221], v[194:197], v[82:85]
	v_mfma_f32_16x16x32_bf16 v[70:73], v[210:213], v[202:205], v[70:73]
	v_mfma_f32_16x16x32_bf16 v[66:69], v[218:221], v[202:205], v[66:69]
	v_mfma_f32_16x16x32_bf16 v[118:121], v[214:217], v[180:183], v[118:121]
	v_mfma_f32_16x16x32_bf16 v[114:117], v[222:225], v[180:183], v[114:117]
	v_mfma_f32_16x16x32_bf16 v[102:105], v[214:217], v[190:193], v[102:105]
	v_mfma_f32_16x16x32_bf16 v[98:101], v[222:225], v[190:193], v[98:101]
	v_mfma_f32_16x16x32_bf16 v[86:89], v[214:217], v[198:201], v[86:89]
	v_mfma_f32_16x16x32_bf16 v[82:85], v[222:225], v[198:201], v[82:85]
	v_mfma_f32_16x16x32_bf16 v[70:73], v[214:217], v[206:209], v[70:73]
	v_mfma_f32_16x16x32_bf16 v[66:69], v[222:225], v[206:209], v[66:69]
	s_nop 0
	s_mov_b32 m0, s48
	s_barrier
	ds_read_b128 v[176:179], v153 offset:16384
	ds_read_b128 v[180:183], v153 offset:17408
	ds_read_b128 v[184:187], v153 offset:18432
	ds_read_b128 v[190:193], v153 offset:19456
	ds_read_b128 v[194:197], v153 offset:20480
	ds_read_b128 v[198:201], v153 offset:21504
	ds_read_b128 v[202:205], v153 offset:22528
	ds_read_b128 v[206:209], v153 offset:23552
	global_load_lds_dwordx4 v134, s[40:41]
	s_mov_b32 m0, s49
	v_mov_b32_e32 v227, v135
	global_load_lds_dwordx4 v226, s[40:41]
	s_barrier
	s_waitcnt lgkmcnt(0)
	v_lshl_add_u64 v[232:233], s[40:41], 0, v[134:135]
	v_lshl_add_u64 v[226:227], s[40:41], 0, v[226:227]
	s_nop 0
	s_waitcnt lgkmcnt(0)
	v_mfma_f32_16x16x32_bf16 v[62:65], v[160:163], v[176:179], v[62:65]
	v_mfma_f32_16x16x32_bf16 v[58:61], v[168:171], v[176:179], v[58:61]
	v_mfma_f32_16x16x32_bf16 v[46:49], v[160:163], v[184:187], v[46:49]
	v_mfma_f32_16x16x32_bf16 v[42:45], v[168:171], v[184:187], v[42:45]
	v_mfma_f32_16x16x32_bf16 v[22:25], v[160:163], v[194:197], v[22:25]
	v_mfma_f32_16x16x32_bf16 v[18:21], v[168:171], v[194:197], v[18:21]
	v_mfma_f32_16x16x32_bf16 v[6:9], v[160:163], v[202:205], v[6:9]
	v_mfma_f32_16x16x32_bf16 v[2:5], v[168:171], v[202:205], v[2:5]
	v_mfma_f32_16x16x32_bf16 v[62:65], v[164:167], v[180:183], v[62:65]
	v_mfma_f32_16x16x32_bf16 v[58:61], v[172:175], v[180:183], v[58:61]
	v_mfma_f32_16x16x32_bf16 v[46:49], v[164:167], v[190:193], v[46:49]
	v_mfma_f32_16x16x32_bf16 v[42:45], v[172:175], v[190:193], v[42:45]
	v_mfma_f32_16x16x32_bf16 v[22:25], v[164:167], v[198:201], v[22:25]
	v_mfma_f32_16x16x32_bf16 v[18:21], v[172:175], v[198:201], v[18:21]
	v_mfma_f32_16x16x32_bf16 v[6:9], v[164:167], v[206:209], v[6:9]
	v_mfma_f32_16x16x32_bf16 v[2:5], v[172:175], v[206:209], v[2:5]
	s_nop 0
	s_barrier
	s_add_u32 s90, s38, 0x80000
	s_addc_u32 s91, s39, 0
	s_add_i32 s0, s78, s45
	v_lshl_add_u64 v[160:161], s[90:91], 0, v[132:133]
	s_mov_b32 m0, s0
	s_nop 0
	global_load_lds_dwordx4 v[160:161], off
	v_lshl_add_u64 v[160:161], s[90:91], 0, v[130:131]
	s_add_i32 m0, s0, 0x2000
	s_nop 0
	global_load_lds_dwordx4 v[160:161], off
	s_waitcnt vmcnt(6)
	s_barrier
	s_nop 0
	v_mfma_f32_16x16x32_bf16 v[54:57], v[210:213], v[176:179], v[54:57]
	v_mfma_f32_16x16x32_bf16 v[50:53], v[218:221], v[176:179], v[50:53]
	v_mfma_f32_16x16x32_bf16 v[30:33], v[210:213], v[184:187], v[30:33]
	v_mfma_f32_16x16x32_bf16 v[26:29], v[218:221], v[184:187], v[26:29]
	v_mfma_f32_16x16x32_bf16 v[34:37], v[210:213], v[194:197], v[34:37]
	v_mfma_f32_16x16x32_bf16 v[38:41], v[218:221], v[194:197], v[38:41]
	v_mfma_f32_16x16x32_bf16 v[10:13], v[210:213], v[202:205], v[10:13]
	v_mfma_f32_16x16x32_bf16 v[14:17], v[218:221], v[202:205], v[14:17]
	v_mfma_f32_16x16x32_bf16 v[54:57], v[214:217], v[180:183], v[54:57]
	v_mfma_f32_16x16x32_bf16 v[50:53], v[222:225], v[180:183], v[50:53]
	v_mfma_f32_16x16x32_bf16 v[30:33], v[214:217], v[190:193], v[30:33]
	v_mfma_f32_16x16x32_bf16 v[26:29], v[222:225], v[190:193], v[26:29]
	v_mfma_f32_16x16x32_bf16 v[34:37], v[214:217], v[198:201], v[34:37]
	v_mfma_f32_16x16x32_bf16 v[38:41], v[222:225], v[198:201], v[38:41]
	v_mfma_f32_16x16x32_bf16 v[10:13], v[214:217], v[206:209], v[10:13]
	v_mfma_f32_16x16x32_bf16 v[14:17], v[222:225], v[206:209], v[14:17]
	s_nop 0
	s_add_i32 s0, 0, 0x18000
	v_add_u32_e32 v134, s0, v150
	s_barrier
	ds_read_b128 v[160:163], v134
	ds_read_b128 v[164:167], v134 offset:1024
	ds_read_b128 v[168:171], v134 offset:2048
	ds_read_b128 v[172:175], v134 offset:3072
	s_mov_b32 m0, s50
	ds_read_b128 v[176:179], v153 offset:32768
	ds_read_b128 v[180:183], v153 offset:33792
	ds_read_b128 v[184:187], v153 offset:34816
	ds_read_b128 v[190:193], v153 offset:35840
	ds_read_b128 v[194:197], v153 offset:36864
	ds_read_b128 v[198:201], v153 offset:37888
	ds_read_b128 v[202:205], v153 offset:38912
	ds_read_b128 v[206:209], v153 offset:39936
	global_load_lds_dwordx4 v137, s[40:41]
	s_mov_b32 m0, s51
	s_nop 0
	global_load_lds_dwordx4 v141, s[40:41]
	s_waitcnt lgkmcnt(8)
	s_barrier
	s_waitcnt lgkmcnt(0)
	s_nop 0
	s_waitcnt lgkmcnt(0)
	v_mfma_f32_16x16x32_bf16 v[126:129], v[160:163], v[176:179], v[126:129]
	v_mfma_f32_16x16x32_bf16 v[122:125], v[168:171], v[176:179], v[122:125]
	v_mfma_f32_16x16x32_bf16 v[110:113], v[160:163], v[184:187], v[110:113]
	v_mfma_f32_16x16x32_bf16 v[106:109], v[168:171], v[184:187], v[106:109]
	v_mfma_f32_16x16x32_bf16 v[94:97], v[160:163], v[194:197], v[94:97]
	v_mfma_f32_16x16x32_bf16 v[90:93], v[168:171], v[194:197], v[90:93]
	v_mfma_f32_16x16x32_bf16 v[78:81], v[160:163], v[202:205], v[78:81]
	v_mfma_f32_16x16x32_bf16 v[74:77], v[168:171], v[202:205], v[74:77]
	v_mfma_f32_16x16x32_bf16 v[126:129], v[164:167], v[180:183], v[126:129]
	v_mfma_f32_16x16x32_bf16 v[122:125], v[172:175], v[180:183], v[122:125]
	v_mfma_f32_16x16x32_bf16 v[110:113], v[164:167], v[190:193], v[110:113]
	v_mfma_f32_16x16x32_bf16 v[106:109], v[172:175], v[190:193], v[106:109]
	v_mfma_f32_16x16x32_bf16 v[94:97], v[164:167], v[198:201], v[94:97]
	v_mfma_f32_16x16x32_bf16 v[90:93], v[172:175], v[198:201], v[90:93]
	v_mfma_f32_16x16x32_bf16 v[78:81], v[164:167], v[206:209], v[78:81]
	v_mfma_f32_16x16x32_bf16 v[74:77], v[172:175], v[206:209], v[74:77]
	s_nop 0
	s_barrier
	s_add_i32 s1, 0, 0x1c000
	s_add_i32 s0, s0, s45
	v_add_u32_e32 v134, s1, v150
	v_lshl_add_u64 v[228:229], v[228:229], 0, s[14:15]
	s_mov_b32 m0, s0
	ds_read_b128 v[210:213], v134
	ds_read_b128 v[214:217], v134 offset:1024
	ds_read_b128 v[218:221], v134 offset:2048
	ds_read_b128 v[222:225], v134 offset:3072
	global_load_lds_dwordx4 v[228:229], off
	v_lshl_add_u64 v[228:229], v[230:231], 0, s[14:15]
	s_add_i32 m0, s0, 0x2000
	s_nop 0
	global_load_lds_dwordx4 v[228:229], off
	s_barrier
	s_waitcnt lgkmcnt(0)
	s_nop 0
	s_waitcnt lgkmcnt(0)
	v_mfma_f32_16x16x32_bf16 v[118:121], v[210:213], v[176:179], v[118:121]
	v_mfma_f32_16x16x32_bf16 v[114:117], v[218:221], v[176:179], v[114:117]
	v_mfma_f32_16x16x32_bf16 v[102:105], v[210:213], v[184:187], v[102:105]
	v_mfma_f32_16x16x32_bf16 v[98:101], v[218:221], v[184:187], v[98:101]
	v_mfma_f32_16x16x32_bf16 v[86:89], v[210:213], v[194:197], v[86:89]
	v_mfma_f32_16x16x32_bf16 v[82:85], v[218:221], v[194:197], v[82:85]
	v_mfma_f32_16x16x32_bf16 v[70:73], v[210:213], v[202:205], v[70:73]
	v_mfma_f32_16x16x32_bf16 v[66:69], v[218:221], v[202:205], v[66:69]
	v_mfma_f32_16x16x32_bf16 v[118:121], v[214:217], v[180:183], v[118:121]
	v_mfma_f32_16x16x32_bf16 v[114:117], v[222:225], v[180:183], v[114:117]
	v_mfma_f32_16x16x32_bf16 v[102:105], v[214:217], v[190:193], v[102:105]
	v_mfma_f32_16x16x32_bf16 v[98:101], v[222:225], v[190:193], v[98:101]
	v_mfma_f32_16x16x32_bf16 v[86:89], v[214:217], v[198:201], v[86:89]
	v_mfma_f32_16x16x32_bf16 v[82:85], v[222:225], v[198:201], v[82:85]
	v_mfma_f32_16x16x32_bf16 v[70:73], v[214:217], v[206:209], v[70:73]
	v_mfma_f32_16x16x32_bf16 v[66:69], v[222:225], v[206:209], v[66:69]
	s_nop 0
	s_mov_b32 m0, s58
	v_lshl_add_u64 v[228:229], v[232:233], 0, s[14:15]
	s_barrier
	ds_read_b128 v[176:179], v153 offset:49152
	ds_read_b128 v[180:183], v153 offset:50176
	ds_read_b128 v[184:187], v153 offset:51200
	ds_read_b128 v[190:193], v153 offset:52224
	ds_read_b128 v[194:197], v153 offset:53248
	ds_read_b128 v[198:201], v153 offset:54272
	ds_read_b128 v[202:205], v153 offset:55296
	ds_read_b128 v[206:209], v153 offset:56320
	global_load_lds_dwordx4 v[228:229], off
	v_lshl_add_u64 v[226:227], v[226:227], 0, s[14:15]
	s_mov_b32 m0, s59
	s_nop 0
	global_load_lds_dwordx4 v[226:227], off
	s_barrier
	s_waitcnt lgkmcnt(0)
	s_nop 0
	s_waitcnt lgkmcnt(0)
	v_mfma_f32_16x16x32_bf16 v[62:65], v[160:163], v[176:179], v[62:65]
	v_mfma_f32_16x16x32_bf16 v[58:61], v[168:171], v[176:179], v[58:61]
	v_mfma_f32_16x16x32_bf16 v[46:49], v[160:163], v[184:187], v[46:49]
	v_mfma_f32_16x16x32_bf16 v[42:45], v[168:171], v[184:187], v[42:45]
	v_mfma_f32_16x16x32_bf16 v[22:25], v[160:163], v[194:197], v[22:25]
	v_mfma_f32_16x16x32_bf16 v[18:21], v[168:171], v[194:197], v[18:21]
	v_mfma_f32_16x16x32_bf16 v[6:9], v[160:163], v[202:205], v[6:9]
	v_mfma_f32_16x16x32_bf16 v[2:5], v[168:171], v[202:205], v[2:5]
	v_mfma_f32_16x16x32_bf16 v[62:65], v[164:167], v[180:183], v[62:65]
	v_mfma_f32_16x16x32_bf16 v[58:61], v[172:175], v[180:183], v[58:61]
	v_mfma_f32_16x16x32_bf16 v[46:49], v[164:167], v[190:193], v[46:49]
	v_mfma_f32_16x16x32_bf16 v[42:45], v[172:175], v[190:193], v[42:45]
	v_mfma_f32_16x16x32_bf16 v[22:25], v[164:167], v[198:201], v[22:25]
	v_mfma_f32_16x16x32_bf16 v[18:21], v[172:175], v[198:201], v[18:21]
	v_mfma_f32_16x16x32_bf16 v[6:9], v[164:167], v[206:209], v[6:9]
	v_mfma_f32_16x16x32_bf16 v[2:5], v[172:175], v[206:209], v[2:5]
	s_nop 0
	s_barrier
	s_add_u32 s38, s38, 0x80080
	s_addc_u32 s39, s39, 0
	s_add_i32 s0, s1, s45
	v_lshl_add_u64 v[160:161], s[38:39], 0, v[132:133]
	s_mov_b32 m0, s0
	s_nop 0
	global_load_lds_dwordx4 v[160:161], off
	v_lshl_add_u64 v[160:161], s[38:39], 0, v[130:131]
	s_add_i32 m0, s0, 0x2000
	s_nop 0
	global_load_lds_dwordx4 v[160:161], off
	s_waitcnt vmcnt(6)
	s_barrier
	s_nop 0
	v_mfma_f32_16x16x32_bf16 v[54:57], v[210:213], v[176:179], v[54:57]
	v_mfma_f32_16x16x32_bf16 v[50:53], v[218:221], v[176:179], v[50:53]
	v_mfma_f32_16x16x32_bf16 v[30:33], v[210:213], v[184:187], v[30:33]
	v_mfma_f32_16x16x32_bf16 v[26:29], v[218:221], v[184:187], v[26:29]
	v_mfma_f32_16x16x32_bf16 v[34:37], v[210:213], v[194:197], v[34:37]
	v_mfma_f32_16x16x32_bf16 v[38:41], v[218:221], v[194:197], v[38:41]
	v_mfma_f32_16x16x32_bf16 v[10:13], v[210:213], v[202:205], v[10:13]
	v_mfma_f32_16x16x32_bf16 v[14:17], v[218:221], v[202:205], v[14:17]
	v_mfma_f32_16x16x32_bf16 v[54:57], v[214:217], v[180:183], v[54:57]
	v_mfma_f32_16x16x32_bf16 v[50:53], v[222:225], v[180:183], v[50:53]
	v_mfma_f32_16x16x32_bf16 v[30:33], v[214:217], v[190:193], v[30:33]
	v_mfma_f32_16x16x32_bf16 v[26:29], v[222:225], v[190:193], v[26:29]
	v_mfma_f32_16x16x32_bf16 v[34:37], v[214:217], v[198:201], v[34:37]
	v_mfma_f32_16x16x32_bf16 v[38:41], v[222:225], v[198:201], v[38:41]
	v_mfma_f32_16x16x32_bf16 v[10:13], v[214:217], v[206:209], v[10:13]
	v_mfma_f32_16x16x32_bf16 v[14:17], v[222:225], v[206:209], v[14:17]
	s_nop 0
	s_add_i32 s89, s89, 2
	s_add_u32 s6, s6, 0x100
	s_addc_u32 s7, s7, 0
	s_cmp_gt_u32 s89, 29
	s_barrier
	s_cbranch_scc0 .LBB0_913
	v_mul_f32_e32 v134, 0xbfb8aa3b, v126
	v_exp_f32_e32 v134, v134
	v_mul_f32_e32 v138, 0xbfb8aa3b, v127
	v_exp_f32_e32 v138, v138
	v_mul_f32_e32 v141, 0xbfb8aa3b, v129
	v_add_f32_e32 v134, 1.0, v134
	v_rcp_f32_e32 v140, v134
	v_add_f32_e32 v134, 1.0, v138
	v_mul_f32_e32 v138, 0xbfb8aa3b, v128
	v_exp_f32_e32 v138, v138
	v_exp_f32_e32 v143, v141
	v_rcp_f32_e32 v141, v134
	s_add_i32 s0, s84, s57
	v_add_f32_e32 v134, 1.0, v138
	v_rcp_f32_e32 v142, v134
	v_add_f32_e32 v134, 1.0, v143
	v_rcp_f32_e32 v143, v134
	s_lshr_b32 s1, s0, 31
	s_add_i32 s1, s0, s1
	v_pk_mul_f32 v[126:127], v[126:127], v[140:141]
	v_add_u32_e32 v136, s85, v139
	s_ashr_i32 s1, s1, 1
	v_pk_mul_f32 v[122:123], v[122:123], v[126:127]
	v_pk_mul_f32 v[126:127], v[128:129], v[142:143]
	v_ashrrev_i32_e32 v137, 31, v136
	v_pk_mul_f32 v[124:125], v[124:125], v[126:127]
	v_add_u32_e32 v126, s1, v151
	v_lshlrev_b64 v[136:137], 10, v[136:137]
	v_ashrrev_i32_e32 v127, 31, v126
	v_lshl_add_u64 v[136:137], s[12:13], 0, v[136:137]
	v_cvt_pk_bf16_f32 v128, v122, v123
	v_lshlrev_b64 v[122:123], 1, v[126:127]
	v_cvt_pk_bf16_f32 v129, v124, v125
	v_lshl_add_u64 v[124:125], v[136:137], 0, v[122:123]
	global_store_dwordx2 v[124:125], v[128:129], off
	v_mul_f32_e32 v124, 0xbfb8aa3b, v118
	v_mul_f32_e32 v125, 0xbfb8aa3b, v119
	v_exp_f32_e32 v124, v124
	v_exp_f32_e32 v125, v125
	v_mul_f32_e32 v126, 0xbfb8aa3b, v120
	v_mul_f32_e32 v127, 0xbfb8aa3b, v121
	v_exp_f32_e32 v126, v126
	v_exp_f32_e32 v127, v127
	v_add_f32_e32 v124, 1.0, v124
	v_add_f32_e32 v125, 1.0, v125
	v_rcp_f32_e32 v124, v124
	v_rcp_f32_e32 v125, v125
	v_add_f32_e32 v126, 1.0, v126
	v_add_f32_e32 v127, 1.0, v127
	v_rcp_f32_e32 v126, v126
	v_rcp_f32_e32 v127, v127
	s_addk_i32 s0, 0x80
	s_lshr_b32 s1, s0, 31
	s_add_i32 s0, s0, s1
	v_pk_mul_f32 v[118:119], v[118:119], v[124:125]
	s_ashr_i32 s0, s0, 1
	v_pk_mul_f32 v[114:115], v[114:115], v[118:119]
	v_pk_mul_f32 v[118:119], v[120:121], v[126:127]
	v_cvt_pk_bf16_f32 v120, v114, v115
	v_pk_mul_f32 v[116:117], v[116:117], v[118:119]
	v_add_u32_e32 v118, s0, v151
	v_ashrrev_i32_e32 v119, 31, v118
	v_lshlrev_b64 v[114:115], 1, v[118:119]
	v_mul_f32_e32 v118, 0xbfb8aa3b, v110
	v_mul_f32_e32 v119, 0xbfb8aa3b, v111
	v_exp_f32_e32 v118, v118
	v_exp_f32_e32 v119, v119
	v_cvt_pk_bf16_f32 v121, v116, v117
	v_lshl_add_u64 v[116:117], v[136:137], 0, v[114:115]
	global_store_dwordx2 v[116:117], v[120:121], off
	v_add_f32_e32 v116, 1.0, v118
	v_add_f32_e32 v117, 1.0, v119
	v_mul_f32_e32 v118, 0xbfb8aa3b, v112
	v_mul_f32_e32 v119, 0xbfb8aa3b, v113
	v_exp_f32_e32 v118, v118
	v_exp_f32_e32 v119, v119
	v_rcp_f32_e32 v116, v116
	v_rcp_f32_e32 v117, v117
	v_add_f32_e32 v118, 1.0, v118
	v_add_f32_e32 v119, 1.0, v119
	v_rcp_f32_e32 v118, v118
	v_rcp_f32_e32 v119, v119
	v_pk_mul_f32 v[110:111], v[110:111], v[116:117]
	v_lshl_add_u64 v[120:121], v[136:137], 0, s[18:19]
	v_pk_mul_f32 v[106:107], v[106:107], v[110:111]
	v_pk_mul_f32 v[110:111], v[112:113], v[118:119]
	v_cvt_pk_bf16_f32 v106, v106, v107
	v_pk_mul_f32 v[108:109], v[108:109], v[110:111]
	v_mul_f32_e32 v112, 0xbfb8aa3b, v104
	v_cvt_pk_bf16_f32 v107, v108, v109
	v_mul_f32_e32 v108, 0xbfb8aa3b, v102
	v_exp_f32_e32 v110, v108
	v_mul_f32_e32 v108, 0xbfb8aa3b, v103
	v_exp_f32_e32 v111, v108
	v_mul_f32_e32 v113, 0xbfb8aa3b, v105
	v_exp_f32_e32 v112, v112
	v_exp_f32_e32 v113, v113
	v_add_f32_e32 v110, 1.0, v110
	v_add_f32_e32 v111, 1.0, v111
	v_rcp_f32_e32 v110, v110
	v_rcp_f32_e32 v111, v111
	v_add_f32_e32 v112, 1.0, v112
	v_add_f32_e32 v113, 1.0, v113
	v_rcp_f32_e32 v112, v112
	v_rcp_f32_e32 v113, v113
	v_pk_mul_f32 v[102:103], v[102:103], v[110:111]
	v_lshl_add_u64 v[108:109], v[120:121], 0, v[122:123]
	v_pk_mul_f32 v[98:99], v[98:99], v[102:103]
	v_pk_mul_f32 v[102:103], v[104:105], v[112:113]
	v_cvt_pk_bf16_f32 v98, v98, v99
	v_pk_mul_f32 v[100:101], v[100:101], v[102:103]
	v_mul_f32_e32 v102, 0xbfb8aa3b, v94
	v_cvt_pk_bf16_f32 v99, v100, v101
	v_lshl_add_u64 v[100:101], v[120:121], 0, v[114:115]
	v_mul_f32_e32 v103, 0xbfb8aa3b, v95
	global_store_dwordx2 v[108:109], v[106:107], off
	v_exp_f32_e32 v102, v102
	v_exp_f32_e32 v103, v103
	global_store_dwordx2 v[100:101], v[98:99], off
	v_mul_f32_e32 v100, 0xbfb8aa3b, v96
	v_mul_f32_e32 v101, 0xbfb8aa3b, v97
	v_exp_f32_e32 v100, v100
	v_exp_f32_e32 v101, v101
	v_add_f32_e32 v98, 1.0, v102
	v_add_f32_e32 v99, 1.0, v103
	v_rcp_f32_e32 v98, v98
	v_rcp_f32_e32 v99, v99
	v_add_f32_e32 v100, 1.0, v100
	v_add_f32_e32 v101, 1.0, v101
	v_rcp_f32_e32 v100, v100
	v_rcp_f32_e32 v101, v101
	v_pk_mul_f32 v[94:95], v[94:95], v[98:99]
	v_lshl_add_u64 v[102:103], v[136:137], 0, s[20:21]
	v_pk_mul_f32 v[90:91], v[90:91], v[94:95]
	v_pk_mul_f32 v[94:95], v[96:97], v[100:101]
	v_cvt_pk_bf16_f32 v90, v90, v91
	v_pk_mul_f32 v[92:93], v[92:93], v[94:95]
	v_mul_f32_e32 v96, 0xbfb8aa3b, v88
	v_cvt_pk_bf16_f32 v91, v92, v93
	v_mul_f32_e32 v92, 0xbfb8aa3b, v86
	v_exp_f32_e32 v94, v92
	v_mul_f32_e32 v92, 0xbfb8aa3b, v87
	v_exp_f32_e32 v95, v92
	v_mul_f32_e32 v97, 0xbfb8aa3b, v89
	v_exp_f32_e32 v96, v96
	v_exp_f32_e32 v97, v97
	v_add_f32_e32 v94, 1.0, v94
	v_add_f32_e32 v95, 1.0, v95
	v_rcp_f32_e32 v94, v94
	v_rcp_f32_e32 v95, v95
	v_add_f32_e32 v96, 1.0, v96
	v_add_f32_e32 v97, 1.0, v97
	v_rcp_f32_e32 v96, v96
	v_rcp_f32_e32 v97, v97
	v_pk_mul_f32 v[86:87], v[86:87], v[94:95]
	v_lshl_add_u64 v[92:93], v[102:103], 0, v[122:123]
	v_pk_mul_f32 v[82:83], v[82:83], v[86:87]
	v_pk_mul_f32 v[86:87], v[88:89], v[96:97]
	v_cvt_pk_bf16_f32 v82, v82, v83
	v_pk_mul_f32 v[84:85], v[84:85], v[86:87]
	v_mul_f32_e32 v86, 0xbfb8aa3b, v78
	v_cvt_pk_bf16_f32 v83, v84, v85
	v_lshl_add_u64 v[84:85], v[102:103], 0, v[114:115]
	v_mul_f32_e32 v87, 0xbfb8aa3b, v79
	global_store_dwordx2 v[92:93], v[90:91], off
	v_exp_f32_e32 v86, v86
	v_exp_f32_e32 v87, v87
	global_store_dwordx2 v[84:85], v[82:83], off
	v_mul_f32_e32 v84, 0xbfb8aa3b, v80
	v_mul_f32_e32 v85, 0xbfb8aa3b, v81
	v_exp_f32_e32 v84, v84
	v_exp_f32_e32 v85, v85
	v_add_f32_e32 v82, 1.0, v86
	v_add_f32_e32 v83, 1.0, v87
	v_rcp_f32_e32 v82, v82
	v_rcp_f32_e32 v83, v83
	v_add_f32_e32 v84, 1.0, v84
	v_add_f32_e32 v85, 1.0, v85
	v_rcp_f32_e32 v84, v84
	v_rcp_f32_e32 v85, v85
	v_pk_mul_f32 v[78:79], v[78:79], v[82:83]
	v_lshl_add_u64 v[86:87], v[136:137], 0, s[22:23]
	v_pk_mul_f32 v[74:75], v[74:75], v[78:79]
	v_pk_mul_f32 v[78:79], v[80:81], v[84:85]
	v_cvt_pk_bf16_f32 v74, v74, v75
	v_pk_mul_f32 v[76:77], v[76:77], v[78:79]
	v_mul_f32_e32 v80, 0xbfb8aa3b, v72
	v_cvt_pk_bf16_f32 v75, v76, v77
	v_mul_f32_e32 v76, 0xbfb8aa3b, v70
	v_exp_f32_e32 v78, v76
	v_mul_f32_e32 v76, 0xbfb8aa3b, v71
	v_exp_f32_e32 v79, v76
	v_mul_f32_e32 v81, 0xbfb8aa3b, v73
	v_exp_f32_e32 v80, v80
	v_exp_f32_e32 v81, v81
	v_add_f32_e32 v78, 1.0, v78
	v_add_f32_e32 v79, 1.0, v79
	v_rcp_f32_e32 v78, v78
	v_rcp_f32_e32 v79, v79
	v_add_f32_e32 v80, 1.0, v80
	v_add_f32_e32 v81, 1.0, v81
	v_rcp_f32_e32 v80, v80
	v_rcp_f32_e32 v81, v81
	v_pk_mul_f32 v[70:71], v[70:71], v[78:79]
	v_lshl_add_u64 v[76:77], v[86:87], 0, v[122:123]
	v_pk_mul_f32 v[66:67], v[66:67], v[70:71]
	v_pk_mul_f32 v[70:71], v[72:73], v[80:81]
	v_cvt_pk_bf16_f32 v66, v66, v67
	v_pk_mul_f32 v[68:69], v[68:69], v[70:71]
	v_mul_f32_e32 v70, 0xbfb8aa3b, v62
	v_cvt_pk_bf16_f32 v67, v68, v69
	v_lshl_add_u64 v[68:69], v[86:87], 0, v[114:115]
	v_mul_f32_e32 v71, 0xbfb8aa3b, v63
	global_store_dwordx2 v[76:77], v[74:75], off
	v_exp_f32_e32 v70, v70
	v_exp_f32_e32 v71, v71
	global_store_dwordx2 v[68:69], v[66:67], off
	v_mul_f32_e32 v68, 0xbfb8aa3b, v64
	v_mul_f32_e32 v69, 0xbfb8aa3b, v65
	v_exp_f32_e32 v68, v68
	v_exp_f32_e32 v69, v69
	v_add_f32_e32 v66, 1.0, v70
	v_add_f32_e32 v67, 1.0, v71
	v_rcp_f32_e32 v66, v66
	v_rcp_f32_e32 v67, v67
	v_add_f32_e32 v68, 1.0, v68
	v_add_f32_e32 v69, 1.0, v69
	v_rcp_f32_e32 v68, v68
	v_rcp_f32_e32 v69, v69
	v_pk_mul_f32 v[62:63], v[62:63], v[66:67]
	v_lshl_add_u64 v[70:71], v[136:137], 0, s[24:25]
	v_pk_mul_f32 v[58:59], v[58:59], v[62:63]
	v_pk_mul_f32 v[62:63], v[64:65], v[68:69]
	v_cvt_pk_bf16_f32 v58, v58, v59
	v_pk_mul_f32 v[60:61], v[60:61], v[62:63]
	v_mul_f32_e32 v64, 0xbfb8aa3b, v56
	v_cvt_pk_bf16_f32 v59, v60, v61
	v_mul_f32_e32 v60, 0xbfb8aa3b, v54
	v_exp_f32_e32 v62, v60
	v_mul_f32_e32 v60, 0xbfb8aa3b, v55
	v_exp_f32_e32 v63, v60
	v_mul_f32_e32 v65, 0xbfb8aa3b, v57
	v_exp_f32_e32 v64, v64
	v_exp_f32_e32 v65, v65
	v_add_f32_e32 v62, 1.0, v62
	v_add_f32_e32 v63, 1.0, v63
	v_rcp_f32_e32 v62, v62
	v_rcp_f32_e32 v63, v63
	v_add_f32_e32 v64, 1.0, v64
	v_add_f32_e32 v65, 1.0, v65
	v_rcp_f32_e32 v64, v64
	v_rcp_f32_e32 v65, v65
	v_pk_mul_f32 v[54:55], v[54:55], v[62:63]
	v_lshl_add_u64 v[60:61], v[70:71], 0, v[122:123]
	v_pk_mul_f32 v[50:51], v[50:51], v[54:55]
	v_pk_mul_f32 v[54:55], v[56:57], v[64:65]
	v_cvt_pk_bf16_f32 v50, v50, v51
	v_pk_mul_f32 v[52:53], v[52:53], v[54:55]
	v_mul_f32_e32 v54, 0xbfb8aa3b, v46
	v_cvt_pk_bf16_f32 v51, v52, v53
	v_lshl_add_u64 v[52:53], v[70:71], 0, v[114:115]
	v_mul_f32_e32 v55, 0xbfb8aa3b, v47
	global_store_dwordx2 v[60:61], v[58:59], off
	v_exp_f32_e32 v54, v54
	v_exp_f32_e32 v55, v55
	global_store_dwordx2 v[52:53], v[50:51], off
	v_mul_f32_e32 v52, 0xbfb8aa3b, v48
	v_mul_f32_e32 v53, 0xbfb8aa3b, v49
	v_exp_f32_e32 v52, v52
	v_exp_f32_e32 v53, v53
	v_add_f32_e32 v50, 1.0, v54
	v_add_f32_e32 v51, 1.0, v55
	v_rcp_f32_e32 v50, v50
	v_rcp_f32_e32 v51, v51
	v_add_f32_e32 v52, 1.0, v52
	v_add_f32_e32 v53, 1.0, v53
	v_rcp_f32_e32 v52, v52
	v_rcp_f32_e32 v53, v53
	v_pk_mul_f32 v[46:47], v[46:47], v[50:51]
	v_lshl_add_u64 v[54:55], v[136:137], 0, s[26:27]
	v_pk_mul_f32 v[42:43], v[42:43], v[46:47]
	v_pk_mul_f32 v[46:47], v[48:49], v[52:53]
	v_cvt_pk_bf16_f32 v42, v42, v43
	v_pk_mul_f32 v[44:45], v[44:45], v[46:47]
	v_mul_f32_e32 v48, 0xbfb8aa3b, v32
	v_cvt_pk_bf16_f32 v43, v44, v45
	v_mul_f32_e32 v44, 0xbfb8aa3b, v30
	v_exp_f32_e32 v46, v44
	v_mul_f32_e32 v44, 0xbfb8aa3b, v31
	v_exp_f32_e32 v47, v44
	v_mul_f32_e32 v49, 0xbfb8aa3b, v33
	v_exp_f32_e32 v48, v48
	v_exp_f32_e32 v49, v49
	v_add_f32_e32 v46, 1.0, v46
	v_add_f32_e32 v47, 1.0, v47
	v_rcp_f32_e32 v46, v46
	v_rcp_f32_e32 v47, v47
	v_add_f32_e32 v48, 1.0, v48
	v_add_f32_e32 v49, 1.0, v49
	v_rcp_f32_e32 v48, v48
	v_rcp_f32_e32 v49, v49
	v_pk_mul_f32 v[30:31], v[30:31], v[46:47]
	v_lshl_add_u64 v[44:45], v[54:55], 0, v[122:123]
	v_pk_mul_f32 v[26:27], v[26:27], v[30:31]
	v_pk_mul_f32 v[30:31], v[32:33], v[48:49]
	v_cvt_pk_bf16_f32 v26, v26, v27
	v_pk_mul_f32 v[28:29], v[28:29], v[30:31]
	v_mul_f32_e32 v30, 0xbfb8aa3b, v22
	v_cvt_pk_bf16_f32 v27, v28, v29
	v_lshl_add_u64 v[28:29], v[54:55], 0, v[114:115]
	v_mul_f32_e32 v31, 0xbfb8aa3b, v23
	global_store_dwordx2 v[44:45], v[42:43], off
	v_exp_f32_e32 v30, v30
	v_exp_f32_e32 v31, v31
	global_store_dwordx2 v[28:29], v[26:27], off
	v_mul_f32_e32 v28, 0xbfb8aa3b, v24
	v_mul_f32_e32 v29, 0xbfb8aa3b, v25
	v_exp_f32_e32 v28, v28
	v_exp_f32_e32 v29, v29
	v_add_f32_e32 v26, 1.0, v30
	v_add_f32_e32 v27, 1.0, v31
	v_rcp_f32_e32 v26, v26
	v_rcp_f32_e32 v27, v27
	v_add_f32_e32 v28, 1.0, v28
	v_add_f32_e32 v29, 1.0, v29
	v_rcp_f32_e32 v28, v28
	v_rcp_f32_e32 v29, v29
	v_pk_mul_f32 v[22:23], v[22:23], v[26:27]
	v_lshl_add_u64 v[30:31], v[136:137], 0, s[28:29]
	v_pk_mul_f32 v[18:19], v[18:19], v[22:23]
	v_pk_mul_f32 v[22:23], v[24:25], v[28:29]
	v_cvt_pk_bf16_f32 v18, v18, v19
	v_pk_mul_f32 v[20:21], v[20:21], v[22:23]
	v_mul_f32_e32 v24, 0xbfb8aa3b, v36
	v_cvt_pk_bf16_f32 v19, v20, v21
	v_mul_f32_e32 v20, 0xbfb8aa3b, v34
	v_exp_f32_e32 v22, v20
	v_mul_f32_e32 v20, 0xbfb8aa3b, v35
	v_mul_f32_e32 v25, 0xbfb8aa3b, v37
	v_exp_f32_e32 v23, v20
	v_exp_f32_e32 v24, v24
	v_exp_f32_e32 v25, v25
	v_add_f32_e32 v22, 1.0, v22
	v_add_f32_e32 v23, 1.0, v23
	v_add_f32_e32 v24, 1.0, v24
	v_add_f32_e32 v25, 1.0, v25
	v_rcp_f32_e32 v22, v22
	v_rcp_f32_e32 v23, v23
	v_rcp_f32_e32 v24, v24
	v_rcp_f32_e32 v25, v25
	v_lshl_add_u64 v[20:21], v[30:31], 0, v[122:123]
	global_store_dwordx2 v[20:21], v[18:19], off
	v_pk_mul_f32 v[18:19], v[34:35], v[22:23]
	v_pk_mul_f32 v[20:21], v[36:37], v[24:25]
	v_pk_mul_f32 v[18:19], v[38:39], v[18:19]
	v_pk_mul_f32 v[20:21], v[40:41], v[20:21]
	v_cvt_pk_bf16_f32 v18, v18, v19
	v_cvt_pk_bf16_f32 v19, v20, v21
	v_lshl_add_u64 v[20:21], v[30:31], 0, v[114:115]
	v_mul_f32_e32 v22, 0xbfb8aa3b, v6
	v_mul_f32_e32 v23, 0xbfb8aa3b, v7
	v_exp_f32_e32 v22, v22
	v_exp_f32_e32 v23, v23
	global_store_dwordx2 v[20:21], v[18:19], off
	v_mul_f32_e32 v20, 0xbfb8aa3b, v8
	v_mul_f32_e32 v21, 0xbfb8aa3b, v9
	v_exp_f32_e32 v20, v20
	v_exp_f32_e32 v21, v21
	v_add_f32_e32 v18, 1.0, v22
	v_add_f32_e32 v19, 1.0, v23
	v_rcp_f32_e32 v18, v18
	v_rcp_f32_e32 v19, v19
	v_add_f32_e32 v20, 1.0, v20
	v_add_f32_e32 v21, 1.0, v21
	v_rcp_f32_e32 v20, v20
	v_rcp_f32_e32 v21, v21
	v_pk_mul_f32 v[6:7], v[6:7], v[18:19]
	v_lshl_add_u64 v[22:23], v[136:137], 0, s[30:31]
	v_pk_mul_f32 v[2:3], v[2:3], v[6:7]
	v_pk_mul_f32 v[6:7], v[8:9], v[20:21]
	v_cvt_pk_bf16_f32 v2, v2, v3
	v_pk_mul_f32 v[4:5], v[4:5], v[6:7]
	v_mul_f32_e32 v8, 0xbfb8aa3b, v12
	v_cvt_pk_bf16_f32 v3, v4, v5
	v_mul_f32_e32 v4, 0xbfb8aa3b, v10
	v_exp_f32_e32 v6, v4
	v_mul_f32_e32 v4, 0xbfb8aa3b, v11
	v_mul_f32_e32 v9, 0xbfb8aa3b, v13
	v_exp_f32_e32 v7, v4
	v_exp_f32_e32 v8, v8
	v_exp_f32_e32 v9, v9
	v_add_f32_e32 v6, 1.0, v6
	v_add_f32_e32 v7, 1.0, v7
	v_add_f32_e32 v8, 1.0, v8
	v_add_f32_e32 v9, 1.0, v9
	v_rcp_f32_e32 v6, v6
	v_rcp_f32_e32 v7, v7
	v_rcp_f32_e32 v8, v8
	v_rcp_f32_e32 v9, v9
	v_lshl_add_u64 v[4:5], v[22:23], 0, v[122:123]
	global_store_dwordx2 v[4:5], v[2:3], off
	v_pk_mul_f32 v[2:3], v[10:11], v[6:7]
	v_pk_mul_f32 v[4:5], v[12:13], v[8:9]
	v_pk_mul_f32 v[2:3], v[14:15], v[2:3]
	v_pk_mul_f32 v[4:5], v[16:17], v[4:5]
	v_cvt_pk_bf16_f32 v2, v2, v3
	v_cvt_pk_bf16_f32 v3, v4, v5
	v_lshl_add_u64 v[4:5], v[22:23], 0, v[114:115]
	s_and_b64 vcc, exec, s[4:5]
	v_mov_b32_e32 v138, v156
	v_mov_b32_e32 v158, v154
	v_mov_b32_e32 v140, v157
	v_mov_b32_e32 v136, v155
	s_mov_b32 s84, s82
	s_mov_b32 s85, s83
	s_mov_b64 s[38:39], s[36:37]
	global_store_dwordx2 v[4:5], v[2:3], off
	s_cbranch_vccz .LBB0_908
	v_readlane_b32 s74, v255, 6
	v_readlane_b32 s75, v255, 7
	s_load_dwordx2 s[72:73], s[74:75], 0x148
	s_waitcnt vmcnt(0)
	s_cmpk_gt_u32 s42, 0xff
	v_readlane_b32 s71, v255, 4
	v_readlane_b32 s82, v255, 5
	s_cbranch_scc1 .LBB0_917
	s_barrier

.LBB0_986:
	s_add_u32 s0, s54, s6
	s_addc_u32 s1, s55, s7
	s_add_u32 s0, s0, 0x31600100
	ds_read_b128 v[162:165], v153
	ds_read_b128 v[166:169], v153 offset:1024
	ds_read_b128 v[170:173], v153 offset:2048
	ds_read_b128 v[174:177], v153 offset:3072
	s_addc_u32 s1, s1, 0
	s_add_u32 s91, s88, s6
	s_addc_u32 s92, s89, s7
	s_cmpk_eq_i32 s6, 0x300
	s_cselect_b64 vcc, -1, 0
	s_and_b64 s[38:39], vcc, exec
	v_cndmask_b32_e32 v134, v156, v157, vcc
	s_cselect_b32 s41, s11, s1
	s_cselect_b32 s40, s10, s0
	v_cndmask_b32_e32 v139, v138, v158, vcc
	v_cndmask_b32_e32 v186, v136, v159, vcc
	v_cndmask_b32_e32 v141, v140, v160, vcc
	s_cselect_b32 s39, s35, s92
	s_cselect_b32 s38, s87, s91
	v_lshl_add_u64 v[214:215], v[144:145], 0, s[6:7]
	s_add_i32 m0, s46, 0xc000
	ds_read_b128 v[178:181], v154
	ds_read_b128 v[182:185], v154 offset:1024
	ds_read_b128 v[190:193], v154 offset:2048
	ds_read_b128 v[194:197], v154 offset:3072
	ds_read_b128 v[198:201], v154 offset:4096
	ds_read_b128 v[202:205], v154 offset:5120
	ds_read_b128 v[206:209], v154 offset:6144
	ds_read_b128 v[210:213], v154 offset:7168
	global_load_lds_dwordx4 v[214:215], off
	v_lshl_add_u64 v[214:215], v[142:143], 0, s[6:7]
	s_add_i32 m0, s46, 0xe000
	s_nop 0
	global_load_lds_dwordx4 v[214:215], off
	s_waitcnt lgkmcnt(8)
	s_barrier
	s_waitcnt lgkmcnt(0)
	s_nop 0
	s_waitcnt lgkmcnt(0)
	v_mfma_f32_16x16x32_bf16 v[126:129], v[162:165], v[178:181], v[126:129]
	v_mfma_f32_16x16x32_bf16 v[122:125], v[170:173], v[178:181], v[122:125]
	v_mfma_f32_16x16x32_bf16 v[118:121], v[162:165], v[190:193], v[118:121]
	v_mfma_f32_16x16x32_bf16 v[114:117], v[170:173], v[190:193], v[114:117]
	v_mfma_f32_16x16x32_bf16 v[110:113], v[162:165], v[198:201], v[110:113]
	v_mfma_f32_16x16x32_bf16 v[106:109], v[170:173], v[198:201], v[106:109]
	v_mfma_f32_16x16x32_bf16 v[102:105], v[162:165], v[206:209], v[102:105]
	v_mfma_f32_16x16x32_bf16 v[98:101], v[170:173], v[206:209], v[98:101]
	v_mfma_f32_16x16x32_bf16 v[126:129], v[166:169], v[182:185], v[126:129]
	v_mfma_f32_16x16x32_bf16 v[122:125], v[174:177], v[182:185], v[122:125]
	v_mfma_f32_16x16x32_bf16 v[118:121], v[166:169], v[194:197], v[118:121]
	v_mfma_f32_16x16x32_bf16 v[114:117], v[174:177], v[194:197], v[114:117]
	v_mfma_f32_16x16x32_bf16 v[110:113], v[166:169], v[202:205], v[110:113]
	v_mfma_f32_16x16x32_bf16 v[106:109], v[174:177], v[202:205], v[106:109]
	v_mfma_f32_16x16x32_bf16 v[102:105], v[166:169], v[210:213], v[102:105]
	v_mfma_f32_16x16x32_bf16 v[98:101], v[174:177], v[210:213], v[98:101]
	s_nop 0
	s_barrier
	s_add_i32 s0, s75, s43
	v_lshl_add_u64 v[230:231], s[38:39], 0, v[132:133]
	s_mov_b32 m0, s0
	ds_read_b128 v[214:217], v155
	ds_read_b128 v[218:221], v155 offset:1024
	ds_read_b128 v[222:225], v155 offset:2048
	ds_read_b128 v[226:229], v155 offset:3072
	global_load_lds_dwordx4 v[230:231], off
	v_lshl_add_u64 v[232:233], s[38:39], 0, v[130:131]
	s_add_i32 m0, s0, 0x2000
	s_nop 0
	global_load_lds_dwordx4 v[232:233], off
	s_barrier
	s_waitcnt lgkmcnt(0)
	s_nop 0
	s_waitcnt lgkmcnt(0)
	v_mfma_f32_16x16x32_bf16 v[86:89], v[214:217], v[178:181], v[86:89]
	v_mfma_f32_16x16x32_bf16 v[78:81], v[222:225], v[178:181], v[78:81]
	v_mfma_f32_16x16x32_bf16 v[70:73], v[214:217], v[190:193], v[70:73]
	v_mfma_f32_16x16x32_bf16 v[62:65], v[222:225], v[190:193], v[62:65]
	v_mfma_f32_16x16x32_bf16 v[38:41], v[214:217], v[198:201], v[38:41]
	v_mfma_f32_16x16x32_bf16 v[34:37], v[222:225], v[198:201], v[34:37]
	v_mfma_f32_16x16x32_bf16 v[26:29], v[214:217], v[206:209], v[26:29]
	v_mfma_f32_16x16x32_bf16 v[18:21], v[222:225], v[206:209], v[18:21]
	v_mfma_f32_16x16x32_bf16 v[86:89], v[218:221], v[182:185], v[86:89]
	v_mfma_f32_16x16x32_bf16 v[78:81], v[226:229], v[182:185], v[78:81]
	v_mfma_f32_16x16x32_bf16 v[70:73], v[218:221], v[194:197], v[70:73]
	v_mfma_f32_16x16x32_bf16 v[62:65], v[226:229], v[194:197], v[62:65]
	v_mfma_f32_16x16x32_bf16 v[38:41], v[218:221], v[202:205], v[38:41]
	v_mfma_f32_16x16x32_bf16 v[34:37], v[226:229], v[202:205], v[34:37]
	v_mfma_f32_16x16x32_bf16 v[26:29], v[218:221], v[210:213], v[26:29]
	v_mfma_f32_16x16x32_bf16 v[18:21], v[226:229], v[210:213], v[18:21]
	s_nop 0
	s_mov_b32 m0, s46
	s_barrier
	ds_read_b128 v[178:181], v154 offset:16384
	ds_read_b128 v[182:185], v154 offset:17408
	ds_read_b128 v[190:193], v154 offset:18432
	ds_read_b128 v[194:197], v154 offset:19456
	ds_read_b128 v[198:201], v154 offset:20480
	ds_read_b128 v[202:205], v154 offset:21504
	ds_read_b128 v[206:209], v154 offset:22528
	ds_read_b128 v[210:213], v154 offset:23552
	global_load_lds_dwordx4 v134, s[40:41]
	s_mov_b32 m0, s47
	v_mov_b32_e32 v187, v135
	global_load_lds_dwordx4 v186, s[40:41]
	s_barrier
	s_waitcnt lgkmcnt(0)
	v_lshl_add_u64 v[234:235], s[40:41], 0, v[134:135]
	v_lshl_add_u64 v[186:187], s[40:41], 0, v[186:187]
	s_nop 0
	s_waitcnt lgkmcnt(0)
	v_mfma_f32_16x16x32_bf16 v[94:97], v[162:165], v[178:181], v[94:97]
	v_mfma_f32_16x16x32_bf16 v[90:93], v[170:173], v[178:181], v[90:93]
	v_mfma_f32_16x16x32_bf16 v[82:85], v[162:165], v[190:193], v[82:85]
	v_mfma_f32_16x16x32_bf16 v[74:77], v[170:173], v[190:193], v[74:77]
	v_mfma_f32_16x16x32_bf16 v[46:49], v[162:165], v[198:201], v[46:49]
	v_mfma_f32_16x16x32_bf16 v[42:45], v[170:173], v[198:201], v[42:45]
	v_mfma_f32_16x16x32_bf16 v[30:33], v[162:165], v[206:209], v[30:33]
	v_mfma_f32_16x16x32_bf16 v[22:25], v[170:173], v[206:209], v[22:25]
	v_mfma_f32_16x16x32_bf16 v[94:97], v[166:169], v[182:185], v[94:97]
	v_mfma_f32_16x16x32_bf16 v[90:93], v[174:177], v[182:185], v[90:93]
	v_mfma_f32_16x16x32_bf16 v[82:85], v[166:169], v[194:197], v[82:85]
	v_mfma_f32_16x16x32_bf16 v[74:77], v[174:177], v[194:197], v[74:77]
	v_mfma_f32_16x16x32_bf16 v[46:49], v[166:169], v[202:205], v[46:49]
	v_mfma_f32_16x16x32_bf16 v[42:45], v[174:177], v[202:205], v[42:45]
	v_mfma_f32_16x16x32_bf16 v[30:33], v[166:169], v[210:213], v[30:33]
	v_mfma_f32_16x16x32_bf16 v[22:25], v[174:177], v[210:213], v[22:25]
	s_nop 0
	s_barrier
	s_add_u32 s92, s38, 0x20000
	s_addc_u32 s93, s39, 0
	s_add_i32 s0, s76, s43
	v_lshl_add_u64 v[162:163], s[92:93], 0, v[132:133]
	s_mov_b32 m0, s0
	s_nop 0
	global_load_lds_dwordx4 v[162:163], off
	v_lshl_add_u64 v[162:163], s[92:93], 0, v[130:131]
	s_add_i32 m0, s0, 0x2000
	s_nop 0
	global_load_lds_dwordx4 v[162:163], off
	s_waitcnt vmcnt(6)
	s_barrier
	s_nop 0
	v_mfma_f32_16x16x32_bf16 v[14:17], v[214:217], v[178:181], v[14:17]
	v_mfma_f32_16x16x32_bf16 v[10:13], v[222:225], v[178:181], v[10:13]
	v_mfma_f32_16x16x32_bf16 v[6:9], v[214:217], v[190:193], v[6:9]
	v_mfma_f32_16x16x32_bf16 v[2:5], v[222:225], v[190:193], v[2:5]
	v_mfma_f32_16x16x32_bf16 v[54:57], v[214:217], v[198:201], v[54:57]
	v_mfma_f32_16x16x32_bf16 v[66:69], v[222:225], v[198:201], v[66:69]
	v_mfma_f32_16x16x32_bf16 v[50:53], v[214:217], v[206:209], v[50:53]
	v_mfma_f32_16x16x32_bf16 v[58:61], v[222:225], v[206:209], v[58:61]
	v_mfma_f32_16x16x32_bf16 v[14:17], v[218:221], v[182:185], v[14:17]
	v_mfma_f32_16x16x32_bf16 v[10:13], v[226:229], v[182:185], v[10:13]
	v_mfma_f32_16x16x32_bf16 v[6:9], v[218:221], v[194:197], v[6:9]
	v_mfma_f32_16x16x32_bf16 v[2:5], v[226:229], v[194:197], v[2:5]
	v_mfma_f32_16x16x32_bf16 v[54:57], v[218:221], v[202:205], v[54:57]
	v_mfma_f32_16x16x32_bf16 v[66:69], v[226:229], v[202:205], v[66:69]
	v_mfma_f32_16x16x32_bf16 v[50:53], v[218:221], v[210:213], v[50:53]
	v_mfma_f32_16x16x32_bf16 v[58:61], v[226:229], v[210:213], v[58:61]
	s_nop 0
	s_add_i32 s0, 0, 0x18000
	v_add_u32_e32 v134, s0, v150
	s_barrier
	ds_read_b128 v[162:165], v134
	ds_read_b128 v[166:169], v134 offset:1024
	ds_read_b128 v[170:173], v134 offset:2048
	ds_read_b128 v[174:177], v134 offset:3072
	s_mov_b32 m0, s48
	ds_read_b128 v[178:181], v154 offset:32768
	ds_read_b128 v[182:185], v154 offset:33792
	ds_read_b128 v[190:193], v154 offset:34816
	ds_read_b128 v[194:197], v154 offset:35840
	ds_read_b128 v[198:201], v154 offset:36864
	ds_read_b128 v[202:205], v154 offset:37888
	ds_read_b128 v[206:209], v154 offset:38912
	ds_read_b128 v[210:213], v154 offset:39936
	global_load_lds_dwordx4 v139, s[40:41]
	s_mov_b32 m0, s49
	s_nop 0
	global_load_lds_dwordx4 v141, s[40:41]
	s_waitcnt lgkmcnt(8)
	s_barrier
	s_waitcnt lgkmcnt(0)
	s_nop 0
	s_waitcnt lgkmcnt(0)
	v_mfma_f32_16x16x32_bf16 v[126:129], v[162:165], v[178:181], v[126:129]
	v_mfma_f32_16x16x32_bf16 v[122:125], v[170:173], v[178:181], v[122:125]
	v_mfma_f32_16x16x32_bf16 v[118:121], v[162:165], v[190:193], v[118:121]
	v_mfma_f32_16x16x32_bf16 v[114:117], v[170:173], v[190:193], v[114:117]
	v_mfma_f32_16x16x32_bf16 v[110:113], v[162:165], v[198:201], v[110:113]
	v_mfma_f32_16x16x32_bf16 v[106:109], v[170:173], v[198:201], v[106:109]
	v_mfma_f32_16x16x32_bf16 v[102:105], v[162:165], v[206:209], v[102:105]
	v_mfma_f32_16x16x32_bf16 v[98:101], v[170:173], v[206:209], v[98:101]
	v_mfma_f32_16x16x32_bf16 v[126:129], v[166:169], v[182:185], v[126:129]
	v_mfma_f32_16x16x32_bf16 v[122:125], v[174:177], v[182:185], v[122:125]
	v_mfma_f32_16x16x32_bf16 v[118:121], v[166:169], v[194:197], v[118:121]
	v_mfma_f32_16x16x32_bf16 v[114:117], v[174:177], v[194:197], v[114:117]
	v_mfma_f32_16x16x32_bf16 v[110:113], v[166:169], v[202:205], v[110:113]
	v_mfma_f32_16x16x32_bf16 v[106:109], v[174:177], v[202:205], v[106:109]
	v_mfma_f32_16x16x32_bf16 v[102:105], v[166:169], v[210:213], v[102:105]
	v_mfma_f32_16x16x32_bf16 v[98:101], v[174:177], v[210:213], v[98:101]
	s_nop 0
	s_barrier
	s_add_i32 s1, 0, 0x1c000
	s_add_i32 s0, s0, s43
	v_add_u32_e32 v134, s1, v150
	v_lshl_add_u64 v[230:231], v[230:231], 0, s[16:17]
	s_mov_b32 m0, s0
	ds_read_b128 v[214:217], v134
	ds_read_b128 v[218:221], v134 offset:1024
	ds_read_b128 v[222:225], v134 offset:2048
	ds_read_b128 v[226:229], v134 offset:3072
	global_load_lds_dwordx4 v[230:231], off
	v_lshl_add_u64 v[230:231], v[232:233], 0, s[16:17]
	s_add_i32 m0, s0, 0x2000
	s_nop 0
	global_load_lds_dwordx4 v[230:231], off
	s_barrier
	s_waitcnt lgkmcnt(0)
	s_nop 0
	s_waitcnt lgkmcnt(0)
	v_mfma_f32_16x16x32_bf16 v[86:89], v[214:217], v[178:181], v[86:89]
	v_mfma_f32_16x16x32_bf16 v[78:81], v[222:225], v[178:181], v[78:81]
	v_mfma_f32_16x16x32_bf16 v[70:73], v[214:217], v[190:193], v[70:73]
	v_mfma_f32_16x16x32_bf16 v[62:65], v[222:225], v[190:193], v[62:65]
	v_mfma_f32_16x16x32_bf16 v[38:41], v[214:217], v[198:201], v[38:41]
	v_mfma_f32_16x16x32_bf16 v[34:37], v[222:225], v[198:201], v[34:37]
	v_mfma_f32_16x16x32_bf16 v[26:29], v[214:217], v[206:209], v[26:29]
	v_mfma_f32_16x16x32_bf16 v[18:21], v[222:225], v[206:209], v[18:21]
	v_mfma_f32_16x16x32_bf16 v[86:89], v[218:221], v[182:185], v[86:89]
	v_mfma_f32_16x16x32_bf16 v[78:81], v[226:229], v[182:185], v[78:81]
	v_mfma_f32_16x16x32_bf16 v[70:73], v[218:221], v[194:197], v[70:73]
	v_mfma_f32_16x16x32_bf16 v[62:65], v[226:229], v[194:197], v[62:65]
	v_mfma_f32_16x16x32_bf16 v[38:41], v[218:221], v[202:205], v[38:41]
	v_mfma_f32_16x16x32_bf16 v[34:37], v[226:229], v[202:205], v[34:37]
	v_mfma_f32_16x16x32_bf16 v[26:29], v[218:221], v[210:213], v[26:29]
	v_mfma_f32_16x16x32_bf16 v[18:21], v[226:229], v[210:213], v[18:21]
	s_nop 0
	s_mov_b32 m0, s51
	v_lshl_add_u64 v[230:231], v[234:235], 0, s[16:17]
	s_barrier
	ds_read_b128 v[178:181], v154 offset:49152
	ds_read_b128 v[182:185], v154 offset:50176
	ds_read_b128 v[190:193], v154 offset:51200
	ds_read_b128 v[194:197], v154 offset:52224
	ds_read_b128 v[198:201], v154 offset:53248
	ds_read_b128 v[202:205], v154 offset:54272
	ds_read_b128 v[206:209], v154 offset:55296
	ds_read_b128 v[210:213], v154 offset:56320
	global_load_lds_dwordx4 v[230:231], off
	v_lshl_add_u64 v[186:187], v[186:187], 0, s[16:17]
	s_mov_b32 m0, s56
	s_nop 0
	global_load_lds_dwordx4 v[186:187], off
	s_barrier
	s_waitcnt lgkmcnt(0)
	s_nop 0
	s_waitcnt lgkmcnt(0)
	v_mfma_f32_16x16x32_bf16 v[94:97], v[162:165], v[178:181], v[94:97]
	v_mfma_f32_16x16x32_bf16 v[90:93], v[170:173], v[178:181], v[90:93]
	v_mfma_f32_16x16x32_bf16 v[82:85], v[162:165], v[190:193], v[82:85]
	v_mfma_f32_16x16x32_bf16 v[74:77], v[170:173], v[190:193], v[74:77]
	v_mfma_f32_16x16x32_bf16 v[46:49], v[162:165], v[198:201], v[46:49]
	v_mfma_f32_16x16x32_bf16 v[42:45], v[170:173], v[198:201], v[42:45]
	v_mfma_f32_16x16x32_bf16 v[30:33], v[162:165], v[206:209], v[30:33]
	v_mfma_f32_16x16x32_bf16 v[22:25], v[170:173], v[206:209], v[22:25]
	v_mfma_f32_16x16x32_bf16 v[94:97], v[166:169], v[182:185], v[94:97]
	v_mfma_f32_16x16x32_bf16 v[90:93], v[174:177], v[182:185], v[90:93]
	v_mfma_f32_16x16x32_bf16 v[82:85], v[166:169], v[194:197], v[82:85]
	v_mfma_f32_16x16x32_bf16 v[74:77], v[174:177], v[194:197], v[74:77]
	v_mfma_f32_16x16x32_bf16 v[46:49], v[166:169], v[202:205], v[46:49]
	v_mfma_f32_16x16x32_bf16 v[42:45], v[174:177], v[202:205], v[42:45]
	v_mfma_f32_16x16x32_bf16 v[30:33], v[166:169], v[210:213], v[30:33]
	v_mfma_f32_16x16x32_bf16 v[22:25], v[174:177], v[210:213], v[22:25]
	s_nop 0
	s_barrier
	s_add_u32 s38, s38, 0x20080
	s_addc_u32 s39, s39, 0
	s_add_i32 s0, s1, s43
	v_lshl_add_u64 v[162:163], s[38:39], 0, v[132:133]
	s_mov_b32 m0, s0
	s_nop 0
	global_load_lds_dwordx4 v[162:163], off
	v_lshl_add_u64 v[162:163], s[38:39], 0, v[130:131]
	s_add_i32 m0, s0, 0x2000
	s_nop 0
	global_load_lds_dwordx4 v[162:163], off
	s_waitcnt vmcnt(6)
	s_barrier
	s_nop 0
	v_mfma_f32_16x16x32_bf16 v[14:17], v[214:217], v[178:181], v[14:17]
	v_mfma_f32_16x16x32_bf16 v[10:13], v[222:225], v[178:181], v[10:13]
	v_mfma_f32_16x16x32_bf16 v[6:9], v[214:217], v[190:193], v[6:9]
	v_mfma_f32_16x16x32_bf16 v[2:5], v[222:225], v[190:193], v[2:5]
	v_mfma_f32_16x16x32_bf16 v[54:57], v[214:217], v[198:201], v[54:57]
	v_mfma_f32_16x16x32_bf16 v[66:69], v[222:225], v[198:201], v[66:69]
	v_mfma_f32_16x16x32_bf16 v[50:53], v[214:217], v[206:209], v[50:53]
	v_mfma_f32_16x16x32_bf16 v[58:61], v[222:225], v[206:209], v[58:61]
	v_mfma_f32_16x16x32_bf16 v[14:17], v[218:221], v[182:185], v[14:17]
	v_mfma_f32_16x16x32_bf16 v[10:13], v[226:229], v[182:185], v[10:13]
	v_mfma_f32_16x16x32_bf16 v[6:9], v[218:221], v[194:197], v[6:9]
	v_mfma_f32_16x16x32_bf16 v[2:5], v[226:229], v[194:197], v[2:5]
	v_mfma_f32_16x16x32_bf16 v[54:57], v[218:221], v[202:205], v[54:57]
	v_mfma_f32_16x16x32_bf16 v[66:69], v[226:229], v[202:205], v[66:69]
	v_mfma_f32_16x16x32_bf16 v[50:53], v[218:221], v[210:213], v[50:53]
	v_mfma_f32_16x16x32_bf16 v[58:61], v[226:229], v[210:213], v[58:61]
	s_nop 0
	s_add_i32 s90, s90, 2
	s_add_u32 s6, s6, 0x100
	s_addc_u32 s7, s7, 0
	s_cmp_gt_u32 s90, 5
	s_barrier
	s_cbranch_scc0 .LBB0_986
	v_add_u32_e32 v138, s84, v137
	v_add_u32_e32 v140, s83, v151
	v_ashrrev_i32_e32 v141, 31, v140
	v_ashrrev_i32_e32 v139, 31, v138
	v_lshl_add_u64 v[140:141], v[140:141], 1, s[14:15]
	v_cvt_pk_bf16_f32 v126, v126, v127
	v_cvt_pk_bf16_f32 v127, v128, v129
	v_cvt_pk_bf16_f32 v128, v122, v123
	v_lshlrev_b64 v[122:123], 12, v[138:139]
	v_lshl_add_u64 v[122:123], v[140:141], 0, v[122:123]
	v_cvt_pk_bf16_f32 v118, v118, v119
	v_cvt_pk_bf16_f32 v119, v120, v121
	v_cvt_pk_bf16_f32 v121, v116, v117
	v_add_co_u32_e32 v116, vcc, s50, v122
	v_cvt_pk_bf16_f32 v110, v110, v111
	s_nop 0
	v_addc_co_u32_e32 v117, vcc, 0, v123, vcc
	v_cvt_pk_bf16_f32 v111, v112, v113
	v_cvt_pk_bf16_f32 v113, v108, v109
	v_add_co_u32_e32 v108, vcc, s77, v122
	v_cvt_pk_bf16_f32 v102, v102, v103
	s_nop 0
	v_addc_co_u32_e32 v109, vcc, 0, v123, vcc
	v_cvt_pk_bf16_f32 v103, v104, v105
	v_cvt_pk_bf16_f32 v105, v100, v101
	v_add_co_u32_e32 v100, vcc, s78, v122
	v_cvt_pk_bf16_f32 v94, v94, v95
	s_nop 0
	v_addc_co_u32_e32 v101, vcc, 0, v123, vcc
	v_cvt_pk_bf16_f32 v95, v96, v97
	v_cvt_pk_bf16_f32 v97, v92, v93
	v_add_co_u32_e32 v92, vcc, s79, v122
	v_cvt_pk_bf16_f32 v82, v82, v83
	s_nop 0
	v_addc_co_u32_e32 v93, vcc, 0, v123, vcc
	v_cvt_pk_bf16_f32 v83, v84, v85
	v_cvt_pk_bf16_f32 v85, v76, v77
	v_add_co_u32_e32 v76, vcc, s80, v122
	v_cvt_pk_bf16_f32 v46, v46, v47
	s_nop 0
	v_addc_co_u32_e32 v77, vcc, 0, v123, vcc
	v_cvt_pk_bf16_f32 v47, v48, v49
	v_cvt_pk_bf16_f32 v49, v44, v45
	v_add_co_u32_e32 v44, vcc, s81, v122
	v_cvt_pk_bf16_f32 v30, v30, v31
	s_nop 0
	v_addc_co_u32_e32 v45, vcc, 0, v123, vcc
	v_cvt_pk_bf16_f32 v31, v32, v33
	v_cvt_pk_bf16_f32 v32, v22, v23
	v_add_co_u32_e32 v22, vcc, s82, v122
	v_cvt_pk_bf16_f32 v33, v24, v25
	s_nop 0
	v_addc_co_u32_e32 v23, vcc, 0, v123, vcc
	global_store_dwordx4 v[22:23], v[30:33], off
	v_cvt_pk_bf16_f32 v22, v86, v87
	v_cvt_pk_bf16_f32 v23, v88, v89
	v_cvt_pk_bf16_f32 v24, v78, v79
	v_cvt_pk_bf16_f32 v25, v80, v81
	v_cvt_pk_bf16_f32 v120, v114, v115
	v_lshl_add_u64 v[114:115], v[122:123], 0, s[20:21]
	global_store_dwordx4 v[122:123], v[22:25], off offset:256
	v_cvt_pk_bf16_f32 v112, v106, v107
	v_lshl_add_u64 v[106:107], v[122:123], 0, s[12:13]
	v_cvt_pk_bf16_f32 v22, v70, v71
	v_cvt_pk_bf16_f32 v23, v72, v73
	v_cvt_pk_bf16_f32 v24, v62, v63
	v_cvt_pk_bf16_f32 v25, v64, v65
	v_cvt_pk_bf16_f32 v48, v42, v43
	v_lshl_add_u64 v[42:43], v[122:123], 0, s[28:29]
	global_store_dwordx4 v[114:115], v[22:25], off offset:256
	v_cvt_pk_bf16_f32 v6, v6, v7
	v_cvt_pk_bf16_f32 v7, v8, v9
	v_cvt_pk_bf16_f32 v22, v38, v39
	v_cvt_pk_bf16_f32 v23, v40, v41
	v_cvt_pk_bf16_f32 v24, v34, v35
	v_cvt_pk_bf16_f32 v25, v36, v37
	v_cvt_pk_bf16_f32 v8, v2, v3
	v_cvt_pk_bf16_f32 v9, v4, v5
	v_cvt_pk_bf16_f32 v2, v54, v55
	v_cvt_pk_bf16_f32 v3, v56, v57
	v_cvt_pk_bf16_f32 v4, v66, v67
	v_cvt_pk_bf16_f32 v5, v68, v69
	v_cvt_pk_bf16_f32 v129, v124, v125
	v_cvt_pk_bf16_f32 v104, v98, v99
	v_lshl_add_u64 v[98:99], v[122:123], 0, s[22:23]
	v_cvt_pk_bf16_f32 v96, v90, v91
	v_lshl_add_u64 v[90:91], v[122:123], 0, s[24:25]
	v_cvt_pk_bf16_f32 v84, v74, v75
	v_lshl_add_u64 v[74:75], v[122:123], 0, s[26:27]
	global_store_dwordx4 v[44:45], v[46:49], off
	v_lshl_add_u64 v[44:45], v[122:123], 0, s[30:31]
	global_store_dwordx4 v[106:107], v[22:25], off offset:256
	v_cvt_pk_bf16_f32 v14, v14, v15
	v_cvt_pk_bf16_f32 v15, v16, v17
	v_cvt_pk_bf16_f32 v22, v26, v27
	v_cvt_pk_bf16_f32 v23, v28, v29
	v_cvt_pk_bf16_f32 v24, v18, v19
	v_cvt_pk_bf16_f32 v25, v20, v21
	v_cvt_pk_bf16_f32 v16, v10, v11
	v_cvt_pk_bf16_f32 v17, v12, v13
	global_store_dwordx4 v[42:43], v[2:5], off offset:256
	s_and_b64 vcc, exec, s[4:5]
	v_mov_b32_e32 v136, v159
	v_cvt_pk_bf16_f32 v2, v50, v51
	v_cvt_pk_bf16_f32 v3, v52, v53
	v_cvt_pk_bf16_f32 v4, v58, v59
	v_cvt_pk_bf16_f32 v5, v60, v61
	v_mov_b32_e32 v156, v157
	v_mov_b32_e32 v140, v160
	v_mov_b32_e32 v138, v158
	s_mov_b32 s83, s85
	s_mov_b32 s84, s86
	s_mov_b64 s[38:39], s[36:37]
	global_store_dwordx4 v[122:123], v[126:129], off
	global_store_dwordx4 v[116:117], v[118:121], off
	global_store_dwordx4 v[108:109], v[110:113], off
	global_store_dwordx4 v[100:101], v[102:105], off
	global_store_dwordx4 v[92:93], v[94:97], off
	global_store_dwordx4 v[76:77], v[82:85], off
	global_store_dwordx4 v[98:99], v[22:25], off offset:256
	global_store_dwordx4 v[90:91], v[14:17], off offset:256
	global_store_dwordx4 v[74:75], v[6:9], off offset:256
	global_store_dwordx4 v[44:45], v[2:5], off offset:256
	s_cbranch_vccz .LBB0_981
	v_readlane_b32 s74, v255, 6
	v_readlane_b32 s75, v255, 7
	s_load_dwordx2 s[72:73], s[74:75], 0x148
	s_waitcnt vmcnt(0)
	s_cmpk_gt_u32 s42, 0xff
	v_readlane_b32 s71, v255, 4
	v_readlane_b32 s82, v255, 5
	s_cbranch_scc1 .LBB0_990
	s_barrier

.LBB0_1324:
	v_add_u32_e32 v164, s72, v139
	s_add_u32 s0, s14, s8
	ds_read_b128 v[152:155], v164
	ds_read_b128 v[156:159], v164 offset:1024
	ds_read_b128 v[160:163], v164 offset:2048
	ds_read_b128 v[164:167], v164 offset:3072
	s_addc_u32 s1, s15, s9
	s_cmpk_eq_i32 s8, 0x1000
	s_cselect_b64 vcc, -1, 0
	s_and_b64 s[42:43], vcc, exec
	s_cselect_b32 s44, 0, s8
	s_cselect_b32 s45, 0, s9
	s_cselect_b32 s42, s78, s0
	s_cselect_b32 s43, s39, s1
	s_add_u32 s44, s54, s44
	v_cndmask_b32_e32 v142, v138, v186, vcc
	v_cndmask_b32_e32 v137, v136, v183, vcc
	v_cndmask_b32_e32 v234, v134, v184, vcc
	v_cndmask_b32_e32 v141, v140, v185, vcc
	s_addc_u32 s45, s55, s45
	v_lshl_add_u64 v[218:219], v[148:149], 0, s[8:9]
	v_lshl_add_u64 v[218:219], v[218:219], 0, s[18:19]
	s_add_i32 m0, s51, 0xc000
	ds_read_b128 v[168:171], v179
	ds_read_b128 v[190:193], v179 offset:1024
	ds_read_b128 v[194:197], v179 offset:2048
	ds_read_b128 v[198:201], v179 offset:3072
	ds_read_b128 v[202:205], v179 offset:4096
	ds_read_b128 v[206:209], v179 offset:5120
	ds_read_b128 v[210:213], v179 offset:6144
	ds_read_b128 v[214:217], v179 offset:7168
	global_load_lds_dwordx4 v[218:219], off
	v_lshl_add_u64 v[218:219], v[150:151], 0, s[8:9]
	v_lshl_add_u64 v[218:219], v[218:219], 0, s[18:19]
	s_add_i32 m0, s51, 0xe000
	s_nop 0
	global_load_lds_dwordx4 v[218:219], off
	s_waitcnt lgkmcnt(8)
	s_barrier
	s_waitcnt lgkmcnt(0)
	s_nop 0
	s_waitcnt lgkmcnt(0)
	v_mfma_f32_16x16x32_bf16 v[110:113], v[152:155], v[168:171], v[110:113]
	v_mfma_f32_16x16x32_bf16 v[106:109], v[160:163], v[168:171], v[106:109]
	v_mfma_f32_16x16x32_bf16 v[102:105], v[152:155], v[194:197], v[102:105]
	v_mfma_f32_16x16x32_bf16 v[98:101], v[160:163], v[194:197], v[98:101]
	v_mfma_f32_16x16x32_bf16 v[94:97], v[152:155], v[202:205], v[94:97]
	v_mfma_f32_16x16x32_bf16 v[90:93], v[160:163], v[202:205], v[90:93]
	v_mfma_f32_16x16x32_bf16 v[86:89], v[152:155], v[210:213], v[86:89]
	v_mfma_f32_16x16x32_bf16 v[82:85], v[160:163], v[210:213], v[82:85]
	v_mfma_f32_16x16x32_bf16 v[110:113], v[156:159], v[190:193], v[110:113]
	v_mfma_f32_16x16x32_bf16 v[106:109], v[164:167], v[190:193], v[106:109]
	v_mfma_f32_16x16x32_bf16 v[102:105], v[156:159], v[198:201], v[102:105]
	v_mfma_f32_16x16x32_bf16 v[98:101], v[164:167], v[198:201], v[98:101]
	v_mfma_f32_16x16x32_bf16 v[94:97], v[156:159], v[206:209], v[94:97]
	v_mfma_f32_16x16x32_bf16 v[90:93], v[164:167], v[206:209], v[90:93]
	v_mfma_f32_16x16x32_bf16 v[86:89], v[156:159], v[214:217], v[86:89]
	v_mfma_f32_16x16x32_bf16 v[82:85], v[164:167], v[214:217], v[82:85]
	s_nop 0
	s_barrier
	s_add_i32 s0, s72, s50
	v_add_u32_e32 v187, s73, v139
	v_lshl_add_u64 v[236:237], s[42:43], 0, v[130:131]
	s_mov_b32 m0, s0
	ds_read_b128 v[218:221], v187
	ds_read_b128 v[222:225], v187 offset:1024
	ds_read_b128 v[226:229], v187 offset:2048
	ds_read_b128 v[230:233], v187 offset:3072
	global_load_lds_dwordx4 v[236:237], off
	v_lshl_add_u64 v[238:239], s[42:43], 0, v[132:133]
	s_add_i32 m0, s0, 0x2000
	s_nop 0
	global_load_lds_dwordx4 v[238:239], off
	s_barrier
	s_waitcnt lgkmcnt(0)
	s_nop 0
	s_waitcnt lgkmcnt(0)
	v_mfma_f32_16x16x32_bf16 v[78:81], v[218:221], v[168:171], v[78:81]
	v_mfma_f32_16x16x32_bf16 v[74:77], v[226:229], v[168:171], v[74:77]
	v_mfma_f32_16x16x32_bf16 v[70:73], v[218:221], v[194:197], v[70:73]
	v_mfma_f32_16x16x32_bf16 v[66:69], v[226:229], v[194:197], v[66:69]
	v_mfma_f32_16x16x32_bf16 v[62:65], v[218:221], v[202:205], v[62:65]
	v_mfma_f32_16x16x32_bf16 v[58:61], v[226:229], v[202:205], v[58:61]
	v_mfma_f32_16x16x32_bf16 v[54:57], v[218:221], v[210:213], v[54:57]
	v_mfma_f32_16x16x32_bf16 v[50:53], v[226:229], v[210:213], v[50:53]
	v_mfma_f32_16x16x32_bf16 v[78:81], v[222:225], v[190:193], v[78:81]
	v_mfma_f32_16x16x32_bf16 v[74:77], v[230:233], v[190:193], v[74:77]
	v_mfma_f32_16x16x32_bf16 v[70:73], v[222:225], v[198:201], v[70:73]
	v_mfma_f32_16x16x32_bf16 v[66:69], v[230:233], v[198:201], v[66:69]
	v_mfma_f32_16x16x32_bf16 v[62:65], v[222:225], v[206:209], v[62:65]
	v_mfma_f32_16x16x32_bf16 v[58:61], v[230:233], v[206:209], v[58:61]
	v_mfma_f32_16x16x32_bf16 v[54:57], v[222:225], v[214:217], v[54:57]
	v_mfma_f32_16x16x32_bf16 v[50:53], v[230:233], v[214:217], v[50:53]
	s_nop 0
	s_mov_b32 m0, s51
	s_barrier
	ds_read_b128 v[168:171], v179 offset:16384
	ds_read_b128 v[190:193], v179 offset:17408
	ds_read_b128 v[194:197], v179 offset:18432
	ds_read_b128 v[198:201], v179 offset:19456
	ds_read_b128 v[202:205], v179 offset:20480
	ds_read_b128 v[206:209], v179 offset:21504
	ds_read_b128 v[210:213], v179 offset:22528
	ds_read_b128 v[214:217], v179 offset:23552
	global_load_lds_dwordx4 v142, s[44:45]
	s_mov_b32 m0, s56
	v_mov_b32_e32 v235, v143
	global_load_lds_dwordx4 v234, s[44:45]
	s_barrier
	s_waitcnt lgkmcnt(0)
	v_lshl_add_u64 v[240:241], s[44:45], 0, v[142:143]
	v_lshl_add_u64 v[234:235], s[44:45], 0, v[234:235]
	s_nop 0
	s_waitcnt lgkmcnt(0)
	v_mfma_f32_16x16x32_bf16 v[46:49], v[152:155], v[168:171], v[46:49]
	v_mfma_f32_16x16x32_bf16 v[42:45], v[160:163], v[168:171], v[42:45]
	v_mfma_f32_16x16x32_bf16 v[38:41], v[152:155], v[194:197], v[38:41]
	v_mfma_f32_16x16x32_bf16 v[34:37], v[160:163], v[194:197], v[34:37]
	v_mfma_f32_16x16x32_bf16 v[30:33], v[152:155], v[202:205], v[30:33]
	v_mfma_f32_16x16x32_bf16 v[26:29], v[160:163], v[202:205], v[26:29]
	v_mfma_f32_16x16x32_bf16 v[22:25], v[152:155], v[210:213], v[22:25]
	v_mfma_f32_16x16x32_bf16 v[18:21], v[160:163], v[210:213], v[18:21]
	v_mfma_f32_16x16x32_bf16 v[46:49], v[156:159], v[190:193], v[46:49]
	v_mfma_f32_16x16x32_bf16 v[42:45], v[164:167], v[190:193], v[42:45]
	v_mfma_f32_16x16x32_bf16 v[38:41], v[156:159], v[198:201], v[38:41]
	v_mfma_f32_16x16x32_bf16 v[34:37], v[164:167], v[198:201], v[34:37]
	v_mfma_f32_16x16x32_bf16 v[30:33], v[156:159], v[206:209], v[30:33]
	v_mfma_f32_16x16x32_bf16 v[26:29], v[164:167], v[206:209], v[26:29]
	v_mfma_f32_16x16x32_bf16 v[22:25], v[156:159], v[214:217], v[22:25]
	v_mfma_f32_16x16x32_bf16 v[18:21], v[164:167], v[214:217], v[18:21]
	s_nop 0
	s_barrier
	s_add_u32 s80, s42, 0x80000
	s_addc_u32 s81, s43, 0
	s_add_i32 s0, s73, s50
	v_lshl_add_u64 v[152:153], s[80:81], 0, v[130:131]
	s_mov_b32 m0, s0
	s_nop 0
	global_load_lds_dwordx4 v[152:153], off
	v_lshl_add_u64 v[152:153], s[80:81], 0, v[132:133]
	s_add_i32 m0, s0, 0x2000
	s_nop 0
	global_load_lds_dwordx4 v[152:153], off
	s_waitcnt vmcnt(6)
	s_barrier
	s_nop 0
	v_mfma_f32_16x16x32_bf16 v[14:17], v[218:221], v[168:171], v[14:17]
	v_mfma_f32_16x16x32_bf16 v[10:13], v[226:229], v[168:171], v[10:13]
	v_mfma_f32_16x16x32_bf16 v[6:9], v[218:221], v[194:197], v[6:9]
	v_mfma_f32_16x16x32_bf16 v[2:5], v[226:229], v[194:197], v[2:5]
	v_mfma_f32_16x16x32_bf16 v[114:117], v[218:221], v[202:205], v[114:117]
	v_mfma_f32_16x16x32_bf16 v[118:121], v[226:229], v[202:205], v[118:121]
	v_mfma_f32_16x16x32_bf16 v[122:125], v[218:221], v[210:213], v[122:125]
	v_mfma_f32_16x16x32_bf16 v[126:129], v[226:229], v[210:213], v[126:129]
	v_mfma_f32_16x16x32_bf16 v[14:17], v[222:225], v[190:193], v[14:17]
	v_mfma_f32_16x16x32_bf16 v[10:13], v[230:233], v[190:193], v[10:13]
	v_mfma_f32_16x16x32_bf16 v[6:9], v[222:225], v[198:201], v[6:9]
	v_mfma_f32_16x16x32_bf16 v[2:5], v[230:233], v[198:201], v[2:5]
	v_mfma_f32_16x16x32_bf16 v[114:117], v[222:225], v[206:209], v[114:117]
	v_mfma_f32_16x16x32_bf16 v[118:121], v[230:233], v[206:209], v[118:121]
	v_mfma_f32_16x16x32_bf16 v[122:125], v[222:225], v[214:217], v[122:125]
	v_mfma_f32_16x16x32_bf16 v[126:129], v[230:233], v[214:217], v[126:129]
	s_nop 0
	s_add_i32 s0, 0, 0x18000
	v_add_u32_e32 v142, s0, v139
	s_barrier
	ds_read_b128 v[152:155], v142
	ds_read_b128 v[156:159], v142 offset:1024
	ds_read_b128 v[160:163], v142 offset:2048
	ds_read_b128 v[164:167], v142 offset:3072
	s_mov_b32 m0, s57
	ds_read_b128 v[168:171], v179 offset:32768
	ds_read_b128 v[190:193], v179 offset:33792
	ds_read_b128 v[194:197], v179 offset:34816
	ds_read_b128 v[198:201], v179 offset:35840
	ds_read_b128 v[202:205], v179 offset:36864
	ds_read_b128 v[206:209], v179 offset:37888
	ds_read_b128 v[210:213], v179 offset:38912
	ds_read_b128 v[214:217], v179 offset:39936
	global_load_lds_dwordx4 v137, s[44:45]
	s_mov_b32 m0, s58
	s_nop 0
	global_load_lds_dwordx4 v141, s[44:45]
	s_waitcnt lgkmcnt(8)
	s_barrier
	s_waitcnt lgkmcnt(0)
	s_nop 0
	s_waitcnt lgkmcnt(0)
	v_mfma_f32_16x16x32_bf16 v[110:113], v[152:155], v[168:171], v[110:113]
	v_mfma_f32_16x16x32_bf16 v[106:109], v[160:163], v[168:171], v[106:109]
	v_mfma_f32_16x16x32_bf16 v[102:105], v[152:155], v[194:197], v[102:105]
	v_mfma_f32_16x16x32_bf16 v[98:101], v[160:163], v[194:197], v[98:101]
	v_mfma_f32_16x16x32_bf16 v[94:97], v[152:155], v[202:205], v[94:97]
	v_mfma_f32_16x16x32_bf16 v[90:93], v[160:163], v[202:205], v[90:93]
	v_mfma_f32_16x16x32_bf16 v[86:89], v[152:155], v[210:213], v[86:89]
	v_mfma_f32_16x16x32_bf16 v[82:85], v[160:163], v[210:213], v[82:85]
	v_mfma_f32_16x16x32_bf16 v[110:113], v[156:159], v[190:193], v[110:113]
	v_mfma_f32_16x16x32_bf16 v[106:109], v[164:167], v[190:193], v[106:109]
	v_mfma_f32_16x16x32_bf16 v[102:105], v[156:159], v[198:201], v[102:105]
	v_mfma_f32_16x16x32_bf16 v[98:101], v[164:167], v[198:201], v[98:101]
	v_mfma_f32_16x16x32_bf16 v[94:97], v[156:159], v[206:209], v[94:97]
	v_mfma_f32_16x16x32_bf16 v[90:93], v[164:167], v[206:209], v[90:93]
	v_mfma_f32_16x16x32_bf16 v[86:89], v[156:159], v[214:217], v[86:89]
	v_mfma_f32_16x16x32_bf16 v[82:85], v[164:167], v[214:217], v[82:85]
	s_nop 0
	s_barrier
	s_add_i32 s1, 0, 0x1c000
	s_add_i32 s0, s0, s50
	v_add_u32_e32 v137, s1, v139
	v_lshl_add_u64 v[236:237], v[236:237], 0, s[16:17]
	s_mov_b32 m0, s0
	ds_read_b128 v[218:221], v137
	ds_read_b128 v[222:225], v137 offset:1024
	ds_read_b128 v[226:229], v137 offset:2048
	ds_read_b128 v[230:233], v137 offset:3072
	global_load_lds_dwordx4 v[236:237], off
	v_lshl_add_u64 v[236:237], v[238:239], 0, s[16:17]
	s_add_i32 m0, s0, 0x2000
	s_nop 0
	global_load_lds_dwordx4 v[236:237], off
	s_barrier
	s_waitcnt lgkmcnt(0)
	s_nop 0
	s_waitcnt lgkmcnt(0)
	v_mfma_f32_16x16x32_bf16 v[78:81], v[218:221], v[168:171], v[78:81]
	v_mfma_f32_16x16x32_bf16 v[74:77], v[226:229], v[168:171], v[74:77]
	v_mfma_f32_16x16x32_bf16 v[70:73], v[218:221], v[194:197], v[70:73]
	v_mfma_f32_16x16x32_bf16 v[66:69], v[226:229], v[194:197], v[66:69]
	v_mfma_f32_16x16x32_bf16 v[62:65], v[218:221], v[202:205], v[62:65]
	v_mfma_f32_16x16x32_bf16 v[58:61], v[226:229], v[202:205], v[58:61]
	v_mfma_f32_16x16x32_bf16 v[54:57], v[218:221], v[210:213], v[54:57]
	v_mfma_f32_16x16x32_bf16 v[50:53], v[226:229], v[210:213], v[50:53]
	v_mfma_f32_16x16x32_bf16 v[78:81], v[222:225], v[190:193], v[78:81]
	v_mfma_f32_16x16x32_bf16 v[74:77], v[230:233], v[190:193], v[74:77]
	v_mfma_f32_16x16x32_bf16 v[70:73], v[222:225], v[198:201], v[70:73]
	v_mfma_f32_16x16x32_bf16 v[66:69], v[230:233], v[198:201], v[66:69]
	v_mfma_f32_16x16x32_bf16 v[62:65], v[222:225], v[206:209], v[62:65]
	v_mfma_f32_16x16x32_bf16 v[58:61], v[230:233], v[206:209], v[58:61]
	v_mfma_f32_16x16x32_bf16 v[54:57], v[222:225], v[214:217], v[54:57]
	v_mfma_f32_16x16x32_bf16 v[50:53], v[230:233], v[214:217], v[50:53]
	s_nop 0
	s_mov_b32 m0, s70
	v_lshl_add_u64 v[236:237], v[240:241], 0, s[16:17]
	s_barrier
	ds_read_b128 v[168:171], v179 offset:49152
	ds_read_b128 v[190:193], v179 offset:50176
	ds_read_b128 v[194:197], v179 offset:51200
	ds_read_b128 v[198:201], v179 offset:52224
	ds_read_b128 v[202:205], v179 offset:53248
	ds_read_b128 v[206:209], v179 offset:54272
	ds_read_b128 v[210:213], v179 offset:55296
	ds_read_b128 v[214:217], v179 offset:56320
	global_load_lds_dwordx4 v[236:237], off
	v_lshl_add_u64 v[234:235], v[234:235], 0, s[16:17]
	s_mov_b32 m0, s71
	s_nop 0
	global_load_lds_dwordx4 v[234:235], off
	s_barrier
	s_waitcnt lgkmcnt(0)
	s_nop 0
	s_waitcnt lgkmcnt(0)
	v_mfma_f32_16x16x32_bf16 v[46:49], v[152:155], v[168:171], v[46:49]
	v_mfma_f32_16x16x32_bf16 v[42:45], v[160:163], v[168:171], v[42:45]
	v_mfma_f32_16x16x32_bf16 v[38:41], v[152:155], v[194:197], v[38:41]
	v_mfma_f32_16x16x32_bf16 v[34:37], v[160:163], v[194:197], v[34:37]
	v_mfma_f32_16x16x32_bf16 v[30:33], v[152:155], v[202:205], v[30:33]
	v_mfma_f32_16x16x32_bf16 v[26:29], v[160:163], v[202:205], v[26:29]
	v_mfma_f32_16x16x32_bf16 v[22:25], v[152:155], v[210:213], v[22:25]
	v_mfma_f32_16x16x32_bf16 v[18:21], v[160:163], v[210:213], v[18:21]
	v_mfma_f32_16x16x32_bf16 v[46:49], v[156:159], v[190:193], v[46:49]
	v_mfma_f32_16x16x32_bf16 v[42:45], v[164:167], v[190:193], v[42:45]
	v_mfma_f32_16x16x32_bf16 v[38:41], v[156:159], v[198:201], v[38:41]
	v_mfma_f32_16x16x32_bf16 v[34:37], v[164:167], v[198:201], v[34:37]
	v_mfma_f32_16x16x32_bf16 v[30:33], v[156:159], v[206:209], v[30:33]
	v_mfma_f32_16x16x32_bf16 v[26:29], v[164:167], v[206:209], v[26:29]
	v_mfma_f32_16x16x32_bf16 v[22:25], v[156:159], v[214:217], v[22:25]
	v_mfma_f32_16x16x32_bf16 v[18:21], v[164:167], v[214:217], v[18:21]
	s_nop 0
	s_barrier
	s_add_u32 s42, s42, 0x80080
	s_addc_u32 s43, s43, 0
	s_add_i32 s0, s1, s50
	v_lshl_add_u64 v[152:153], s[42:43], 0, v[130:131]
	s_mov_b32 m0, s0
	s_nop 0
	global_load_lds_dwordx4 v[152:153], off
	v_lshl_add_u64 v[152:153], s[42:43], 0, v[132:133]
	s_add_i32 m0, s0, 0x2000
	s_nop 0
	global_load_lds_dwordx4 v[152:153], off
	s_waitcnt vmcnt(6)
	s_barrier
	s_nop 0
	v_mfma_f32_16x16x32_bf16 v[14:17], v[218:221], v[168:171], v[14:17]
	v_mfma_f32_16x16x32_bf16 v[10:13], v[226:229], v[168:171], v[10:13]
	v_mfma_f32_16x16x32_bf16 v[6:9], v[218:221], v[194:197], v[6:9]
	v_mfma_f32_16x16x32_bf16 v[2:5], v[226:229], v[194:197], v[2:5]
	v_mfma_f32_16x16x32_bf16 v[114:117], v[218:221], v[202:205], v[114:117]
	v_mfma_f32_16x16x32_bf16 v[118:121], v[226:229], v[202:205], v[118:121]
	v_mfma_f32_16x16x32_bf16 v[122:125], v[218:221], v[210:213], v[122:125]
	v_mfma_f32_16x16x32_bf16 v[126:129], v[226:229], v[210:213], v[126:129]
	v_mfma_f32_16x16x32_bf16 v[14:17], v[222:225], v[190:193], v[14:17]
	v_mfma_f32_16x16x32_bf16 v[10:13], v[230:233], v[190:193], v[10:13]
	v_mfma_f32_16x16x32_bf16 v[6:9], v[222:225], v[198:201], v[6:9]
	v_mfma_f32_16x16x32_bf16 v[2:5], v[230:233], v[198:201], v[2:5]
	v_mfma_f32_16x16x32_bf16 v[114:117], v[222:225], v[206:209], v[114:117]
	v_mfma_f32_16x16x32_bf16 v[118:121], v[230:233], v[206:209], v[118:121]
	v_mfma_f32_16x16x32_bf16 v[122:125], v[222:225], v[214:217], v[122:125]
	v_mfma_f32_16x16x32_bf16 v[126:129], v[230:233], v[214:217], v[126:129]
	s_nop 0
	s_add_i32 s79, s79, 2
	s_add_u32 s8, s8, 0x100
	s_addc_u32 s9, s9, 0
	s_cmp_gt_u32 s79, 29
	s_barrier
	s_cbranch_scc0 .LBB0_1324
	s_lshl_b32 s0, s21, 2
	s_lshr_b32 s1, 0x210, s0
	s_and_b32 s1, s1, 3
	s_mul_i32 s1, s1, 0x1100000
	s_add_u32 s42, s67, s1
	s_addc_u32 s43, s68, 0
	s_lshr_b32 s0, 0x201, s0
	s_and_b32 s39, s0, 3
	v_add_u32_e32 v150, s47, v178
	s_cmp_eq_u32 s39, 0
	v_add_u32_e32 v148, s46, v135
	v_ashrrev_i32_e32 v151, 31, v150
	s_cbranch_scc1 .LBB0_1334
	s_cmp_eq_u32 s39, 3
	s_cselect_b64 s[8:9], -1, 0
	v_lshl_add_u64 v[156:157], v[150:151], 2, s[12:13]
	v_bfrev_b32_e32 v152, 1
	s_and_b64 vcc, exec, s[8:9]
	v_bfrev_b32_e32 v164, 1
	v_bfrev_b32_e32 v165, 1
	v_bfrev_b32_e32 v160, 1
	v_bfrev_b32_e32 v161, 1
	v_bfrev_b32_e32 v166, 1
	v_bfrev_b32_e32 v167, 1
	v_bfrev_b32_e32 v162, 1
	v_bfrev_b32_e32 v163, 1
	s_cbranch_vccz .LBB0_1328
	global_load_dwordx4 v[158:161], v[156:157], off
	global_load_dwordx4 v[168:171], v[156:157], off offset:16
	s_waitcnt vmcnt(0)
	v_pk_mul_f32 v[162:163], v[160:161], s[20:21] op_sel_hi:[1,0]
	v_pk_mul_f32 v[166:167], v[158:159], s[20:21] op_sel_hi:[1,0]
	v_pk_mul_f32 v[160:161], v[170:171], s[20:21] op_sel_hi:[1,0]
	v_pk_mul_f32 v[164:165], v[168:169], s[20:21] op_sel_hi:[1,0]

.LBB0_1446:
	v_add_u32_e32 v171, s65, v139
	s_add_u32 s0, s12, s8
	ds_read_b128 v[158:161], v171
	ds_read_b128 v[162:165], v171 offset:1024
	ds_read_b128 v[166:169], v171 offset:2048
	ds_read_b128 v[174:177], v171 offset:3072
	s_addc_u32 s1, s13, s9
	s_cmpk_eq_i32 s8, 0x1000
	s_cselect_b64 vcc, -1, 0
	s_and_b64 s[38:39], vcc, exec
	s_cselect_b32 s40, 0, s8
	s_cselect_b32 s41, 0, s9
	s_cselect_b32 s38, s77, s0
	s_cselect_b32 s39, s35, s1
	s_add_u32 s40, s54, s40
	v_cndmask_b32_e32 v142, v138, v157, vcc
	v_cndmask_b32_e32 v137, v136, v154, vcc
	v_cndmask_b32_e32 v170, v134, v155, vcc
	v_cndmask_b32_e32 v141, v140, v156, vcc
	s_addc_u32 s41, s55, s41
	v_lshl_add_u64 v[186:187], v[148:149], 0, s[8:9]
	v_lshl_add_u64 v[186:187], v[186:187], 0, s[18:19]
	s_add_i32 m0, s50, 0xc000
	ds_read_b128 v[178:181], v153
	ds_read_b128 v[182:185], v153 offset:1024
	ds_read_b128 v[190:193], v153 offset:2048
	ds_read_b128 v[194:197], v153 offset:3072
	ds_read_b128 v[198:201], v153 offset:4096
	ds_read_b128 v[202:205], v153 offset:5120
	ds_read_b128 v[206:209], v153 offset:6144
	ds_read_b128 v[210:213], v153 offset:7168
	global_load_lds_dwordx4 v[186:187], off
	v_lshl_add_u64 v[186:187], v[150:151], 0, s[8:9]
	v_lshl_add_u64 v[186:187], v[186:187], 0, s[18:19]
	s_add_i32 m0, s50, 0xe000
	s_nop 0
	global_load_lds_dwordx4 v[186:187], off
	s_waitcnt lgkmcnt(8)
	s_barrier
	s_waitcnt lgkmcnt(0)
	s_nop 0
	s_waitcnt lgkmcnt(0)
	v_mfma_f32_16x16x32_bf16 v[110:113], v[158:161], v[178:181], v[110:113]
	v_mfma_f32_16x16x32_bf16 v[106:109], v[166:169], v[178:181], v[106:109]
	v_mfma_f32_16x16x32_bf16 v[102:105], v[158:161], v[190:193], v[102:105]
	v_mfma_f32_16x16x32_bf16 v[98:101], v[166:169], v[190:193], v[98:101]
	v_mfma_f32_16x16x32_bf16 v[94:97], v[158:161], v[198:201], v[94:97]
	v_mfma_f32_16x16x32_bf16 v[90:93], v[166:169], v[198:201], v[90:93]
	v_mfma_f32_16x16x32_bf16 v[86:89], v[158:161], v[206:209], v[86:89]
	v_mfma_f32_16x16x32_bf16 v[82:85], v[166:169], v[206:209], v[82:85]
	v_mfma_f32_16x16x32_bf16 v[110:113], v[162:165], v[182:185], v[110:113]
	v_mfma_f32_16x16x32_bf16 v[106:109], v[174:177], v[182:185], v[106:109]
	v_mfma_f32_16x16x32_bf16 v[102:105], v[162:165], v[194:197], v[102:105]
	v_mfma_f32_16x16x32_bf16 v[98:101], v[174:177], v[194:197], v[98:101]
	v_mfma_f32_16x16x32_bf16 v[94:97], v[162:165], v[202:205], v[94:97]
	v_mfma_f32_16x16x32_bf16 v[90:93], v[174:177], v[202:205], v[90:93]
	v_mfma_f32_16x16x32_bf16 v[86:89], v[162:165], v[210:213], v[86:89]
	v_mfma_f32_16x16x32_bf16 v[82:85], v[174:177], v[210:213], v[82:85]
	s_nop 0
	s_barrier
	s_add_i32 s0, s65, s49
	v_add_u32_e32 v171, s66, v139
	v_lshl_add_u64 v[186:187], s[38:39], 0, v[130:131]
	s_mov_b32 m0, s0
	ds_read_b128 v[214:217], v171
	ds_read_b128 v[218:221], v171 offset:1024
	ds_read_b128 v[222:225], v171 offset:2048
	ds_read_b128 v[226:229], v171 offset:3072
	global_load_lds_dwordx4 v[186:187], off
	v_lshl_add_u64 v[230:231], s[38:39], 0, v[132:133]
	s_add_i32 m0, s0, 0x2000
	s_nop 0
	global_load_lds_dwordx4 v[230:231], off
	s_barrier
	s_waitcnt lgkmcnt(0)
	s_nop 0
	s_waitcnt lgkmcnt(0)
	v_mfma_f32_16x16x32_bf16 v[78:81], v[214:217], v[178:181], v[78:81]
	v_mfma_f32_16x16x32_bf16 v[74:77], v[222:225], v[178:181], v[74:77]
	v_mfma_f32_16x16x32_bf16 v[70:73], v[214:217], v[190:193], v[70:73]
	v_mfma_f32_16x16x32_bf16 v[66:69], v[222:225], v[190:193], v[66:69]
	v_mfma_f32_16x16x32_bf16 v[62:65], v[214:217], v[198:201], v[62:65]
	v_mfma_f32_16x16x32_bf16 v[58:61], v[222:225], v[198:201], v[58:61]
	v_mfma_f32_16x16x32_bf16 v[54:57], v[214:217], v[206:209], v[54:57]
	v_mfma_f32_16x16x32_bf16 v[50:53], v[222:225], v[206:209], v[50:53]
	v_mfma_f32_16x16x32_bf16 v[78:81], v[218:221], v[182:185], v[78:81]
	v_mfma_f32_16x16x32_bf16 v[74:77], v[226:229], v[182:185], v[74:77]
	v_mfma_f32_16x16x32_bf16 v[70:73], v[218:221], v[194:197], v[70:73]
	v_mfma_f32_16x16x32_bf16 v[66:69], v[226:229], v[194:197], v[66:69]
	v_mfma_f32_16x16x32_bf16 v[62:65], v[218:221], v[202:205], v[62:65]
	v_mfma_f32_16x16x32_bf16 v[58:61], v[226:229], v[202:205], v[58:61]
	v_mfma_f32_16x16x32_bf16 v[54:57], v[218:221], v[210:213], v[54:57]
	v_mfma_f32_16x16x32_bf16 v[50:53], v[226:229], v[210:213], v[50:53]
	s_nop 0
	s_mov_b32 m0, s50
	s_barrier
	ds_read_b128 v[178:181], v153 offset:16384
	ds_read_b128 v[182:185], v153 offset:17408
	ds_read_b128 v[190:193], v153 offset:18432
	ds_read_b128 v[194:197], v153 offset:19456
	ds_read_b128 v[198:201], v153 offset:20480
	ds_read_b128 v[202:205], v153 offset:21504
	ds_read_b128 v[206:209], v153 offset:22528
	ds_read_b128 v[210:213], v153 offset:23552
	global_load_lds_dwordx4 v142, s[40:41]
	s_mov_b32 m0, s51
	v_mov_b32_e32 v171, v143
	global_load_lds_dwordx4 v170, s[40:41]
	s_barrier
	s_waitcnt lgkmcnt(0)
	v_lshl_add_u64 v[232:233], s[40:41], 0, v[142:143]
	v_lshl_add_u64 v[170:171], s[40:41], 0, v[170:171]
	s_nop 0
	s_waitcnt lgkmcnt(0)
	v_mfma_f32_16x16x32_bf16 v[46:49], v[158:161], v[178:181], v[46:49]
	v_mfma_f32_16x16x32_bf16 v[42:45], v[166:169], v[178:181], v[42:45]
	v_mfma_f32_16x16x32_bf16 v[38:41], v[158:161], v[190:193], v[38:41]
	v_mfma_f32_16x16x32_bf16 v[34:37], v[166:169], v[190:193], v[34:37]
	v_mfma_f32_16x16x32_bf16 v[30:33], v[158:161], v[198:201], v[30:33]
	v_mfma_f32_16x16x32_bf16 v[26:29], v[166:169], v[198:201], v[26:29]
	v_mfma_f32_16x16x32_bf16 v[22:25], v[158:161], v[206:209], v[22:25]
	v_mfma_f32_16x16x32_bf16 v[18:21], v[166:169], v[206:209], v[18:21]
	v_mfma_f32_16x16x32_bf16 v[46:49], v[162:165], v[182:185], v[46:49]
	v_mfma_f32_16x16x32_bf16 v[42:45], v[174:177], v[182:185], v[42:45]
	v_mfma_f32_16x16x32_bf16 v[38:41], v[162:165], v[194:197], v[38:41]
	v_mfma_f32_16x16x32_bf16 v[34:37], v[174:177], v[194:197], v[34:37]
	v_mfma_f32_16x16x32_bf16 v[30:33], v[162:165], v[202:205], v[30:33]
	v_mfma_f32_16x16x32_bf16 v[26:29], v[174:177], v[202:205], v[26:29]
	v_mfma_f32_16x16x32_bf16 v[22:25], v[162:165], v[210:213], v[22:25]
	v_mfma_f32_16x16x32_bf16 v[18:21], v[174:177], v[210:213], v[18:21]
	s_nop 0
	s_barrier
	s_add_u32 s80, s38, 0x80000
	s_addc_u32 s81, s39, 0
	s_add_i32 s0, s66, s49
	v_lshl_add_u64 v[158:159], s[80:81], 0, v[130:131]
	s_mov_b32 m0, s0
	s_nop 0
	global_load_lds_dwordx4 v[158:159], off
	v_lshl_add_u64 v[158:159], s[80:81], 0, v[132:133]
	s_add_i32 m0, s0, 0x2000
	s_nop 0
	global_load_lds_dwordx4 v[158:159], off
	s_waitcnt vmcnt(6)
	s_barrier
	s_nop 0
	v_mfma_f32_16x16x32_bf16 v[14:17], v[214:217], v[178:181], v[14:17]
	v_mfma_f32_16x16x32_bf16 v[10:13], v[222:225], v[178:181], v[10:13]
	v_mfma_f32_16x16x32_bf16 v[6:9], v[214:217], v[190:193], v[6:9]
	v_mfma_f32_16x16x32_bf16 v[2:5], v[222:225], v[190:193], v[2:5]
	v_mfma_f32_16x16x32_bf16 v[114:117], v[214:217], v[198:201], v[114:117]
	v_mfma_f32_16x16x32_bf16 v[118:121], v[222:225], v[198:201], v[118:121]
	v_mfma_f32_16x16x32_bf16 v[122:125], v[214:217], v[206:209], v[122:125]
	v_mfma_f32_16x16x32_bf16 v[126:129], v[222:225], v[206:209], v[126:129]
	v_mfma_f32_16x16x32_bf16 v[14:17], v[218:221], v[182:185], v[14:17]
	v_mfma_f32_16x16x32_bf16 v[10:13], v[226:229], v[182:185], v[10:13]
	v_mfma_f32_16x16x32_bf16 v[6:9], v[218:221], v[194:197], v[6:9]
	v_mfma_f32_16x16x32_bf16 v[2:5], v[226:229], v[194:197], v[2:5]
	v_mfma_f32_16x16x32_bf16 v[114:117], v[218:221], v[202:205], v[114:117]
	v_mfma_f32_16x16x32_bf16 v[118:121], v[226:229], v[202:205], v[118:121]
	v_mfma_f32_16x16x32_bf16 v[122:125], v[218:221], v[210:213], v[122:125]
	v_mfma_f32_16x16x32_bf16 v[126:129], v[226:229], v[210:213], v[126:129]
	s_nop 0
	s_add_i32 s0, 0, 0x18000
	v_add_u32_e32 v142, s0, v139
	s_barrier
	ds_read_b128 v[158:161], v142
	ds_read_b128 v[162:165], v142 offset:1024
	ds_read_b128 v[166:169], v142 offset:2048
	ds_read_b128 v[174:177], v142 offset:3072
	s_mov_b32 m0, s56
	ds_read_b128 v[178:181], v153 offset:32768
	ds_read_b128 v[182:185], v153 offset:33792
	ds_read_b128 v[190:193], v153 offset:34816
	ds_read_b128 v[194:197], v153 offset:35840
	ds_read_b128 v[198:201], v153 offset:36864
	ds_read_b128 v[202:205], v153 offset:37888
	ds_read_b128 v[206:209], v153 offset:38912
	ds_read_b128 v[210:213], v153 offset:39936
	global_load_lds_dwordx4 v137, s[40:41]
	s_mov_b32 m0, s57
	s_nop 0
	global_load_lds_dwordx4 v141, s[40:41]
	s_waitcnt lgkmcnt(8)
	s_barrier
	s_waitcnt lgkmcnt(0)
	s_nop 0
	s_waitcnt lgkmcnt(0)
	v_mfma_f32_16x16x32_bf16 v[110:113], v[158:161], v[178:181], v[110:113]
	v_mfma_f32_16x16x32_bf16 v[106:109], v[166:169], v[178:181], v[106:109]
	v_mfma_f32_16x16x32_bf16 v[102:105], v[158:161], v[190:193], v[102:105]
	v_mfma_f32_16x16x32_bf16 v[98:101], v[166:169], v[190:193], v[98:101]
	v_mfma_f32_16x16x32_bf16 v[94:97], v[158:161], v[198:201], v[94:97]
	v_mfma_f32_16x16x32_bf16 v[90:93], v[166:169], v[198:201], v[90:93]
	v_mfma_f32_16x16x32_bf16 v[86:89], v[158:161], v[206:209], v[86:89]
	v_mfma_f32_16x16x32_bf16 v[82:85], v[166:169], v[206:209], v[82:85]
	v_mfma_f32_16x16x32_bf16 v[110:113], v[162:165], v[182:185], v[110:113]
	v_mfma_f32_16x16x32_bf16 v[106:109], v[174:177], v[182:185], v[106:109]
	v_mfma_f32_16x16x32_bf16 v[102:105], v[162:165], v[194:197], v[102:105]
	v_mfma_f32_16x16x32_bf16 v[98:101], v[174:177], v[194:197], v[98:101]
	v_mfma_f32_16x16x32_bf16 v[94:97], v[162:165], v[202:205], v[94:97]
	v_mfma_f32_16x16x32_bf16 v[90:93], v[174:177], v[202:205], v[90:93]
	v_mfma_f32_16x16x32_bf16 v[86:89], v[162:165], v[210:213], v[86:89]
	v_mfma_f32_16x16x32_bf16 v[82:85], v[174:177], v[210:213], v[82:85]
	s_nop 0
	s_barrier
	s_add_i32 s1, 0, 0x1c000
	s_add_i32 s0, s0, s49
	v_add_u32_e32 v137, s1, v139
	v_lshl_add_u64 v[186:187], v[186:187], 0, s[16:17]
	s_mov_b32 m0, s0
	ds_read_b128 v[214:217], v137
	ds_read_b128 v[218:221], v137 offset:1024
	ds_read_b128 v[222:225], v137 offset:2048
	ds_read_b128 v[226:229], v137 offset:3072
	global_load_lds_dwordx4 v[186:187], off
	v_lshl_add_u64 v[186:187], v[230:231], 0, s[16:17]
	s_add_i32 m0, s0, 0x2000
	s_nop 0
	global_load_lds_dwordx4 v[186:187], off
	s_barrier
	s_waitcnt lgkmcnt(0)
	s_nop 0
	s_waitcnt lgkmcnt(0)
	v_mfma_f32_16x16x32_bf16 v[78:81], v[214:217], v[178:181], v[78:81]
	v_mfma_f32_16x16x32_bf16 v[74:77], v[222:225], v[178:181], v[74:77]
	v_mfma_f32_16x16x32_bf16 v[70:73], v[214:217], v[190:193], v[70:73]
	v_mfma_f32_16x16x32_bf16 v[66:69], v[222:225], v[190:193], v[66:69]
	v_mfma_f32_16x16x32_bf16 v[62:65], v[214:217], v[198:201], v[62:65]
	v_mfma_f32_16x16x32_bf16 v[58:61], v[222:225], v[198:201], v[58:61]
	v_mfma_f32_16x16x32_bf16 v[54:57], v[214:217], v[206:209], v[54:57]
	v_mfma_f32_16x16x32_bf16 v[50:53], v[222:225], v[206:209], v[50:53]
	v_mfma_f32_16x16x32_bf16 v[78:81], v[218:221], v[182:185], v[78:81]
	v_mfma_f32_16x16x32_bf16 v[74:77], v[226:229], v[182:185], v[74:77]
	v_mfma_f32_16x16x32_bf16 v[70:73], v[218:221], v[194:197], v[70:73]
	v_mfma_f32_16x16x32_bf16 v[66:69], v[226:229], v[194:197], v[66:69]
	v_mfma_f32_16x16x32_bf16 v[62:65], v[218:221], v[202:205], v[62:65]
	v_mfma_f32_16x16x32_bf16 v[58:61], v[226:229], v[202:205], v[58:61]
	v_mfma_f32_16x16x32_bf16 v[54:57], v[218:221], v[210:213], v[54:57]
	v_mfma_f32_16x16x32_bf16 v[50:53], v[226:229], v[210:213], v[50:53]
	s_nop 0
	s_mov_b32 m0, s62
	v_lshl_add_u64 v[186:187], v[232:233], 0, s[16:17]
	s_barrier
	ds_read_b128 v[178:181], v153 offset:49152
	ds_read_b128 v[182:185], v153 offset:50176
	ds_read_b128 v[190:193], v153 offset:51200
	ds_read_b128 v[194:197], v153 offset:52224
	ds_read_b128 v[198:201], v153 offset:53248
	ds_read_b128 v[202:205], v153 offset:54272
	ds_read_b128 v[206:209], v153 offset:55296
	ds_read_b128 v[210:213], v153 offset:56320
	global_load_lds_dwordx4 v[186:187], off
	v_lshl_add_u64 v[170:171], v[170:171], 0, s[16:17]
	s_mov_b32 m0, s63
	s_nop 0
	global_load_lds_dwordx4 v[170:171], off
	s_barrier
	s_waitcnt lgkmcnt(0)
	s_nop 0
	s_waitcnt lgkmcnt(0)
	v_mfma_f32_16x16x32_bf16 v[46:49], v[158:161], v[178:181], v[46:49]
	v_mfma_f32_16x16x32_bf16 v[42:45], v[166:169], v[178:181], v[42:45]
	v_mfma_f32_16x16x32_bf16 v[38:41], v[158:161], v[190:193], v[38:41]
	v_mfma_f32_16x16x32_bf16 v[34:37], v[166:169], v[190:193], v[34:37]
	v_mfma_f32_16x16x32_bf16 v[30:33], v[158:161], v[198:201], v[30:33]
	v_mfma_f32_16x16x32_bf16 v[26:29], v[166:169], v[198:201], v[26:29]
	v_mfma_f32_16x16x32_bf16 v[22:25], v[158:161], v[206:209], v[22:25]
	v_mfma_f32_16x16x32_bf16 v[18:21], v[166:169], v[206:209], v[18:21]
	v_mfma_f32_16x16x32_bf16 v[46:49], v[162:165], v[182:185], v[46:49]
	v_mfma_f32_16x16x32_bf16 v[42:45], v[174:177], v[182:185], v[42:45]
	v_mfma_f32_16x16x32_bf16 v[38:41], v[162:165], v[194:197], v[38:41]
	v_mfma_f32_16x16x32_bf16 v[34:37], v[174:177], v[194:197], v[34:37]
	v_mfma_f32_16x16x32_bf16 v[30:33], v[162:165], v[202:205], v[30:33]
	v_mfma_f32_16x16x32_bf16 v[26:29], v[174:177], v[202:205], v[26:29]
	v_mfma_f32_16x16x32_bf16 v[22:25], v[162:165], v[210:213], v[22:25]
	v_mfma_f32_16x16x32_bf16 v[18:21], v[174:177], v[210:213], v[18:21]
	s_nop 0
	s_barrier
	s_add_u32 s38, s38, 0x80080
	s_addc_u32 s39, s39, 0
	s_add_i32 s0, s1, s49
	v_lshl_add_u64 v[158:159], s[38:39], 0, v[130:131]
	s_mov_b32 m0, s0
	s_nop 0
	global_load_lds_dwordx4 v[158:159], off
	v_lshl_add_u64 v[158:159], s[38:39], 0, v[132:133]
	s_add_i32 m0, s0, 0x2000
	s_nop 0
	global_load_lds_dwordx4 v[158:159], off
	s_waitcnt vmcnt(6)
	s_barrier
	s_nop 0
	v_mfma_f32_16x16x32_bf16 v[14:17], v[214:217], v[178:181], v[14:17]
	v_mfma_f32_16x16x32_bf16 v[10:13], v[222:225], v[178:181], v[10:13]
	v_mfma_f32_16x16x32_bf16 v[6:9], v[214:217], v[190:193], v[6:9]
	v_mfma_f32_16x16x32_bf16 v[2:5], v[222:225], v[190:193], v[2:5]
	v_mfma_f32_16x16x32_bf16 v[114:117], v[214:217], v[198:201], v[114:117]
	v_mfma_f32_16x16x32_bf16 v[118:121], v[222:225], v[198:201], v[118:121]
	v_mfma_f32_16x16x32_bf16 v[122:125], v[214:217], v[206:209], v[122:125]
	v_mfma_f32_16x16x32_bf16 v[126:129], v[222:225], v[206:209], v[126:129]
	v_mfma_f32_16x16x32_bf16 v[14:17], v[218:221], v[182:185], v[14:17]
	v_mfma_f32_16x16x32_bf16 v[10:13], v[226:229], v[182:185], v[10:13]
	v_mfma_f32_16x16x32_bf16 v[6:9], v[218:221], v[194:197], v[6:9]
	v_mfma_f32_16x16x32_bf16 v[2:5], v[226:229], v[194:197], v[2:5]
	v_mfma_f32_16x16x32_bf16 v[114:117], v[218:221], v[202:205], v[114:117]
	v_mfma_f32_16x16x32_bf16 v[118:121], v[226:229], v[202:205], v[118:121]
	v_mfma_f32_16x16x32_bf16 v[122:125], v[218:221], v[210:213], v[122:125]
	v_mfma_f32_16x16x32_bf16 v[126:129], v[226:229], v[210:213], v[126:129]
	s_nop 0
	s_add_i32 s78, s78, 2
	s_add_u32 s8, s8, 0x100
	s_addc_u32 s9, s9, 0
	s_cmp_gt_u32 s78, 29
	s_barrier
	s_cbranch_scc0 .LBB0_1446
	s_lshl_b32 s0, s44, 2
	s_lshr_b32 s0, 0x210, s0
	s_and_b32 s0, s0, 3
	s_mul_i32 s0, s0, 0x8200000
	s_add_u32 s8, s60, s0
	v_add_u32_e32 v158, s45, v135
	v_add_u32_e32 v148, s46, v152
	s_addc_u32 s9, s61, 0
	v_ashrrev_i32_e32 v149, 31, v148
	v_ashrrev_i32_e32 v159, 31, v158
	v_lshl_add_u64 v[160:161], v[148:149], 1, s[8:9]
	v_lshlrev_b64 v[158:159], 12, v[158:159]
	v_lshl_add_u64 v[158:159], v[160:161], 0, v[158:159]
	v_add_co_u32_e32 v162, vcc, s58, v158
	v_cvt_pk_bf16_f32 v148, v110, v111
	s_nop 0
	v_addc_co_u32_e32 v163, vcc, 0, v159, vcc
	v_add_co_u32_e32 v164, vcc, s67, v158
	v_cvt_pk_bf16_f32 v149, v112, v113
	s_nop 0
	v_addc_co_u32_e32 v165, vcc, 0, v159, vcc
	v_add_co_u32_e32 v166, vcc, s68, v158
	v_cvt_pk_bf16_f32 v150, v106, v107
	s_nop 0
	v_addc_co_u32_e32 v167, vcc, 0, v159, vcc
	v_cvt_pk_bf16_f32 v151, v108, v109
	v_add_co_u32_e32 v168, vcc, s69, v158
	global_store_dwordx4 v[158:159], v[148:151], off
	s_nop 0
	v_addc_co_u32_e32 v169, vcc, 0, v159, vcc
	v_cvt_pk_bf16_f32 v148, v102, v103
	v_cvt_pk_bf16_f32 v149, v104, v105
	v_cvt_pk_bf16_f32 v150, v98, v99
	v_cvt_pk_bf16_f32 v151, v100, v101
	global_store_dwordx4 v[162:163], v[148:151], off
	v_add_co_u32_e32 v170, vcc, s70, v158
	s_nop 0
	v_cvt_pk_bf16_f32 v148, v94, v95
	v_cvt_pk_bf16_f32 v149, v96, v97
	v_cvt_pk_bf16_f32 v150, v90, v91
	v_cvt_pk_bf16_f32 v151, v92, v93
	global_store_dwordx4 v[164:165], v[148:151], off
	v_addc_co_u32_e32 v171, vcc, 0, v159, vcc
	s_nop 0
	v_cvt_pk_bf16_f32 v148, v86, v87
	v_cvt_pk_bf16_f32 v149, v88, v89
	v_cvt_pk_bf16_f32 v150, v82, v83
	v_cvt_pk_bf16_f32 v151, v84, v85
	global_store_dwordx4 v[166:167], v[148:151], off
	v_add_co_u32_e32 v174, vcc, s71, v158
	s_nop 0
	v_cvt_pk_bf16_f32 v148, v46, v47
	v_cvt_pk_bf16_f32 v149, v48, v49
	v_cvt_pk_bf16_f32 v150, v42, v43
	v_cvt_pk_bf16_f32 v151, v44, v45
	global_store_dwordx4 v[168:169], v[148:151], off
	v_addc_co_u32_e32 v175, vcc, 0, v159, vcc
	s_nop 0
	v_cvt_pk_bf16_f32 v148, v38, v39
	v_cvt_pk_bf16_f32 v149, v40, v41
	v_cvt_pk_bf16_f32 v150, v34, v35
	v_cvt_pk_bf16_f32 v151, v36, v37
	global_store_dwordx4 v[170:171], v[148:151], off
	v_add_co_u32_e32 v176, vcc, s72, v158
	s_nop 0
	v_cvt_pk_bf16_f32 v148, v30, v31
	v_cvt_pk_bf16_f32 v149, v32, v33
	v_cvt_pk_bf16_f32 v150, v26, v27
	v_cvt_pk_bf16_f32 v151, v28, v29
	global_store_dwordx4 v[174:175], v[148:151], off
	v_addc_co_u32_e32 v177, vcc, 0, v159, vcc
	s_nop 0
	v_cvt_pk_bf16_f32 v148, v22, v23
	v_cvt_pk_bf16_f32 v149, v24, v25
	v_cvt_pk_bf16_f32 v150, v18, v19
	v_cvt_pk_bf16_f32 v151, v20, v21
	global_store_dwordx4 v[176:177], v[148:151], off
	v_lshl_add_u64 v[160:161], v[158:159], 0, s[20:21]
	v_lshl_add_u64 v[162:163], v[158:159], 0, s[22:23]
	v_cvt_pk_bf16_f32 v148, v78, v79
	v_cvt_pk_bf16_f32 v149, v80, v81
	v_cvt_pk_bf16_f32 v150, v74, v75
	v_cvt_pk_bf16_f32 v151, v76, v77
	global_store_dwordx4 v[158:159], v[148:151], off offset:256
	v_lshl_add_u64 v[164:165], v[158:159], 0, s[24:25]
	v_lshl_add_u64 v[166:167], v[158:159], 0, s[14:15]
	v_cvt_pk_bf16_f32 v148, v70, v71
	v_cvt_pk_bf16_f32 v149, v72, v73
	v_cvt_pk_bf16_f32 v150, v66, v67
	v_cvt_pk_bf16_f32 v151, v68, v69
	global_store_dwordx4 v[160:161], v[148:151], off offset:256
	v_lshl_add_u64 v[168:169], v[158:159], 0, s[26:27]
	v_lshl_add_u64 v[170:171], v[158:159], 0, s[28:29]
	v_cvt_pk_bf16_f32 v148, v62, v63
	v_cvt_pk_bf16_f32 v149, v64, v65
	v_cvt_pk_bf16_f32 v150, v58, v59
	v_cvt_pk_bf16_f32 v151, v60, v61
	global_store_dwordx4 v[162:163], v[148:151], off offset:256
	v_lshl_add_u64 v[174:175], v[158:159], 0, s[30:31]
	s_and_b64 vcc, exec, s[6:7]
	v_cvt_pk_bf16_f32 v148, v54, v55
	v_cvt_pk_bf16_f32 v149, v56, v57
	v_cvt_pk_bf16_f32 v150, v50, v51
	v_cvt_pk_bf16_f32 v151, v52, v53
	global_store_dwordx4 v[164:165], v[148:151], off offset:256
	s_nop 1
	v_cvt_pk_bf16_f32 v148, v14, v15
	v_cvt_pk_bf16_f32 v149, v16, v17
	v_cvt_pk_bf16_f32 v150, v10, v11
	v_cvt_pk_bf16_f32 v151, v12, v13
	global_store_dwordx4 v[166:167], v[148:151], off offset:256
	s_nop 1
	v_cvt_pk_bf16_f32 v148, v6, v7
	v_cvt_pk_bf16_f32 v149, v8, v9
	v_cvt_pk_bf16_f32 v150, v2, v3
	v_cvt_pk_bf16_f32 v151, v4, v5
	global_store_dwordx4 v[168:169], v[148:151], off offset:256
	s_nop 1
	v_cvt_pk_bf16_f32 v148, v114, v115
	v_cvt_pk_bf16_f32 v149, v116, v117
	v_cvt_pk_bf16_f32 v150, v118, v119
	v_cvt_pk_bf16_f32 v151, v120, v121
	global_store_dwordx4 v[170:171], v[148:151], off offset:256
	s_nop 1
	v_cvt_pk_bf16_f32 v148, v122, v123
	v_cvt_pk_bf16_f32 v149, v124, v125
	v_cvt_pk_bf16_f32 v150, v126, v127
	v_cvt_pk_bf16_f32 v151, v128, v129
	global_store_dwordx4 v[174:175], v[148:151], off offset:256
	s_cbranch_vccnz .LBB0_1392
	v_mov_b32_e32 v2, 0
	v_mov_b32_e32 v134, v155
	v_mov_b32_e32 v138, v157
	v_mov_b32_e32 v140, v156
	v_mov_b32_e32 v136, v154
	s_mov_b32 s44, s73
	s_mov_b32 s46, s75
	s_mov_b32 s45, s74
	s_mov_b64 s[12:13], s[36:37]
	s_mov_b32 s59, s76
	v_mov_b32_e32 v3, v2
	v_mov_b32_e32 v4, v2
	v_mov_b32_e32 v5, v2
	v_mov_b32_e32 v6, v2
	v_mov_b32_e32 v7, v2
	v_mov_b32_e32 v8, v2
	v_mov_b32_e32 v9, v2
	v_mov_b32_e32 v10, v2
	v_mov_b32_e32 v11, v2
	v_mov_b32_e32 v12, v2
	v_mov_b32_e32 v13, v2
	v_mov_b32_e32 v14, v2
	v_mov_b32_e32 v15, v2
	v_mov_b32_e32 v16, v2
	v_mov_b32_e32 v17, v2
	v_mov_b32_e32 v18, v2
	v_mov_b32_e32 v19, v2
	v_mov_b32_e32 v20, v2
	v_mov_b32_e32 v21, v2
	v_mov_b32_e32 v22, v2
	v_mov_b32_e32 v23, v2
	v_mov_b32_e32 v24, v2
	v_mov_b32_e32 v25, v2
	v_mov_b32_e32 v26, v2
	v_mov_b32_e32 v27, v2
	v_mov_b32_e32 v28, v2
	v_mov_b32_e32 v29, v2
	v_mov_b32_e32 v30, v2
	v_mov_b32_e32 v31, v2
	v_mov_b32_e32 v32, v2
	v_mov_b32_e32 v33, v2
	v_mov_b32_e32 v34, v2
	v_mov_b32_e32 v35, v2
	v_mov_b32_e32 v36, v2
	v_mov_b32_e32 v37, v2
	v_mov_b32_e32 v38, v2
	v_mov_b32_e32 v39, v2
	v_mov_b32_e32 v40, v2
	v_mov_b32_e32 v41, v2
	v_mov_b32_e32 v42, v2
	v_mov_b32_e32 v43, v2
	v_mov_b32_e32 v44, v2
	v_mov_b32_e32 v45, v2
	v_mov_b32_e32 v46, v2
	v_mov_b32_e32 v47, v2
	v_mov_b32_e32 v48, v2
	v_mov_b32_e32 v49, v2
	v_mov_b32_e32 v50, v2
	v_mov_b32_e32 v51, v2
	v_mov_b32_e32 v52, v2
	v_mov_b32_e32 v53, v2
	v_mov_b32_e32 v54, v2
	v_mov_b32_e32 v55, v2
	v_mov_b32_e32 v56, v2
	v_mov_b32_e32 v57, v2
	v_mov_b32_e32 v58, v2
	v_mov_b32_e32 v59, v2
	v_mov_b32_e32 v60, v2
	v_mov_b32_e32 v61, v2
	v_mov_b32_e32 v62, v2
	v_mov_b32_e32 v63, v2
	v_mov_b32_e32 v64, v2
	v_mov_b32_e32 v65, v2
	v_mov_b32_e32 v66, v2
	v_mov_b32_e32 v67, v2
	v_mov_b32_e32 v68, v2
	v_mov_b32_e32 v69, v2
	v_mov_b32_e32 v70, v2
	v_mov_b32_e32 v71, v2
	v_mov_b32_e32 v72, v2
	v_mov_b32_e32 v73, v2
	v_mov_b32_e32 v74, v2
	v_mov_b32_e32 v75, v2
	v_mov_b32_e32 v76, v2
	v_mov_b32_e32 v77, v2
	v_mov_b32_e32 v78, v2
	v_mov_b32_e32 v79, v2
	v_mov_b32_e32 v80, v2
	v_mov_b32_e32 v81, v2
	v_mov_b32_e32 v82, v2
	v_mov_b32_e32 v83, v2
	v_mov_b32_e32 v84, v2
	v_mov_b32_e32 v85, v2
	v_mov_b32_e32 v86, v2
	v_mov_b32_e32 v87, v2
	v_mov_b32_e32 v88, v2
	v_mov_b32_e32 v89, v2
	v_mov_b32_e32 v90, v2
	v_mov_b32_e32 v91, v2
	v_mov_b32_e32 v92, v2
	v_mov_b32_e32 v93, v2
	v_mov_b32_e32 v94, v2
	v_mov_b32_e32 v95, v2
	v_mov_b32_e32 v96, v2
	v_mov_b32_e32 v97, v2
	v_mov_b32_e32 v98, v2
	v_mov_b32_e32 v99, v2
	v_mov_b32_e32 v100, v2
	v_mov_b32_e32 v101, v2
	v_mov_b32_e32 v102, v2
	v_mov_b32_e32 v103, v2
	v_mov_b32_e32 v104, v2
	v_mov_b32_e32 v105, v2
	v_mov_b32_e32 v106, v2
	v_mov_b32_e32 v107, v2
	v_mov_b32_e32 v108, v2
	v_mov_b32_e32 v109, v2
	v_mov_b32_e32 v110, v2
	v_mov_b32_e32 v111, v2
	v_mov_b32_e32 v112, v2
	v_mov_b32_e32 v113, v2
	v_mov_b32_e32 v114, v2
	v_mov_b32_e32 v115, v2
	v_mov_b32_e32 v116, v2
	v_mov_b32_e32 v117, v2
	v_mov_b32_e32 v118, v2
	v_mov_b32_e32 v119, v2
	v_mov_b32_e32 v120, v2
	v_mov_b32_e32 v121, v2
	v_mov_b32_e32 v122, v2
	v_mov_b32_e32 v123, v2
	v_mov_b32_e32 v124, v2
	v_mov_b32_e32 v125, v2
	v_mov_b32_e32 v126, v2
	v_mov_b32_e32 v127, v2
	v_mov_b32_e32 v128, v2
	v_mov_b32_e32 v129, v2
	s_branch .LBB0_1392

.LBB0_1653:
	s_ashr_i32 s59, s58, 31
	s_lshl_b64 s[64:65], s[58:59], 8
	s_add_u32 s64, s71, s64
	s_addc_u32 s65, s72, s65
	s_and_b64 s[10:11], s[10:11], exec
	s_cselect_b32 s11, s65, s57
	s_cselect_b32 s10, s64, s56
	s_add_i32 s0, 0, 0x10000
	v_add_u32_e32 v157, s0, v155
	ds_read_b128 v[162:165], v157
	ds_read_b128 v[166:169], v157 offset:1024
	ds_read_b128 v[170:173], v157 offset:2048
	ds_read_b128 v[174:177], v157 offset:3072
	v_mov_b32_e32 v157, v131
	v_lshl_add_u64 v[186:187], s[54:55], 0, v[130:131]
	v_lshl_add_u64 v[186:187], v[186:187], 0, s[30:31]
	s_add_i32 m0, s63, 0xc000
	ds_read_b128 v[178:181], v200
	ds_read_b128 v[182:185], v200 offset:1024
	ds_read_b128 v[202:205], v200 offset:2048
	ds_read_b128 v[206:209], v200 offset:3072
	ds_read_b128 v[210:213], v200 offset:4096
	ds_read_b128 v[214:217], v200 offset:5120
	ds_read_b128 v[218:221], v200 offset:6144
	ds_read_b128 v[222:225], v200 offset:7168
	global_load_lds_dwordx4 v[186:187], off
	v_lshl_add_u64 v[186:187], s[54:55], 0, v[156:157]
	v_lshl_add_u64 v[186:187], v[186:187], 0, s[30:31]
	s_add_i32 m0, s63, 0xe000
	s_nop 0
	global_load_lds_dwordx4 v[186:187], off
	s_waitcnt lgkmcnt(8)
	s_barrier
	s_waitcnt lgkmcnt(0)
	s_nop 0
	s_waitcnt lgkmcnt(0)
	v_mfma_f32_16x16x32_bf16 v[110:113], v[162:165], v[178:181], v[110:113]
	v_mfma_f32_16x16x32_bf16 v[106:109], v[170:173], v[178:181], v[106:109]
	v_mfma_f32_16x16x32_bf16 v[102:105], v[162:165], v[202:205], v[102:105]
	v_mfma_f32_16x16x32_bf16 v[98:101], v[170:173], v[202:205], v[98:101]
	v_mfma_f32_16x16x32_bf16 v[94:97], v[162:165], v[210:213], v[94:97]
	v_mfma_f32_16x16x32_bf16 v[90:93], v[170:173], v[210:213], v[90:93]
	v_mfma_f32_16x16x32_bf16 v[86:89], v[162:165], v[218:221], v[86:89]
	v_mfma_f32_16x16x32_bf16 v[82:85], v[170:173], v[218:221], v[82:85]
	v_mfma_f32_16x16x32_bf16 v[110:113], v[166:169], v[182:185], v[110:113]
	v_mfma_f32_16x16x32_bf16 v[106:109], v[174:177], v[182:185], v[106:109]
	v_mfma_f32_16x16x32_bf16 v[102:105], v[166:169], v[206:209], v[102:105]
	v_mfma_f32_16x16x32_bf16 v[98:101], v[174:177], v[206:209], v[98:101]
	v_mfma_f32_16x16x32_bf16 v[94:97], v[166:169], v[214:217], v[94:97]
	v_mfma_f32_16x16x32_bf16 v[90:93], v[174:177], v[214:217], v[90:93]
	v_mfma_f32_16x16x32_bf16 v[86:89], v[166:169], v[222:225], v[86:89]
	v_mfma_f32_16x16x32_bf16 v[82:85], v[174:177], v[222:225], v[82:85]
	s_nop 0
	s_barrier
	s_add_i32 s1, 0, 0x14000
	s_add_i32 s0, s0, s61
	v_add_u32_e32 v157, s1, v155
	v_lshl_add_u64 v[186:187], s[10:11], 0, v[140:141]
	s_mov_b32 m0, s0
	ds_read_b128 v[226:229], v157
	ds_read_b128 v[230:233], v157 offset:1024
	ds_read_b128 v[234:237], v157 offset:2048
	ds_read_b128 v[238:241], v157 offset:3072
	global_load_lds_dwordx4 v[186:187], off
	v_lshl_add_u64 v[242:243], s[10:11], 0, v[142:143]
	s_add_i32 m0, s0, 0x2000
	s_nop 0
	global_load_lds_dwordx4 v[242:243], off
	s_barrier
	s_waitcnt lgkmcnt(0)
	s_nop 0
	s_waitcnt lgkmcnt(0)
	v_mfma_f32_16x16x32_bf16 v[78:81], v[226:229], v[178:181], v[78:81]
	v_mfma_f32_16x16x32_bf16 v[74:77], v[234:237], v[178:181], v[74:77]
	v_mfma_f32_16x16x32_bf16 v[70:73], v[226:229], v[202:205], v[70:73]
	v_mfma_f32_16x16x32_bf16 v[66:69], v[234:237], v[202:205], v[66:69]
	v_mfma_f32_16x16x32_bf16 v[62:65], v[226:229], v[210:213], v[62:65]
	v_mfma_f32_16x16x32_bf16 v[58:61], v[234:237], v[210:213], v[58:61]
	v_mfma_f32_16x16x32_bf16 v[54:57], v[226:229], v[218:221], v[54:57]
	v_mfma_f32_16x16x32_bf16 v[50:53], v[234:237], v[218:221], v[50:53]
	v_mfma_f32_16x16x32_bf16 v[78:81], v[230:233], v[182:185], v[78:81]
	v_mfma_f32_16x16x32_bf16 v[74:77], v[238:241], v[182:185], v[74:77]
	v_mfma_f32_16x16x32_bf16 v[70:73], v[230:233], v[206:209], v[70:73]
	v_mfma_f32_16x16x32_bf16 v[66:69], v[238:241], v[206:209], v[66:69]
	v_mfma_f32_16x16x32_bf16 v[62:65], v[230:233], v[214:217], v[62:65]
	v_mfma_f32_16x16x32_bf16 v[58:61], v[238:241], v[214:217], v[58:61]
	v_mfma_f32_16x16x32_bf16 v[54:57], v[230:233], v[222:225], v[54:57]
	v_mfma_f32_16x16x32_bf16 v[50:53], v[238:241], v[222:225], v[50:53]
	s_nop 0
	s_mov_b32 m0, s63
	s_barrier
	ds_read_b128 v[178:181], v200 offset:16384
	ds_read_b128 v[182:185], v200 offset:17408
	ds_read_b128 v[202:205], v200 offset:18432
	ds_read_b128 v[206:209], v200 offset:19456
	ds_read_b128 v[210:213], v200 offset:20480
	ds_read_b128 v[214:217], v200 offset:21504
	ds_read_b128 v[218:221], v200 offset:22528
	ds_read_b128 v[222:225], v200 offset:23552
	global_load_lds_dwordx4 v160, s[54:55]
	s_mov_b32 m0, s82
	v_mov_b32_e32 v161, v131
	global_load_lds_dwordx4 v158, s[54:55]
	s_barrier
	s_waitcnt lgkmcnt(0)
	v_mov_b32_e32 v159, v131
	v_lshl_add_u64 v[244:245], s[54:55], 0, v[160:161]
	v_lshl_add_u64 v[246:247], s[54:55], 0, v[158:159]
	s_nop 0
	s_waitcnt lgkmcnt(0)
	v_mfma_f32_16x16x32_bf16 v[46:49], v[162:165], v[178:181], v[46:49]
	v_mfma_f32_16x16x32_bf16 v[42:45], v[170:173], v[178:181], v[42:45]
	v_mfma_f32_16x16x32_bf16 v[38:41], v[162:165], v[202:205], v[38:41]
	v_mfma_f32_16x16x32_bf16 v[34:37], v[170:173], v[202:205], v[34:37]
	v_mfma_f32_16x16x32_bf16 v[30:33], v[162:165], v[210:213], v[30:33]
	v_mfma_f32_16x16x32_bf16 v[26:29], v[170:173], v[210:213], v[26:29]
	v_mfma_f32_16x16x32_bf16 v[22:25], v[162:165], v[218:221], v[22:25]
	v_mfma_f32_16x16x32_bf16 v[18:21], v[170:173], v[218:221], v[18:21]
	v_mfma_f32_16x16x32_bf16 v[46:49], v[166:169], v[182:185], v[46:49]
	v_mfma_f32_16x16x32_bf16 v[42:45], v[174:177], v[182:185], v[42:45]
	v_mfma_f32_16x16x32_bf16 v[38:41], v[166:169], v[206:209], v[38:41]
	v_mfma_f32_16x16x32_bf16 v[34:37], v[174:177], v[206:209], v[34:37]
	v_mfma_f32_16x16x32_bf16 v[30:33], v[166:169], v[214:217], v[30:33]
	v_mfma_f32_16x16x32_bf16 v[26:29], v[174:177], v[214:217], v[26:29]
	v_mfma_f32_16x16x32_bf16 v[22:25], v[166:169], v[222:225], v[22:25]
	v_mfma_f32_16x16x32_bf16 v[18:21], v[174:177], v[222:225], v[18:21]
	s_nop 0
	s_barrier
	s_add_u32 s66, s10, 0x8000
	s_addc_u32 s67, s11, 0
	s_add_i32 s0, s1, s61
	v_lshl_add_u64 v[162:163], s[66:67], 0, v[140:141]
	s_mov_b32 m0, s0
	s_nop 0
	global_load_lds_dwordx4 v[162:163], off
	v_lshl_add_u64 v[162:163], s[66:67], 0, v[142:143]
	s_add_i32 m0, s0, 0x2000
	s_nop 0
	global_load_lds_dwordx4 v[162:163], off
	s_waitcnt vmcnt(6)
	s_barrier
	s_nop 0
	v_mfma_f32_16x16x32_bf16 v[14:17], v[226:229], v[178:181], v[14:17]
	v_mfma_f32_16x16x32_bf16 v[10:13], v[234:237], v[178:181], v[10:13]
	v_mfma_f32_16x16x32_bf16 v[6:9], v[226:229], v[202:205], v[6:9]
	v_mfma_f32_16x16x32_bf16 v[2:5], v[234:237], v[202:205], v[2:5]
	v_mfma_f32_16x16x32_bf16 v[114:117], v[226:229], v[210:213], v[114:117]
	v_mfma_f32_16x16x32_bf16 v[118:121], v[234:237], v[210:213], v[118:121]
	v_mfma_f32_16x16x32_bf16 v[122:125], v[226:229], v[218:221], v[122:125]
	v_mfma_f32_16x16x32_bf16 v[126:129], v[234:237], v[218:221], v[126:129]
	v_mfma_f32_16x16x32_bf16 v[14:17], v[230:233], v[182:185], v[14:17]
	v_mfma_f32_16x16x32_bf16 v[10:13], v[238:241], v[182:185], v[10:13]
	v_mfma_f32_16x16x32_bf16 v[6:9], v[230:233], v[206:209], v[6:9]
	v_mfma_f32_16x16x32_bf16 v[2:5], v[238:241], v[206:209], v[2:5]
	v_mfma_f32_16x16x32_bf16 v[114:117], v[230:233], v[214:217], v[114:117]
	v_mfma_f32_16x16x32_bf16 v[118:121], v[238:241], v[214:217], v[118:121]
	v_mfma_f32_16x16x32_bf16 v[122:125], v[230:233], v[222:225], v[122:125]
	v_mfma_f32_16x16x32_bf16 v[126:129], v[238:241], v[222:225], v[126:129]
	s_nop 0
	s_add_i32 s0, 0, 0x18000
	v_add_u32_e32 v157, s0, v155
	s_barrier
	ds_read_b128 v[162:165], v157
	ds_read_b128 v[166:169], v157 offset:1024
	ds_read_b128 v[170:173], v157 offset:2048
	ds_read_b128 v[174:177], v157 offset:3072
	s_mov_b32 m0, s83
	ds_read_b128 v[178:181], v200 offset:32768
	ds_read_b128 v[182:185], v200 offset:33792
	ds_read_b128 v[202:205], v200 offset:34816
	ds_read_b128 v[206:209], v200 offset:35840
	ds_read_b128 v[210:213], v200 offset:36864
	ds_read_b128 v[214:217], v200 offset:37888
	ds_read_b128 v[218:221], v200 offset:38912
	ds_read_b128 v[222:225], v200 offset:39936
	global_load_lds_dwordx4 v189, s[54:55]
	s_mov_b32 m0, s84
	s_nop 0
	global_load_lds_dwordx4 v201, s[54:55]
	s_waitcnt lgkmcnt(8)
	s_barrier
	s_waitcnt lgkmcnt(0)
	s_nop 0
	s_waitcnt lgkmcnt(0)
	v_mfma_f32_16x16x32_bf16 v[110:113], v[162:165], v[178:181], v[110:113]
	v_mfma_f32_16x16x32_bf16 v[106:109], v[170:173], v[178:181], v[106:109]
	v_mfma_f32_16x16x32_bf16 v[102:105], v[162:165], v[202:205], v[102:105]
	v_mfma_f32_16x16x32_bf16 v[98:101], v[170:173], v[202:205], v[98:101]
	v_mfma_f32_16x16x32_bf16 v[94:97], v[162:165], v[210:213], v[94:97]
	v_mfma_f32_16x16x32_bf16 v[90:93], v[170:173], v[210:213], v[90:93]
	v_mfma_f32_16x16x32_bf16 v[86:89], v[162:165], v[218:221], v[86:89]
	v_mfma_f32_16x16x32_bf16 v[82:85], v[170:173], v[218:221], v[82:85]
	v_mfma_f32_16x16x32_bf16 v[110:113], v[166:169], v[182:185], v[110:113]
	v_mfma_f32_16x16x32_bf16 v[106:109], v[174:177], v[182:185], v[106:109]
	v_mfma_f32_16x16x32_bf16 v[102:105], v[166:169], v[206:209], v[102:105]
	v_mfma_f32_16x16x32_bf16 v[98:101], v[174:177], v[206:209], v[98:101]
	v_mfma_f32_16x16x32_bf16 v[94:97], v[166:169], v[214:217], v[94:97]
	v_mfma_f32_16x16x32_bf16 v[90:93], v[174:177], v[214:217], v[90:93]
	v_mfma_f32_16x16x32_bf16 v[86:89], v[166:169], v[222:225], v[86:89]
	v_mfma_f32_16x16x32_bf16 v[82:85], v[174:177], v[222:225], v[82:85]
	s_nop 0
	s_barrier
	s_add_i32 s1, 0, 0x1c000
	s_add_i32 s0, s0, s61
	v_add_u32_e32 v157, s1, v155
	v_lshl_add_u64 v[186:187], v[186:187], 0, s[30:31]
	s_mov_b32 m0, s0
	ds_read_b128 v[226:229], v157
	ds_read_b128 v[230:233], v157 offset:1024
	ds_read_b128 v[234:237], v157 offset:2048
	ds_read_b128 v[238:241], v157 offset:3072
	global_load_lds_dwordx4 v[186:187], off
	v_lshl_add_u64 v[186:187], v[242:243], 0, s[30:31]
	s_add_i32 m0, s0, 0x2000
	s_nop 0
	global_load_lds_dwordx4 v[186:187], off
	s_barrier
	s_waitcnt lgkmcnt(0)
	s_nop 0
	s_waitcnt lgkmcnt(0)
	v_mfma_f32_16x16x32_bf16 v[78:81], v[226:229], v[178:181], v[78:81]
	v_mfma_f32_16x16x32_bf16 v[74:77], v[234:237], v[178:181], v[74:77]
	v_mfma_f32_16x16x32_bf16 v[70:73], v[226:229], v[202:205], v[70:73]
	v_mfma_f32_16x16x32_bf16 v[66:69], v[234:237], v[202:205], v[66:69]
	v_mfma_f32_16x16x32_bf16 v[62:65], v[226:229], v[210:213], v[62:65]
	v_mfma_f32_16x16x32_bf16 v[58:61], v[234:237], v[210:213], v[58:61]
	v_mfma_f32_16x16x32_bf16 v[54:57], v[226:229], v[218:221], v[54:57]
	v_mfma_f32_16x16x32_bf16 v[50:53], v[234:237], v[218:221], v[50:53]
	v_mfma_f32_16x16x32_bf16 v[78:81], v[230:233], v[182:185], v[78:81]
	v_mfma_f32_16x16x32_bf16 v[74:77], v[238:241], v[182:185], v[74:77]
	v_mfma_f32_16x16x32_bf16 v[70:73], v[230:233], v[206:209], v[70:73]
	v_mfma_f32_16x16x32_bf16 v[66:69], v[238:241], v[206:209], v[66:69]
	v_mfma_f32_16x16x32_bf16 v[62:65], v[230:233], v[214:217], v[62:65]
	v_mfma_f32_16x16x32_bf16 v[58:61], v[238:241], v[214:217], v[58:61]
	v_mfma_f32_16x16x32_bf16 v[54:57], v[230:233], v[222:225], v[54:57]
	v_mfma_f32_16x16x32_bf16 v[50:53], v[238:241], v[222:225], v[50:53]
	s_nop 0
	s_mov_b32 m0, s85
	v_lshl_add_u64 v[186:187], v[244:245], 0, s[30:31]
	s_barrier
	ds_read_b128 v[178:181], v200 offset:49152
	ds_read_b128 v[182:185], v200 offset:50176
	ds_read_b128 v[202:205], v200 offset:51200
	ds_read_b128 v[206:209], v200 offset:52224
	ds_read_b128 v[210:213], v200 offset:53248
	ds_read_b128 v[214:217], v200 offset:54272
	ds_read_b128 v[218:221], v200 offset:55296
	ds_read_b128 v[222:225], v200 offset:56320
	global_load_lds_dwordx4 v[186:187], off
	v_lshl_add_u64 v[186:187], v[246:247], 0, s[30:31]
	s_mov_b32 m0, s86
	s_nop 0
	global_load_lds_dwordx4 v[186:187], off
	s_barrier
	s_waitcnt lgkmcnt(0)
	s_nop 0
	s_waitcnt lgkmcnt(0)
	v_mfma_f32_16x16x32_bf16 v[46:49], v[162:165], v[178:181], v[46:49]
	v_mfma_f32_16x16x32_bf16 v[42:45], v[170:173], v[178:181], v[42:45]
	v_mfma_f32_16x16x32_bf16 v[38:41], v[162:165], v[202:205], v[38:41]
	v_mfma_f32_16x16x32_bf16 v[34:37], v[170:173], v[202:205], v[34:37]
	v_mfma_f32_16x16x32_bf16 v[30:33], v[162:165], v[210:213], v[30:33]
	v_mfma_f32_16x16x32_bf16 v[26:29], v[170:173], v[210:213], v[26:29]
	v_mfma_f32_16x16x32_bf16 v[22:25], v[162:165], v[218:221], v[22:25]
	v_mfma_f32_16x16x32_bf16 v[18:21], v[170:173], v[218:221], v[18:21]
	v_mfma_f32_16x16x32_bf16 v[46:49], v[166:169], v[182:185], v[46:49]
	v_mfma_f32_16x16x32_bf16 v[42:45], v[174:177], v[182:185], v[42:45]
	v_mfma_f32_16x16x32_bf16 v[38:41], v[166:169], v[206:209], v[38:41]
	v_mfma_f32_16x16x32_bf16 v[34:37], v[174:177], v[206:209], v[34:37]
	v_mfma_f32_16x16x32_bf16 v[30:33], v[166:169], v[214:217], v[30:33]
	v_mfma_f32_16x16x32_bf16 v[26:29], v[174:177], v[214:217], v[26:29]
	v_mfma_f32_16x16x32_bf16 v[22:25], v[166:169], v[222:225], v[22:25]
	v_mfma_f32_16x16x32_bf16 v[18:21], v[174:177], v[222:225], v[18:21]
	s_nop 0
	s_barrier
	s_add_u32 s10, s10, 0x8080
	s_addc_u32 s11, s11, 0
	s_add_i32 s0, s1, s61
	v_lshl_add_u64 v[162:163], s[10:11], 0, v[140:141]
	s_mov_b32 m0, s0
	s_nop 0
	global_load_lds_dwordx4 v[162:163], off
	v_lshl_add_u64 v[162:163], s[10:11], 0, v[142:143]
	s_add_i32 m0, s0, 0x2000
	s_nop 0
	global_load_lds_dwordx4 v[162:163], off
	s_waitcnt vmcnt(6)
	s_barrier
	s_nop 0
	v_mfma_f32_16x16x32_bf16 v[14:17], v[226:229], v[178:181], v[14:17]
	v_mfma_f32_16x16x32_bf16 v[10:13], v[234:237], v[178:181], v[10:13]
	v_mfma_f32_16x16x32_bf16 v[6:9], v[226:229], v[202:205], v[6:9]
	v_mfma_f32_16x16x32_bf16 v[2:5], v[234:237], v[202:205], v[2:5]
	v_mfma_f32_16x16x32_bf16 v[114:117], v[226:229], v[210:213], v[114:117]
	v_mfma_f32_16x16x32_bf16 v[118:121], v[234:237], v[210:213], v[118:121]
	v_mfma_f32_16x16x32_bf16 v[122:125], v[226:229], v[218:221], v[122:125]
	v_mfma_f32_16x16x32_bf16 v[126:129], v[234:237], v[218:221], v[126:129]
	v_mfma_f32_16x16x32_bf16 v[14:17], v[230:233], v[182:185], v[14:17]
	v_mfma_f32_16x16x32_bf16 v[10:13], v[238:241], v[182:185], v[10:13]
	v_mfma_f32_16x16x32_bf16 v[6:9], v[230:233], v[206:209], v[6:9]
	v_mfma_f32_16x16x32_bf16 v[2:5], v[238:241], v[206:209], v[2:5]
	v_mfma_f32_16x16x32_bf16 v[114:117], v[230:233], v[214:217], v[114:117]
	v_mfma_f32_16x16x32_bf16 v[118:121], v[238:241], v[214:217], v[118:121]
	v_mfma_f32_16x16x32_bf16 v[122:125], v[230:233], v[222:225], v[122:125]
	v_mfma_f32_16x16x32_bf16 v[126:129], v[238:241], v[222:225], v[126:129]
	s_nop 0
	s_lshl_b32 s0, s88, 2
	s_lshr_b32 s1, 0x6540, s0
	s_and_b32 s1, s1, 7
	s_mul_i32 s1, s1, 0x8200000
	s_add_u32 s66, s3, s1
	s_addc_u32 s67, s35, 0
	s_lshr_b32 s0, 0x4433, s0
	s_and_b32 s10, s0, 7
	v_add_u32_e32 v164, s89, v199
	s_cmp_eq_u32 s10, 0
	v_add_u32_e32 v162, s90, v153
	v_ashrrev_i32_e32 v165, 31, v164
	s_barrier
	s_cbranch_scc1 .LBB0_1662
	s_cmp_gt_u32 s10, 2
	s_cselect_b64 s[68:69], -1, 0
	s_cmp_gt_i32 s88, 1
	s_cselect_b32 vcc_hi, s17, 0
	s_cselect_b32 vcc_lo, s16, 0
	s_lshl_b64 vcc, vcc, 2
	s_add_u32 s0, s14, vcc_lo
	s_addc_u32 s1, s15, vcc_hi
	s_bitcmp1_b32 s88, 0
	s_cselect_b32 s11, 0x2000, 0
	s_add_u32 vcc_lo, s0, s11
	s_addc_u32 vcc_hi, s1, 0
	v_lshl_add_u64 v[170:171], v[164:165], 2, vcc
	v_bfrev_b32_e32 v166, 1
	s_and_b64 vcc, exec, s[68:69]
	v_bfrev_b32_e32 v178, 1
	v_bfrev_b32_e32 v179, 1
	v_bfrev_b32_e32 v174, 1
	v_bfrev_b32_e32 v175, 1
	v_bfrev_b32_e32 v180, 1
	v_bfrev_b32_e32 v181, 1
	v_bfrev_b32_e32 v176, 1
	v_bfrev_b32_e32 v177, 1
	s_cbranch_vccz .LBB0_1656
	global_load_dwordx4 v[172:175], v[170:171], off
	global_load_dwordx4 v[182:185], v[170:171], off offset:16
	s_waitcnt vmcnt(0)
	v_pk_mul_f32 v[176:177], v[174:175], s[34:35] op_sel_hi:[1,0]
	v_pk_mul_f32 v[180:181], v[172:173], s[34:35] op_sel_hi:[1,0]
	v_pk_mul_f32 v[174:175], v[184:185], s[34:35] op_sel_hi:[1,0]
	v_pk_mul_f32 v[178:179], v[182:183], s[34:35] op_sel_hi:[1,0]

.LBB0_1721:
	s_and_b32 s56, s83, 31
	s_bfe_u32 s73, s83, 0x10005
	s_lshl_b32 s72, s56, 6
	s_cmp_lt_u32 s83, 64
	s_cselect_b64 s[28:29], -1, 0
	s_and_b64 s[66:67], s[28:29], exec
	s_mov_b32 s0, 0x8c00000
	s_cselect_b32 s0, s0, 0x29400000
	s_add_u32 s66, s54, s0
	s_addc_u32 s67, s55, 0
	s_andn2_b64 vcc, exec, s[50:51]
	s_mov_b64 s[68:69], -1
	s_cbranch_vccnz .LBB0_1737
	s_setprio 3
	s_and_saveexec_b64 s[68:69], s[4:5]
	v_mov_b32_e32 v2, s61
	ds_write_b32 v2, v161
	s_or_b64 exec, exec, s[68:69]
	s_lshl_b32 s0, s72, 1
	s_add_u32 s0, s66, s0
	s_addc_u32 s1, s67, 0
	s_add_u32 s0, s0, s81
	s_addc_u32 s1, s1, 0
	v_lshlrev_b32_e32 v160, 1, v158
	v_mov_b32_e32 v2, 0
	v_lshl_add_u64 v[164:165], s[0:1], 0, v[160:161]
	s_lshl_b32 s70, s73, 14
	s_mov_b32 s71, 0
	v_mov_b32_e32 v3, v2
	v_mov_b32_e32 v4, v2
	v_mov_b32_e32 v5, v2
	v_mov_b32_e32 v10, v2
	v_mov_b32_e32 v11, v2
	v_mov_b32_e32 v12, v2
	v_mov_b32_e32 v13, v2
	v_mov_b32_e32 v6, v2
	v_mov_b32_e32 v7, v2
	v_mov_b32_e32 v8, v2
	v_mov_b32_e32 v9, v2
	v_mov_b32_e32 v14, v2
	v_mov_b32_e32 v15, v2
	v_mov_b32_e32 v16, v2
	v_mov_b32_e32 v17, v2
	v_and_b32_e32 v25, 1, v0
	v_cmp_ne_u32_e64 s[98:99], 0, v25
	v_add_u32_e32 v24, v184, v25
	v_add_u32_e32 v22, 0xffffff00, v24
	v_sub_u32_e32 v23, 0x40ff, v24
	v_cndmask_b32_e64 v22, v23, v22, s[28:29]
	v_add_u32_e32 v22, s70, v22
	v_ashrrev_i32_e32 v23, 31, v22
	v_lshlrev_b64 v[22:23], 12, v[22:23]
	v_lshl_add_u64 v[22:23], v[164:165], 0, v[22:23]
	v_sub_u32_e32 v27, 0, v25
	v_lshlrev_b32_e32 v26, 1, v27
	v_lshl_add_u64 v[210:211], v[22:23], 0, v[26:27]
	v_mov_b32_e32 v28, 0x2000
	v_mov_b32_e32 v29, 0xffffe000
	v_cndmask_b32_e64 v28, v29, v28, s[28:29]
	v_ashrrev_i32_e32 v29, 31, v28
	v_lshl_add_u64 v[212:213], v[210:211], 0, v[28:29]
	s_mov_b32 s100, 0x10000
	s_mov_b32 s101, 0
	s_cmp_lt_u32 s83, 64
	s_cbranch_scc1 .Lx14_dir0
	s_mov_b32 s100, 0xffff0000
	s_mov_b32 s101, -1

.LBB0_1784:
	s_add_i32 s30, s46, 0x100
	s_and_b64 s[0:1], s[38:39], exec
	s_cselect_b32 s1, 0, s30
	s_cselect_b32 s0, 0, 0
	s_add_u32 s48, s8, s1
	s_addc_u32 s49, s9, s0
	s_add_u32 s0, s26, s46
	s_addc_u32 s1, s27, 0
	s_add_u32 s30, s0, 0x100
	s_addc_u32 s31, s1, 0
	s_and_b64 s[0:1], s[38:39], exec
	s_cselect_b32 s57, s29, s31
	s_cselect_b32 s56, s84, s30
	s_add_u32 s58, s8, s46
	s_addc_u32 s59, s9, 0
	s_add_i32 s94, s73, s64
	s_add_i32 m0, s65, 0xc000
	s_add_i32 s0, s65, 0xe000
	s_add_i32 s93, s94, 0x2000
	ds_read_b128 v[162:165], v153
	ds_read_b128 v[166:169], v153 offset:1024
	ds_read_b128 v[170:173], v153 offset:2048
	ds_read_b128 v[174:177], v153 offset:3072
	s_add_u32 s50, s56, 0x10000
	s_addc_u32 s51, s57, 0
	s_add_i32 s90, 0, 0x18000
	s_add_i32 s92, s74, s64
	s_add_i32 s89, s90, s64
	s_add_i32 s91, s92, 0x2000
	s_add_i32 s88, 0, 0x1c000
	s_add_i32 s87, s89, 0x2000
	s_add_u32 s46, s56, 0x10080
	s_addc_u32 s47, s57, 0
	s_add_i32 s86, s88, s64
	s_add_i32 s85, s86, 0x2000
	v_cndmask_b32_e64 v136, v160, v156, s[38:39]
	v_cndmask_b32_e64 v161, v144, v157, s[38:39]
	v_cndmask_b32_e64 v186, v142, v158, s[38:39]
	v_cndmask_b32_e64 v189, v146, v159, s[38:39]
	v_lshl_add_u64 v[214:215], s[58:59], 0, v[144:145]
	v_lshl_add_u64 v[214:215], v[214:215], 0, s[12:13]
	ds_read_b128 v[178:181], v154
	ds_read_b128 v[182:185], v154 offset:1024
	ds_read_b128 v[190:193], v154 offset:2048
	ds_read_b128 v[194:197], v154 offset:3072
	ds_read_b128 v[198:201], v154 offset:4096
	ds_read_b128 v[202:205], v154 offset:5120
	ds_read_b128 v[206:209], v154 offset:6144
	ds_read_b128 v[210:213], v154 offset:7168
	global_load_lds_dwordx4 v[214:215], off
	v_lshl_add_u64 v[214:215], s[58:59], 0, v[146:147]
	v_lshl_add_u64 v[214:215], v[214:215], 0, s[12:13]
	s_mov_b32 m0, s0
	s_nop 0
	global_load_lds_dwordx4 v[214:215], off
	s_waitcnt lgkmcnt(8)
	s_barrier
	s_waitcnt lgkmcnt(0)
	s_nop 0
	s_waitcnt lgkmcnt(0)
	v_mfma_f32_16x16x32_bf16 v[126:129], v[162:165], v[178:181], v[126:129]
	v_mfma_f32_16x16x32_bf16 v[122:125], v[170:173], v[178:181], v[122:125]
	v_mfma_f32_16x16x32_bf16 v[118:121], v[162:165], v[190:193], v[118:121]
	v_mfma_f32_16x16x32_bf16 v[114:117], v[170:173], v[190:193], v[114:117]
	v_mfma_f32_16x16x32_bf16 v[110:113], v[162:165], v[198:201], v[110:113]
	v_mfma_f32_16x16x32_bf16 v[106:109], v[170:173], v[198:201], v[106:109]
	v_mfma_f32_16x16x32_bf16 v[102:105], v[162:165], v[206:209], v[102:105]
	v_mfma_f32_16x16x32_bf16 v[98:101], v[170:173], v[206:209], v[98:101]
	v_mfma_f32_16x16x32_bf16 v[126:129], v[166:169], v[182:185], v[126:129]
	v_mfma_f32_16x16x32_bf16 v[122:125], v[174:177], v[182:185], v[122:125]
	v_mfma_f32_16x16x32_bf16 v[118:121], v[166:169], v[194:197], v[118:121]
	v_mfma_f32_16x16x32_bf16 v[114:117], v[174:177], v[194:197], v[114:117]
	v_mfma_f32_16x16x32_bf16 v[110:113], v[166:169], v[202:205], v[110:113]
	v_mfma_f32_16x16x32_bf16 v[106:109], v[174:177], v[202:205], v[106:109]
	v_mfma_f32_16x16x32_bf16 v[102:105], v[166:169], v[210:213], v[102:105]
	v_mfma_f32_16x16x32_bf16 v[98:101], v[174:177], v[210:213], v[98:101]
	s_nop 0
	s_barrier
	s_mov_b32 m0, s94
	v_lshl_add_u64 v[230:231], s[56:57], 0, v[134:135]
	ds_read_b128 v[214:217], v155
	ds_read_b128 v[218:221], v155 offset:1024
	ds_read_b128 v[222:225], v155 offset:2048
	ds_read_b128 v[226:229], v155 offset:3072
	global_load_lds_dwordx4 v[230:231], off
	v_lshl_add_u64 v[232:233], s[56:57], 0, v[132:133]
	s_mov_b32 m0, s93
	s_nop 0
	global_load_lds_dwordx4 v[232:233], off
	s_barrier
	s_waitcnt lgkmcnt(0)
	s_nop 0
	s_waitcnt lgkmcnt(0)
	v_mfma_f32_16x16x32_bf16 v[86:89], v[214:217], v[178:181], v[86:89]
	v_mfma_f32_16x16x32_bf16 v[78:81], v[222:225], v[178:181], v[78:81]
	v_mfma_f32_16x16x32_bf16 v[70:73], v[214:217], v[190:193], v[70:73]
	v_mfma_f32_16x16x32_bf16 v[62:65], v[222:225], v[190:193], v[62:65]
	v_mfma_f32_16x16x32_bf16 v[38:41], v[214:217], v[198:201], v[38:41]
	v_mfma_f32_16x16x32_bf16 v[34:37], v[222:225], v[198:201], v[34:37]
	v_mfma_f32_16x16x32_bf16 v[26:29], v[214:217], v[206:209], v[26:29]
	v_mfma_f32_16x16x32_bf16 v[18:21], v[222:225], v[206:209], v[18:21]
	v_mfma_f32_16x16x32_bf16 v[86:89], v[218:221], v[182:185], v[86:89]
	v_mfma_f32_16x16x32_bf16 v[78:81], v[226:229], v[182:185], v[78:81]
	v_mfma_f32_16x16x32_bf16 v[70:73], v[218:221], v[194:197], v[70:73]
	v_mfma_f32_16x16x32_bf16 v[62:65], v[226:229], v[194:197], v[62:65]
	v_mfma_f32_16x16x32_bf16 v[38:41], v[218:221], v[202:205], v[38:41]
	v_mfma_f32_16x16x32_bf16 v[34:37], v[226:229], v[202:205], v[34:37]
	v_mfma_f32_16x16x32_bf16 v[26:29], v[218:221], v[210:213], v[26:29]
	v_mfma_f32_16x16x32_bf16 v[18:21], v[226:229], v[210:213], v[18:21]
	s_nop 0
	s_mov_b32 m0, s65
	s_barrier
	ds_read_b128 v[178:181], v154 offset:16384
	ds_read_b128 v[182:185], v154 offset:17408
	ds_read_b128 v[190:193], v154 offset:18432
	ds_read_b128 v[194:197], v154 offset:19456
	ds_read_b128 v[198:201], v154 offset:20480
	ds_read_b128 v[202:205], v154 offset:21504
	ds_read_b128 v[206:209], v154 offset:22528
	ds_read_b128 v[210:213], v154 offset:23552
	global_load_lds_dwordx4 v136, s[48:49]
	s_mov_b32 m0, s66
	v_mov_b32_e32 v187, v137
	global_load_lds_dwordx4 v186, s[48:49]
	s_barrier
	s_waitcnt lgkmcnt(0)
	v_lshl_add_u64 v[234:235], s[48:49], 0, v[136:137]
	v_lshl_add_u64 v[186:187], s[48:49], 0, v[186:187]
	s_nop 0
	s_waitcnt lgkmcnt(0)
	v_mfma_f32_16x16x32_bf16 v[94:97], v[162:165], v[178:181], v[94:97]
	v_mfma_f32_16x16x32_bf16 v[90:93], v[170:173], v[178:181], v[90:93]
	v_mfma_f32_16x16x32_bf16 v[82:85], v[162:165], v[190:193], v[82:85]
	v_mfma_f32_16x16x32_bf16 v[74:77], v[170:173], v[190:193], v[74:77]
	v_mfma_f32_16x16x32_bf16 v[46:49], v[162:165], v[198:201], v[46:49]
	v_mfma_f32_16x16x32_bf16 v[42:45], v[170:173], v[198:201], v[42:45]
	v_mfma_f32_16x16x32_bf16 v[30:33], v[162:165], v[206:209], v[30:33]
	v_mfma_f32_16x16x32_bf16 v[22:25], v[170:173], v[206:209], v[22:25]
	v_mfma_f32_16x16x32_bf16 v[94:97], v[166:169], v[182:185], v[94:97]
	v_mfma_f32_16x16x32_bf16 v[90:93], v[174:177], v[182:185], v[90:93]
	v_mfma_f32_16x16x32_bf16 v[82:85], v[166:169], v[194:197], v[82:85]
	v_mfma_f32_16x16x32_bf16 v[74:77], v[174:177], v[194:197], v[74:77]
	v_mfma_f32_16x16x32_bf16 v[46:49], v[166:169], v[202:205], v[46:49]
	v_mfma_f32_16x16x32_bf16 v[42:45], v[174:177], v[202:205], v[42:45]
	v_mfma_f32_16x16x32_bf16 v[30:33], v[166:169], v[210:213], v[30:33]
	v_mfma_f32_16x16x32_bf16 v[22:25], v[174:177], v[210:213], v[22:25]
	s_nop 0
	s_barrier
	s_mov_b32 m0, s92
	v_lshl_add_u64 v[162:163], s[50:51], 0, v[134:135]
	global_load_lds_dwordx4 v[162:163], off
	v_lshl_add_u64 v[162:163], s[50:51], 0, v[132:133]
	s_mov_b32 m0, s91
	s_nop 0
	global_load_lds_dwordx4 v[162:163], off
	s_waitcnt vmcnt(6)
	s_barrier
	s_nop 0
	v_mfma_f32_16x16x32_bf16 v[14:17], v[214:217], v[178:181], v[14:17]
	v_mfma_f32_16x16x32_bf16 v[10:13], v[222:225], v[178:181], v[10:13]
	v_mfma_f32_16x16x32_bf16 v[6:9], v[214:217], v[190:193], v[6:9]
	v_mfma_f32_16x16x32_bf16 v[2:5], v[222:225], v[190:193], v[2:5]
	v_mfma_f32_16x16x32_bf16 v[54:57], v[214:217], v[198:201], v[54:57]
	v_mfma_f32_16x16x32_bf16 v[66:69], v[222:225], v[198:201], v[66:69]
	v_mfma_f32_16x16x32_bf16 v[50:53], v[214:217], v[206:209], v[50:53]
	v_mfma_f32_16x16x32_bf16 v[58:61], v[222:225], v[206:209], v[58:61]
	v_mfma_f32_16x16x32_bf16 v[14:17], v[218:221], v[182:185], v[14:17]
	v_mfma_f32_16x16x32_bf16 v[10:13], v[226:229], v[182:185], v[10:13]
	v_mfma_f32_16x16x32_bf16 v[6:9], v[218:221], v[194:197], v[6:9]
	v_mfma_f32_16x16x32_bf16 v[2:5], v[226:229], v[194:197], v[2:5]
	v_mfma_f32_16x16x32_bf16 v[54:57], v[218:221], v[202:205], v[54:57]
	v_mfma_f32_16x16x32_bf16 v[66:69], v[226:229], v[202:205], v[66:69]
	v_mfma_f32_16x16x32_bf16 v[50:53], v[218:221], v[210:213], v[50:53]
	v_mfma_f32_16x16x32_bf16 v[58:61], v[226:229], v[210:213], v[58:61]
	s_nop 0
	v_add_u32_e32 v136, s90, v151
	s_barrier
	ds_read_b128 v[162:165], v136
	ds_read_b128 v[166:169], v136 offset:1024
	ds_read_b128 v[170:173], v136 offset:2048
	ds_read_b128 v[174:177], v136 offset:3072
	s_mov_b32 m0, s67
	ds_read_b128 v[178:181], v154 offset:32768
	ds_read_b128 v[182:185], v154 offset:33792
	ds_read_b128 v[190:193], v154 offset:34816
	ds_read_b128 v[194:197], v154 offset:35840
	ds_read_b128 v[198:201], v154 offset:36864
	ds_read_b128 v[202:205], v154 offset:37888
	ds_read_b128 v[206:209], v154 offset:38912
	ds_read_b128 v[210:213], v154 offset:39936
	global_load_lds_dwordx4 v161, s[48:49]
	s_mov_b32 m0, s68
	s_nop 0
	global_load_lds_dwordx4 v189, s[48:49]
	s_waitcnt lgkmcnt(8)
	s_barrier
	s_waitcnt lgkmcnt(0)
	s_nop 0
	s_waitcnt lgkmcnt(0)
	v_mfma_f32_16x16x32_bf16 v[126:129], v[162:165], v[178:181], v[126:129]
	v_mfma_f32_16x16x32_bf16 v[122:125], v[170:173], v[178:181], v[122:125]
	v_mfma_f32_16x16x32_bf16 v[118:121], v[162:165], v[190:193], v[118:121]
	v_mfma_f32_16x16x32_bf16 v[114:117], v[170:173], v[190:193], v[114:117]
	v_mfma_f32_16x16x32_bf16 v[110:113], v[162:165], v[198:201], v[110:113]
	v_mfma_f32_16x16x32_bf16 v[106:109], v[170:173], v[198:201], v[106:109]
	v_mfma_f32_16x16x32_bf16 v[102:105], v[162:165], v[206:209], v[102:105]
	v_mfma_f32_16x16x32_bf16 v[98:101], v[170:173], v[206:209], v[98:101]
	v_mfma_f32_16x16x32_bf16 v[126:129], v[166:169], v[182:185], v[126:129]
	v_mfma_f32_16x16x32_bf16 v[122:125], v[174:177], v[182:185], v[122:125]
	v_mfma_f32_16x16x32_bf16 v[118:121], v[166:169], v[194:197], v[118:121]
	v_mfma_f32_16x16x32_bf16 v[114:117], v[174:177], v[194:197], v[114:117]
	v_mfma_f32_16x16x32_bf16 v[110:113], v[166:169], v[202:205], v[110:113]
	v_mfma_f32_16x16x32_bf16 v[106:109], v[174:177], v[202:205], v[106:109]
	v_mfma_f32_16x16x32_bf16 v[102:105], v[166:169], v[210:213], v[102:105]
	v_mfma_f32_16x16x32_bf16 v[98:101], v[174:177], v[210:213], v[98:101]
	s_nop 0
	s_barrier
	s_mov_b32 m0, s89
	v_add_u32_e32 v136, s88, v151
	v_lshl_add_u64 v[230:231], v[230:231], 0, s[12:13]
	ds_read_b128 v[214:217], v136
	ds_read_b128 v[218:221], v136 offset:1024
	ds_read_b128 v[222:225], v136 offset:2048
	ds_read_b128 v[226:229], v136 offset:3072
	global_load_lds_dwordx4 v[230:231], off
	v_lshl_add_u64 v[230:231], v[232:233], 0, s[12:13]
	s_mov_b32 m0, s87
	s_nop 0
	global_load_lds_dwordx4 v[230:231], off
	s_barrier
	s_waitcnt lgkmcnt(0)
	s_nop 0
	s_waitcnt lgkmcnt(0)
	v_mfma_f32_16x16x32_bf16 v[86:89], v[214:217], v[178:181], v[86:89]
	v_mfma_f32_16x16x32_bf16 v[78:81], v[222:225], v[178:181], v[78:81]
	v_mfma_f32_16x16x32_bf16 v[70:73], v[214:217], v[190:193], v[70:73]
	v_mfma_f32_16x16x32_bf16 v[62:65], v[222:225], v[190:193], v[62:65]
	v_mfma_f32_16x16x32_bf16 v[38:41], v[214:217], v[198:201], v[38:41]
	v_mfma_f32_16x16x32_bf16 v[34:37], v[222:225], v[198:201], v[34:37]
	v_mfma_f32_16x16x32_bf16 v[26:29], v[214:217], v[206:209], v[26:29]
	v_mfma_f32_16x16x32_bf16 v[18:21], v[222:225], v[206:209], v[18:21]
	v_mfma_f32_16x16x32_bf16 v[86:89], v[218:221], v[182:185], v[86:89]
	v_mfma_f32_16x16x32_bf16 v[78:81], v[226:229], v[182:185], v[78:81]
	v_mfma_f32_16x16x32_bf16 v[70:73], v[218:221], v[194:197], v[70:73]
	v_mfma_f32_16x16x32_bf16 v[62:65], v[226:229], v[194:197], v[62:65]
	v_mfma_f32_16x16x32_bf16 v[38:41], v[218:221], v[202:205], v[38:41]
	v_mfma_f32_16x16x32_bf16 v[34:37], v[226:229], v[202:205], v[34:37]
	v_mfma_f32_16x16x32_bf16 v[26:29], v[218:221], v[210:213], v[26:29]
	v_mfma_f32_16x16x32_bf16 v[18:21], v[226:229], v[210:213], v[18:21]
	s_nop 0
	s_mov_b32 m0, s70
	v_lshl_add_u64 v[230:231], v[234:235], 0, s[12:13]
	s_barrier
	ds_read_b128 v[178:181], v154 offset:49152
	ds_read_b128 v[182:185], v154 offset:50176
	ds_read_b128 v[190:193], v154 offset:51200
	ds_read_b128 v[194:197], v154 offset:52224
	ds_read_b128 v[198:201], v154 offset:53248
	ds_read_b128 v[202:205], v154 offset:54272
	ds_read_b128 v[206:209], v154 offset:55296
	ds_read_b128 v[210:213], v154 offset:56320
	global_load_lds_dwordx4 v[230:231], off
	v_lshl_add_u64 v[186:187], v[186:187], 0, s[12:13]
	s_mov_b32 m0, s71
	s_nop 0
	global_load_lds_dwordx4 v[186:187], off
	s_barrier
	s_waitcnt lgkmcnt(0)
	s_nop 0
	s_waitcnt lgkmcnt(0)
	v_mfma_f32_16x16x32_bf16 v[94:97], v[162:165], v[178:181], v[94:97]
	v_mfma_f32_16x16x32_bf16 v[90:93], v[170:173], v[178:181], v[90:93]
	v_mfma_f32_16x16x32_bf16 v[82:85], v[162:165], v[190:193], v[82:85]
	v_mfma_f32_16x16x32_bf16 v[74:77], v[170:173], v[190:193], v[74:77]
	v_mfma_f32_16x16x32_bf16 v[46:49], v[162:165], v[198:201], v[46:49]
	v_mfma_f32_16x16x32_bf16 v[42:45], v[170:173], v[198:201], v[42:45]
	v_mfma_f32_16x16x32_bf16 v[30:33], v[162:165], v[206:209], v[30:33]
	v_mfma_f32_16x16x32_bf16 v[22:25], v[170:173], v[206:209], v[22:25]
	v_mfma_f32_16x16x32_bf16 v[94:97], v[166:169], v[182:185], v[94:97]
	v_mfma_f32_16x16x32_bf16 v[90:93], v[174:177], v[182:185], v[90:93]
	v_mfma_f32_16x16x32_bf16 v[82:85], v[166:169], v[194:197], v[82:85]
	v_mfma_f32_16x16x32_bf16 v[74:77], v[174:177], v[194:197], v[74:77]
	v_mfma_f32_16x16x32_bf16 v[46:49], v[166:169], v[202:205], v[46:49]
	v_mfma_f32_16x16x32_bf16 v[42:45], v[174:177], v[202:205], v[42:45]
	v_mfma_f32_16x16x32_bf16 v[30:33], v[166:169], v[210:213], v[30:33]
	v_mfma_f32_16x16x32_bf16 v[22:25], v[174:177], v[210:213], v[22:25]
	s_nop 0
	s_barrier
	s_mov_b32 m0, s86
	v_lshl_add_u64 v[162:163], s[46:47], 0, v[134:135]
	global_load_lds_dwordx4 v[162:163], off
	v_lshl_add_u64 v[162:163], s[46:47], 0, v[132:133]
	s_mov_b32 m0, s85
	s_nop 0
	global_load_lds_dwordx4 v[162:163], off
	s_waitcnt vmcnt(6)
	s_barrier
	s_nop 0
	v_mfma_f32_16x16x32_bf16 v[14:17], v[214:217], v[178:181], v[14:17]
	v_mfma_f32_16x16x32_bf16 v[10:13], v[222:225], v[178:181], v[10:13]
	v_mfma_f32_16x16x32_bf16 v[6:9], v[214:217], v[190:193], v[6:9]
	v_mfma_f32_16x16x32_bf16 v[2:5], v[222:225], v[190:193], v[2:5]
	v_mfma_f32_16x16x32_bf16 v[54:57], v[214:217], v[198:201], v[54:57]
	v_mfma_f32_16x16x32_bf16 v[66:69], v[222:225], v[198:201], v[66:69]
	v_mfma_f32_16x16x32_bf16 v[50:53], v[214:217], v[206:209], v[50:53]
	v_mfma_f32_16x16x32_bf16 v[58:61], v[222:225], v[206:209], v[58:61]
	v_mfma_f32_16x16x32_bf16 v[14:17], v[218:221], v[182:185], v[14:17]
	v_mfma_f32_16x16x32_bf16 v[10:13], v[226:229], v[182:185], v[10:13]
	v_mfma_f32_16x16x32_bf16 v[6:9], v[218:221], v[194:197], v[6:9]
	v_mfma_f32_16x16x32_bf16 v[2:5], v[226:229], v[194:197], v[2:5]
	v_mfma_f32_16x16x32_bf16 v[54:57], v[218:221], v[202:205], v[54:57]
	v_mfma_f32_16x16x32_bf16 v[66:69], v[226:229], v[202:205], v[66:69]
	v_mfma_f32_16x16x32_bf16 v[50:53], v[218:221], v[210:213], v[50:53]
	v_mfma_f32_16x16x32_bf16 v[58:61], v[226:229], v[210:213], v[58:61]
	s_nop 0
	s_andn2_b64 vcc, exec, s[6:7]
	s_mov_b64 s[38:39], -1
	s_mov_b64 s[6:7], 0
	s_movk_i32 s46, 0x100
	s_barrier
	s_cbranch_vccz .LBB0_1784
	v_add_u32_e32 v144, s81, v143
	v_add_u32_e32 v146, s83, v152
	v_ashrrev_i32_e32 v147, 31, v146
	v_ashrrev_i32_e32 v145, 31, v144
	v_lshl_add_u64 v[146:147], v[146:147], 1, s[10:11]
	v_cvt_pk_bf16_f32 v126, v126, v127
	v_cvt_pk_bf16_f32 v127, v128, v129
	v_cvt_pk_bf16_f32 v128, v122, v123
	v_lshlrev_b64 v[122:123], 12, v[144:145]
	v_lshl_add_u64 v[122:123], v[146:147], 0, v[122:123]
	s_mov_b64 s[0:1], 0x10000
	v_cvt_pk_bf16_f32 v118, v118, v119
	v_cvt_pk_bf16_f32 v119, v120, v121
	v_cvt_pk_bf16_f32 v120, v114, v115
	v_lshl_add_u64 v[114:115], v[122:123], 0, s[0:1]
	s_mov_b32 s0, 0x10000
	v_cvt_pk_bf16_f32 v121, v116, v117
	v_add_co_u32_e32 v116, vcc, s0, v122
	v_cvt_pk_bf16_f32 v110, v110, v111
	s_nop 0
	v_addc_co_u32_e32 v117, vcc, 0, v123, vcc
	v_cvt_pk_bf16_f32 v111, v112, v113
	v_cvt_pk_bf16_f32 v113, v108, v109
	v_add_co_u32_e32 v108, vcc, s75, v122
	v_cvt_pk_bf16_f32 v102, v102, v103
	s_nop 0
	v_addc_co_u32_e32 v109, vcc, 0, v123, vcc
	v_cvt_pk_bf16_f32 v103, v104, v105
	v_cvt_pk_bf16_f32 v105, v100, v101
	v_add_co_u32_e32 v100, vcc, s76, v122
	v_cvt_pk_bf16_f32 v94, v94, v95
	s_nop 0
	v_addc_co_u32_e32 v101, vcc, 0, v123, vcc
	v_cvt_pk_bf16_f32 v95, v96, v97
	v_cvt_pk_bf16_f32 v97, v92, v93
	v_add_co_u32_e32 v92, vcc, s77, v122
	v_cvt_pk_bf16_f32 v82, v82, v83
	s_nop 0
	v_addc_co_u32_e32 v93, vcc, 0, v123, vcc
	v_cvt_pk_bf16_f32 v83, v84, v85
	v_cvt_pk_bf16_f32 v85, v76, v77
	v_add_co_u32_e32 v76, vcc, s78, v122
	v_cvt_pk_bf16_f32 v46, v46, v47
	s_nop 0
	v_addc_co_u32_e32 v77, vcc, 0, v123, vcc
	v_cvt_pk_bf16_f32 v47, v48, v49
	v_cvt_pk_bf16_f32 v49, v44, v45
	v_add_co_u32_e32 v44, vcc, s79, v122
	v_cvt_pk_bf16_f32 v30, v30, v31
	s_nop 0
	v_addc_co_u32_e32 v45, vcc, 0, v123, vcc
	v_cvt_pk_bf16_f32 v31, v32, v33
	v_cvt_pk_bf16_f32 v32, v22, v23
	v_add_co_u32_e32 v22, vcc, s80, v122
	v_cvt_pk_bf16_f32 v33, v24, v25
	s_nop 0
	v_addc_co_u32_e32 v23, vcc, 0, v123, vcc
	global_store_dwordx4 v[22:23], v[30:33], off
	v_cvt_pk_bf16_f32 v22, v86, v87
	v_cvt_pk_bf16_f32 v23, v88, v89
	v_cvt_pk_bf16_f32 v24, v78, v79
	v_cvt_pk_bf16_f32 v25, v80, v81
	global_store_dwordx4 v[122:123], v[22:25], off offset:256
	v_cvt_pk_bf16_f32 v112, v106, v107
	v_lshl_add_u64 v[106:107], v[122:123], 0, s[14:15]
	v_cvt_pk_bf16_f32 v22, v70, v71
	v_cvt_pk_bf16_f32 v23, v72, v73
	v_cvt_pk_bf16_f32 v24, v62, v63
	v_cvt_pk_bf16_f32 v25, v64, v65
	v_cvt_pk_bf16_f32 v48, v42, v43
	v_lshl_add_u64 v[42:43], v[122:123], 0, s[22:23]
	global_store_dwordx4 v[114:115], v[22:25], off offset:256
	v_cvt_pk_bf16_f32 v6, v6, v7
	v_cvt_pk_bf16_f32 v7, v8, v9
	v_cvt_pk_bf16_f32 v22, v38, v39
	v_cvt_pk_bf16_f32 v23, v40, v41
	v_cvt_pk_bf16_f32 v24, v34, v35
	v_cvt_pk_bf16_f32 v25, v36, v37
	v_cvt_pk_bf16_f32 v8, v2, v3
	v_cvt_pk_bf16_f32 v9, v4, v5
	v_cvt_pk_bf16_f32 v2, v54, v55
	v_cvt_pk_bf16_f32 v3, v56, v57
	v_cvt_pk_bf16_f32 v4, v66, v67
	v_cvt_pk_bf16_f32 v5, v68, v69
	v_cvt_pk_bf16_f32 v129, v124, v125
	v_cvt_pk_bf16_f32 v104, v98, v99
	v_lshl_add_u64 v[98:99], v[122:123], 0, s[16:17]
	v_cvt_pk_bf16_f32 v96, v90, v91
	v_lshl_add_u64 v[90:91], v[122:123], 0, s[18:19]
	v_cvt_pk_bf16_f32 v84, v74, v75
	v_lshl_add_u64 v[74:75], v[122:123], 0, s[20:21]
	global_store_dwordx4 v[44:45], v[46:49], off
	v_lshl_add_u64 v[44:45], v[122:123], 0, s[24:25]
	global_store_dwordx4 v[106:107], v[22:25], off offset:256
	v_cvt_pk_bf16_f32 v14, v14, v15
	v_cvt_pk_bf16_f32 v15, v16, v17
	v_cvt_pk_bf16_f32 v22, v26, v27
	v_cvt_pk_bf16_f32 v23, v28, v29
	v_cvt_pk_bf16_f32 v24, v18, v19
	v_cvt_pk_bf16_f32 v25, v20, v21
	v_cvt_pk_bf16_f32 v16, v10, v11
	v_cvt_pk_bf16_f32 v17, v12, v13
	global_store_dwordx4 v[42:43], v[2:5], off offset:256
	s_and_b64 vcc, exec, s[4:5]
	v_mov_b32_e32 v142, v158
	v_cvt_pk_bf16_f32 v2, v50, v51
	v_cvt_pk_bf16_f32 v3, v52, v53
	v_cvt_pk_bf16_f32 v4, v58, v59
	v_cvt_pk_bf16_f32 v5, v60, v61
	v_mov_b32_e32 v160, v156
	v_mov_b32_e32 v146, v159
	v_mov_b32_e32 v144, v157
	s_mov_b32 s83, s28
	s_mov_b32 s81, s82
	s_mov_b64 s[26:27], s[36:37]
	global_store_dwordx4 v[122:123], v[126:129], off
	global_store_dwordx4 v[116:117], v[118:121], off
	global_store_dwordx4 v[108:109], v[110:113], off
	global_store_dwordx4 v[100:101], v[102:105], off
	global_store_dwordx4 v[92:93], v[94:97], off
	global_store_dwordx4 v[76:77], v[82:85], off
	global_store_dwordx4 v[98:99], v[22:25], off offset:256
	global_store_dwordx4 v[90:91], v[14:17], off offset:256
	global_store_dwordx4 v[74:75], v[6:9], off offset:256
	global_store_dwordx4 v[44:45], v[2:5], off offset:256
	s_cbranch_vccz .LBB0_1775
	v_readlane_b32 s74, v255, 6
	v_readlane_b32 s75, v255, 7
	s_load_dwordx2 s[72:73], s[74:75], 0x148
	s_waitcnt vmcnt(0)
	v_readlane_b32 s22, v255, 8
	s_cmpk_gt_u32 s61, 0xff
	v_readlane_b32 s71, v255, 4
	v_readlane_b32 s82, v255, 5
	v_readlane_b32 s23, v255, 9
	s_cbranch_scc1 .LBB0_1788
	s_barrier

.LBB0_1941:
	s_add_u32 s0, s54, s6
	s_addc_u32 s1, s55, s7
	s_add_u32 s40, s0, 0x19000100
	ds_read_b128 v[140:143], v171
	ds_read_b128 v[144:147], v171 offset:1024
	ds_read_b128 v[160:163], v171 offset:2048
	ds_read_b128 v[178:181], v171 offset:3072
	s_addc_u32 s41, s1, 0
	s_add_u32 s69, s66, s6
	s_addc_u32 s70, s67, s7
	s_cmpk_eq_i32 s6, 0xf00
	s_cselect_b64 vcc, -1, 0
	s_and_b64 s[0:1], vcc, exec
	v_cndmask_b32_e32 v154, v131, v174, vcc
	s_cselect_b32 s43, s11, s41
	s_cselect_b32 s42, s10, s40
	v_cndmask_b32_e32 v133, v132, v175, vcc
	v_cndmask_b32_e32 v148, v130, v176, vcc
	v_cndmask_b32_e32 v135, v134, v177, vcc
	s_cselect_b32 s41, s35, s70
	s_cselect_b32 s40, s65, s69
	v_lshl_add_u64 v[164:165], v[138:139], 0, s[6:7]
	s_add_i32 m0, s39, 0xc000
	ds_read_b128 v[182:185], v172
	ds_read_b128 v[190:193], v172 offset:1024
	ds_read_b128 v[194:197], v172 offset:2048
	ds_read_b128 v[198:201], v172 offset:3072
	ds_read_b128 v[202:205], v172 offset:4096
	ds_read_b128 v[206:209], v172 offset:5120
	ds_read_b128 v[210:213], v172 offset:6144
	ds_read_b128 v[214:217], v172 offset:7168
	global_load_lds_dwordx4 v[164:165], off
	v_lshl_add_u64 v[164:165], v[136:137], 0, s[6:7]
	s_add_i32 m0, s39, 0xe000
	s_nop 0
	global_load_lds_dwordx4 v[164:165], off
	s_waitcnt lgkmcnt(8)
	s_barrier
	s_waitcnt lgkmcnt(0)
	s_nop 0
	s_waitcnt lgkmcnt(0)
	v_mfma_f32_16x16x32_bf16 v[126:129], v[140:143], v[182:185], v[126:129]
	v_mfma_f32_16x16x32_bf16 v[122:125], v[160:163], v[182:185], v[122:125]
	v_mfma_f32_16x16x32_bf16 v[114:117], v[140:143], v[194:197], v[114:117]
	v_mfma_f32_16x16x32_bf16 v[106:109], v[160:163], v[194:197], v[106:109]
	v_mfma_f32_16x16x32_bf16 v[98:101], v[140:143], v[202:205], v[98:101]
	v_mfma_f32_16x16x32_bf16 v[90:93], v[160:163], v[202:205], v[90:93]
	v_mfma_f32_16x16x32_bf16 v[82:85], v[140:143], v[210:213], v[82:85]
	v_mfma_f32_16x16x32_bf16 v[74:77], v[160:163], v[210:213], v[74:77]
	v_mfma_f32_16x16x32_bf16 v[126:129], v[144:147], v[190:193], v[126:129]
	v_mfma_f32_16x16x32_bf16 v[122:125], v[178:181], v[190:193], v[122:125]
	v_mfma_f32_16x16x32_bf16 v[114:117], v[144:147], v[198:201], v[114:117]
	v_mfma_f32_16x16x32_bf16 v[106:109], v[178:181], v[198:201], v[106:109]
	v_mfma_f32_16x16x32_bf16 v[98:101], v[144:147], v[206:209], v[98:101]
	v_mfma_f32_16x16x32_bf16 v[90:93], v[178:181], v[206:209], v[90:93]
	v_mfma_f32_16x16x32_bf16 v[82:85], v[144:147], v[214:217], v[82:85]
	v_mfma_f32_16x16x32_bf16 v[74:77], v[178:181], v[214:217], v[74:77]
	s_nop 0
	s_barrier
	s_add_i32 s0, s61, s47
	v_lshl_add_u64 v[164:165], s[40:41], 0, v[150:151]
	s_mov_b32 m0, s0
	ds_read_b128 v[218:221], v173
	ds_read_b128 v[222:225], v173 offset:1024
	ds_read_b128 v[226:229], v173 offset:2048
	ds_read_b128 v[230:233], v173 offset:3072
	global_load_lds_dwordx4 v[164:165], off
	v_lshl_add_u64 v[186:187], s[40:41], 0, v[152:153]
	s_add_i32 m0, s0, 0x2000
	s_nop 0
	global_load_lds_dwordx4 v[186:187], off
	s_barrier
	s_waitcnt lgkmcnt(0)
	s_nop 0
	s_waitcnt lgkmcnt(0)
	v_mfma_f32_16x16x32_bf16 v[118:121], v[218:221], v[182:185], v[118:121]
	v_mfma_f32_16x16x32_bf16 v[110:113], v[226:229], v[182:185], v[110:113]
	v_mfma_f32_16x16x32_bf16 v[102:105], v[218:221], v[194:197], v[102:105]
	v_mfma_f32_16x16x32_bf16 v[94:97], v[226:229], v[194:197], v[94:97]
	v_mfma_f32_16x16x32_bf16 v[86:89], v[218:221], v[202:205], v[86:89]
	v_mfma_f32_16x16x32_bf16 v[78:81], v[226:229], v[202:205], v[78:81]
	v_mfma_f32_16x16x32_bf16 v[70:73], v[218:221], v[210:213], v[70:73]
	v_mfma_f32_16x16x32_bf16 v[66:69], v[226:229], v[210:213], v[66:69]
	v_mfma_f32_16x16x32_bf16 v[118:121], v[222:225], v[190:193], v[118:121]
	v_mfma_f32_16x16x32_bf16 v[110:113], v[230:233], v[190:193], v[110:113]
	v_mfma_f32_16x16x32_bf16 v[102:105], v[222:225], v[198:201], v[102:105]
	v_mfma_f32_16x16x32_bf16 v[94:97], v[230:233], v[198:201], v[94:97]
	v_mfma_f32_16x16x32_bf16 v[86:89], v[222:225], v[206:209], v[86:89]
	v_mfma_f32_16x16x32_bf16 v[78:81], v[230:233], v[206:209], v[78:81]
	v_mfma_f32_16x16x32_bf16 v[70:73], v[222:225], v[214:217], v[70:73]
	v_mfma_f32_16x16x32_bf16 v[66:69], v[230:233], v[214:217], v[66:69]
	s_nop 0
	s_mov_b32 m0, s39
	s_barrier
	ds_read_b128 v[182:185], v172 offset:16384
	ds_read_b128 v[190:193], v172 offset:17408
	ds_read_b128 v[194:197], v172 offset:18432
	ds_read_b128 v[198:201], v172 offset:19456
	ds_read_b128 v[202:205], v172 offset:20480
	ds_read_b128 v[206:209], v172 offset:21504
	ds_read_b128 v[210:213], v172 offset:22528
	ds_read_b128 v[214:217], v172 offset:23552
	global_load_lds_dwordx4 v154, s[42:43]
	s_mov_b32 m0, s48
	v_mov_b32_e32 v149, v155
	global_load_lds_dwordx4 v148, s[42:43]
	s_barrier
	s_waitcnt lgkmcnt(0)
	v_lshl_add_u64 v[234:235], s[42:43], 0, v[154:155]
	v_lshl_add_u64 v[148:149], s[42:43], 0, v[148:149]
	s_nop 0
	s_waitcnt lgkmcnt(0)
	v_mfma_f32_16x16x32_bf16 v[62:65], v[140:143], v[182:185], v[62:65]
	v_mfma_f32_16x16x32_bf16 v[58:61], v[160:163], v[182:185], v[58:61]
	v_mfma_f32_16x16x32_bf16 v[50:53], v[140:143], v[194:197], v[50:53]
	v_mfma_f32_16x16x32_bf16 v[42:45], v[160:163], v[194:197], v[42:45]
	v_mfma_f32_16x16x32_bf16 v[26:29], v[140:143], v[202:205], v[26:29]
	v_mfma_f32_16x16x32_bf16 v[14:17], v[160:163], v[202:205], v[14:17]
	v_mfma_f32_16x16x32_bf16 v[6:9], v[140:143], v[210:213], v[6:9]
	v_mfma_f32_16x16x32_bf16 v[2:5], v[160:163], v[210:213], v[2:5]
	v_mfma_f32_16x16x32_bf16 v[62:65], v[144:147], v[190:193], v[62:65]
	v_mfma_f32_16x16x32_bf16 v[58:61], v[178:181], v[190:193], v[58:61]
	v_mfma_f32_16x16x32_bf16 v[50:53], v[144:147], v[198:201], v[50:53]
	v_mfma_f32_16x16x32_bf16 v[42:45], v[178:181], v[198:201], v[42:45]
	v_mfma_f32_16x16x32_bf16 v[26:29], v[144:147], v[206:209], v[26:29]
	v_mfma_f32_16x16x32_bf16 v[14:17], v[178:181], v[206:209], v[14:17]
	v_mfma_f32_16x16x32_bf16 v[6:9], v[144:147], v[214:217], v[6:9]
	v_mfma_f32_16x16x32_bf16 v[2:5], v[178:181], v[214:217], v[2:5]
	s_nop 0
	s_barrier
	s_add_u32 s0, s40, 0x80000
	s_addc_u32 s1, s41, 0
	s_add_i32 s69, s62, s47
	v_lshl_add_u64 v[140:141], s[0:1], 0, v[150:151]
	s_mov_b32 m0, s69
	s_nop 0
	global_load_lds_dwordx4 v[140:141], off
	v_lshl_add_u64 v[140:141], s[0:1], 0, v[152:153]
	s_add_i32 m0, s69, 0x2000
	s_nop 0
	global_load_lds_dwordx4 v[140:141], off
	s_waitcnt vmcnt(6)
	s_barrier
	s_nop 0
	v_mfma_f32_16x16x32_bf16 v[54:57], v[218:221], v[182:185], v[54:57]
	v_mfma_f32_16x16x32_bf16 v[46:49], v[226:229], v[182:185], v[46:49]
	v_mfma_f32_16x16x32_bf16 v[30:33], v[218:221], v[194:197], v[30:33]
	v_mfma_f32_16x16x32_bf16 v[22:25], v[226:229], v[194:197], v[22:25]
	v_mfma_f32_16x16x32_bf16 v[38:41], v[218:221], v[202:205], v[38:41]
	v_mfma_f32_16x16x32_bf16 v[34:37], v[226:229], v[202:205], v[34:37]
	v_mfma_f32_16x16x32_bf16 v[18:21], v[218:221], v[210:213], v[18:21]
	v_mfma_f32_16x16x32_bf16 v[10:13], v[226:229], v[210:213], v[10:13]
	v_mfma_f32_16x16x32_bf16 v[54:57], v[222:225], v[190:193], v[54:57]
	v_mfma_f32_16x16x32_bf16 v[46:49], v[230:233], v[190:193], v[46:49]
	v_mfma_f32_16x16x32_bf16 v[30:33], v[222:225], v[198:201], v[30:33]
	v_mfma_f32_16x16x32_bf16 v[22:25], v[230:233], v[198:201], v[22:25]
	v_mfma_f32_16x16x32_bf16 v[38:41], v[222:225], v[206:209], v[38:41]
	v_mfma_f32_16x16x32_bf16 v[34:37], v[230:233], v[206:209], v[34:37]
	v_mfma_f32_16x16x32_bf16 v[18:21], v[222:225], v[214:217], v[18:21]
	v_mfma_f32_16x16x32_bf16 v[10:13], v[230:233], v[214:217], v[10:13]
	s_nop 0
	s_add_i32 s0, 0, 0x18000
	v_add_u32_e32 v154, s0, v169
	s_barrier
	ds_read_b128 v[140:143], v154
	ds_read_b128 v[144:147], v154 offset:1024
	ds_read_b128 v[160:163], v154 offset:2048
	ds_read_b128 v[178:181], v154 offset:3072
	s_mov_b32 m0, s49
	ds_read_b128 v[182:185], v172 offset:32768
	ds_read_b128 v[190:193], v172 offset:33792
	ds_read_b128 v[194:197], v172 offset:34816
	ds_read_b128 v[198:201], v172 offset:35840
	ds_read_b128 v[202:205], v172 offset:36864
	ds_read_b128 v[206:209], v172 offset:37888
	ds_read_b128 v[210:213], v172 offset:38912
	ds_read_b128 v[214:217], v172 offset:39936
	global_load_lds_dwordx4 v133, s[42:43]
	s_mov_b32 m0, s50
	s_nop 0
	global_load_lds_dwordx4 v135, s[42:43]
	s_waitcnt lgkmcnt(8)
	s_barrier
	s_waitcnt lgkmcnt(0)
	s_nop 0
	s_waitcnt lgkmcnt(0)
	v_mfma_f32_16x16x32_bf16 v[126:129], v[140:143], v[182:185], v[126:129]
	v_mfma_f32_16x16x32_bf16 v[122:125], v[160:163], v[182:185], v[122:125]
	v_mfma_f32_16x16x32_bf16 v[114:117], v[140:143], v[194:197], v[114:117]
	v_mfma_f32_16x16x32_bf16 v[106:109], v[160:163], v[194:197], v[106:109]
	v_mfma_f32_16x16x32_bf16 v[98:101], v[140:143], v[202:205], v[98:101]
	v_mfma_f32_16x16x32_bf16 v[90:93], v[160:163], v[202:205], v[90:93]
	v_mfma_f32_16x16x32_bf16 v[82:85], v[140:143], v[210:213], v[82:85]
	v_mfma_f32_16x16x32_bf16 v[74:77], v[160:163], v[210:213], v[74:77]
	v_mfma_f32_16x16x32_bf16 v[126:129], v[144:147], v[190:193], v[126:129]
	v_mfma_f32_16x16x32_bf16 v[122:125], v[178:181], v[190:193], v[122:125]
	v_mfma_f32_16x16x32_bf16 v[114:117], v[144:147], v[198:201], v[114:117]
	v_mfma_f32_16x16x32_bf16 v[106:109], v[178:181], v[198:201], v[106:109]
	v_mfma_f32_16x16x32_bf16 v[98:101], v[144:147], v[206:209], v[98:101]
	v_mfma_f32_16x16x32_bf16 v[90:93], v[178:181], v[206:209], v[90:93]
	v_mfma_f32_16x16x32_bf16 v[82:85], v[144:147], v[214:217], v[82:85]
	v_mfma_f32_16x16x32_bf16 v[74:77], v[178:181], v[214:217], v[74:77]
	s_nop 0
	s_barrier
	s_add_i32 s42, 0, 0x1c000
	s_add_i32 s0, s0, s47
	v_add_u32_e32 v133, s42, v169
	v_lshl_add_u64 v[164:165], v[164:165], 0, s[16:17]
	s_mov_b32 m0, s0
	ds_read_b128 v[218:221], v133
	ds_read_b128 v[222:225], v133 offset:1024
	ds_read_b128 v[226:229], v133 offset:2048
	ds_read_b128 v[230:233], v133 offset:3072
	global_load_lds_dwordx4 v[164:165], off
	v_lshl_add_u64 v[164:165], v[186:187], 0, s[16:17]
	s_add_i32 m0, s0, 0x2000
	s_nop 0
	global_load_lds_dwordx4 v[164:165], off
	s_barrier
	s_waitcnt lgkmcnt(0)
	s_nop 0
	s_waitcnt lgkmcnt(0)
	v_mfma_f32_16x16x32_bf16 v[118:121], v[218:221], v[182:185], v[118:121]
	v_mfma_f32_16x16x32_bf16 v[110:113], v[226:229], v[182:185], v[110:113]
	v_mfma_f32_16x16x32_bf16 v[102:105], v[218:221], v[194:197], v[102:105]
	v_mfma_f32_16x16x32_bf16 v[94:97], v[226:229], v[194:197], v[94:97]
	v_mfma_f32_16x16x32_bf16 v[86:89], v[218:221], v[202:205], v[86:89]
	v_mfma_f32_16x16x32_bf16 v[78:81], v[226:229], v[202:205], v[78:81]
	v_mfma_f32_16x16x32_bf16 v[70:73], v[218:221], v[210:213], v[70:73]
	v_mfma_f32_16x16x32_bf16 v[66:69], v[226:229], v[210:213], v[66:69]
	v_mfma_f32_16x16x32_bf16 v[118:121], v[222:225], v[190:193], v[118:121]
	v_mfma_f32_16x16x32_bf16 v[110:113], v[230:233], v[190:193], v[110:113]
	v_mfma_f32_16x16x32_bf16 v[102:105], v[222:225], v[198:201], v[102:105]
	v_mfma_f32_16x16x32_bf16 v[94:97], v[230:233], v[198:201], v[94:97]
	v_mfma_f32_16x16x32_bf16 v[86:89], v[222:225], v[206:209], v[86:89]
	v_mfma_f32_16x16x32_bf16 v[78:81], v[230:233], v[206:209], v[78:81]
	v_mfma_f32_16x16x32_bf16 v[70:73], v[222:225], v[214:217], v[70:73]
	v_mfma_f32_16x16x32_bf16 v[66:69], v[230:233], v[214:217], v[66:69]
	s_nop 0
	s_mov_b32 m0, s58
	v_lshl_add_u64 v[164:165], v[234:235], 0, s[16:17]
	s_barrier
	ds_read_b128 v[182:185], v172 offset:49152
	ds_read_b128 v[190:193], v172 offset:50176
	ds_read_b128 v[194:197], v172 offset:51200
	ds_read_b128 v[198:201], v172 offset:52224
	ds_read_b128 v[202:205], v172 offset:53248
	ds_read_b128 v[206:209], v172 offset:54272
	ds_read_b128 v[210:213], v172 offset:55296
	ds_read_b128 v[214:217], v172 offset:56320
	global_load_lds_dwordx4 v[164:165], off
	v_lshl_add_u64 v[148:149], v[148:149], 0, s[16:17]
	s_mov_b32 m0, s59
	s_nop 0
	global_load_lds_dwordx4 v[148:149], off
	s_barrier
	s_waitcnt lgkmcnt(0)
	s_nop 0
	s_waitcnt lgkmcnt(0)
	v_mfma_f32_16x16x32_bf16 v[62:65], v[140:143], v[182:185], v[62:65]
	v_mfma_f32_16x16x32_bf16 v[58:61], v[160:163], v[182:185], v[58:61]
	v_mfma_f32_16x16x32_bf16 v[50:53], v[140:143], v[194:197], v[50:53]
	v_mfma_f32_16x16x32_bf16 v[42:45], v[160:163], v[194:197], v[42:45]
	v_mfma_f32_16x16x32_bf16 v[26:29], v[140:143], v[202:205], v[26:29]
	v_mfma_f32_16x16x32_bf16 v[14:17], v[160:163], v[202:205], v[14:17]
	v_mfma_f32_16x16x32_bf16 v[6:9], v[140:143], v[210:213], v[6:9]
	v_mfma_f32_16x16x32_bf16 v[2:5], v[160:163], v[210:213], v[2:5]
	v_mfma_f32_16x16x32_bf16 v[62:65], v[144:147], v[190:193], v[62:65]
	v_mfma_f32_16x16x32_bf16 v[58:61], v[178:181], v[190:193], v[58:61]
	v_mfma_f32_16x16x32_bf16 v[50:53], v[144:147], v[198:201], v[50:53]
	v_mfma_f32_16x16x32_bf16 v[42:45], v[178:181], v[198:201], v[42:45]
	v_mfma_f32_16x16x32_bf16 v[26:29], v[144:147], v[206:209], v[26:29]
	v_mfma_f32_16x16x32_bf16 v[14:17], v[178:181], v[206:209], v[14:17]
	v_mfma_f32_16x16x32_bf16 v[6:9], v[144:147], v[214:217], v[6:9]
	v_mfma_f32_16x16x32_bf16 v[2:5], v[178:181], v[214:217], v[2:5]
	s_nop 0
	s_barrier
	s_add_u32 s0, s40, 0x80080
	s_addc_u32 s1, s41, 0
	s_add_i32 s40, s42, s47
	v_lshl_add_u64 v[140:141], s[0:1], 0, v[150:151]
	s_mov_b32 m0, s40
	s_nop 0
	global_load_lds_dwordx4 v[140:141], off
	v_lshl_add_u64 v[140:141], s[0:1], 0, v[152:153]
	s_add_i32 m0, s40, 0x2000
	s_nop 0
	global_load_lds_dwordx4 v[140:141], off
	s_waitcnt vmcnt(6)
	s_barrier
	s_nop 0
	v_mfma_f32_16x16x32_bf16 v[54:57], v[218:221], v[182:185], v[54:57]
	v_mfma_f32_16x16x32_bf16 v[46:49], v[226:229], v[182:185], v[46:49]
	v_mfma_f32_16x16x32_bf16 v[30:33], v[218:221], v[194:197], v[30:33]
	v_mfma_f32_16x16x32_bf16 v[22:25], v[226:229], v[194:197], v[22:25]
	v_mfma_f32_16x16x32_bf16 v[38:41], v[218:221], v[202:205], v[38:41]
	v_mfma_f32_16x16x32_bf16 v[34:37], v[226:229], v[202:205], v[34:37]
	v_mfma_f32_16x16x32_bf16 v[18:21], v[218:221], v[210:213], v[18:21]
	v_mfma_f32_16x16x32_bf16 v[10:13], v[226:229], v[210:213], v[10:13]
	v_mfma_f32_16x16x32_bf16 v[54:57], v[222:225], v[190:193], v[54:57]
	v_mfma_f32_16x16x32_bf16 v[46:49], v[230:233], v[190:193], v[46:49]
	v_mfma_f32_16x16x32_bf16 v[30:33], v[222:225], v[198:201], v[30:33]
	v_mfma_f32_16x16x32_bf16 v[22:25], v[230:233], v[198:201], v[22:25]
	v_mfma_f32_16x16x32_bf16 v[38:41], v[222:225], v[206:209], v[38:41]
	v_mfma_f32_16x16x32_bf16 v[34:37], v[230:233], v[206:209], v[34:37]
	v_mfma_f32_16x16x32_bf16 v[18:21], v[222:225], v[214:217], v[18:21]
	v_mfma_f32_16x16x32_bf16 v[10:13], v[230:233], v[214:217], v[10:13]
	s_nop 0
	s_add_i32 s68, s68, 2
	s_add_u32 s6, s6, 0x100
	s_addc_u32 s7, s7, 0
	s_cmp_gt_u32 s68, 29
	s_barrier
	s_cbranch_scc0 .LBB0_1941
	s_cmpk_gt_i32 s64, 0x7fff
	s_mov_b64 s[6:7], 0x6000
	s_cbranch_scc1 .LBB0_1931
	s_ashr_i32 s0, s64, 31
	s_lshr_b32 s0, s0, 18
	s_add_i32 s0, s64, s0
	s_ashr_i32 s0, s0, 14
	s_mul_i32 s6, s0, 0x3000
	s_ashr_i32 s7, s6, 31
	s_branch .LBB0_1931

.LBB0_2150:
	s_add_u32 s36, s54, s4
	s_addc_u32 s37, s55, s5
	v_add_u32_e32 v141, s75, v150
	s_add_u32 s38, s36, 0x8c00100
	ds_read_b128 v[160:163], v141
	ds_read_b128 v[164:167], v141 offset:1024
	ds_read_b128 v[168:171], v141 offset:2048
	ds_read_b128 v[172:175], v141 offset:3072
	s_addc_u32 s39, s37, 0
	s_add_u32 s88, s85, s4
	s_addc_u32 s89, s86, s5
	s_cmpk_eq_i32 s4, 0xf00
	s_cselect_b64 vcc, -1, 0
	s_and_b64 s[36:37], vcc, exec
	v_cndmask_b32_e32 v134, v158, v154, vcc
	s_cselect_b32 s39, s9, s39
	s_cselect_b32 s38, s8, s38
	v_cndmask_b32_e32 v137, v136, v155, vcc
	v_cndmask_b32_e32 v224, v138, v156, vcc
	v_cndmask_b32_e32 v141, v140, v157, vcc
	s_cselect_b32 s37, s31, s89
	s_cselect_b32 s36, s84, s88
	v_lshl_add_u64 v[208:209], v[144:145], 0, s[4:5]
	s_add_i32 m0, s46, 0xc000
	ds_read_b128 v[176:179], v153
	ds_read_b128 v[180:183], v153 offset:1024
	ds_read_b128 v[184:187], v153 offset:2048
	ds_read_b128 v[188:191], v153 offset:3072
	ds_read_b128 v[192:195], v153 offset:4096
	ds_read_b128 v[196:199], v153 offset:5120
	ds_read_b128 v[200:203], v153 offset:6144
	ds_read_b128 v[204:207], v153 offset:7168
	global_load_lds_dwordx4 v[208:209], off
	v_lshl_add_u64 v[208:209], v[142:143], 0, s[4:5]
	s_add_i32 m0, s46, 0xe000
	s_nop 0
	global_load_lds_dwordx4 v[208:209], off
	s_waitcnt lgkmcnt(8)
	s_barrier
	s_waitcnt lgkmcnt(0)
	s_nop 0
	s_waitcnt lgkmcnt(0)
	v_mfma_f32_16x16x32_bf16 v[126:129], v[160:163], v[176:179], v[126:129]
	v_mfma_f32_16x16x32_bf16 v[122:125], v[168:171], v[176:179], v[122:125]
	v_mfma_f32_16x16x32_bf16 v[110:113], v[160:163], v[184:187], v[110:113]
	v_mfma_f32_16x16x32_bf16 v[106:109], v[168:171], v[184:187], v[106:109]
	v_mfma_f32_16x16x32_bf16 v[94:97], v[160:163], v[192:195], v[94:97]
	v_mfma_f32_16x16x32_bf16 v[90:93], v[168:171], v[192:195], v[90:93]
	v_mfma_f32_16x16x32_bf16 v[78:81], v[160:163], v[200:203], v[78:81]
	v_mfma_f32_16x16x32_bf16 v[74:77], v[168:171], v[200:203], v[74:77]
	v_mfma_f32_16x16x32_bf16 v[126:129], v[164:167], v[180:183], v[126:129]
	v_mfma_f32_16x16x32_bf16 v[122:125], v[172:175], v[180:183], v[122:125]
	v_mfma_f32_16x16x32_bf16 v[110:113], v[164:167], v[188:191], v[110:113]
	v_mfma_f32_16x16x32_bf16 v[106:109], v[172:175], v[188:191], v[106:109]
	v_mfma_f32_16x16x32_bf16 v[94:97], v[164:167], v[196:199], v[94:97]
	v_mfma_f32_16x16x32_bf16 v[90:93], v[172:175], v[196:199], v[90:93]
	v_mfma_f32_16x16x32_bf16 v[78:81], v[164:167], v[204:207], v[78:81]
	v_mfma_f32_16x16x32_bf16 v[74:77], v[172:175], v[204:207], v[74:77]
	s_nop 0
	s_barrier
	s_add_i32 s88, s75, s43
	v_add_u32_e32 v159, s76, v150
	v_lshl_add_u64 v[226:227], s[36:37], 0, v[132:133]
	s_mov_b32 m0, s88
	ds_read_b128 v[208:211], v159
	ds_read_b128 v[212:215], v159 offset:1024
	ds_read_b128 v[216:219], v159 offset:2048
	ds_read_b128 v[220:223], v159 offset:3072
	global_load_lds_dwordx4 v[226:227], off
	v_lshl_add_u64 v[228:229], s[36:37], 0, v[130:131]
	s_add_i32 m0, s88, 0x2000
	s_nop 0
	global_load_lds_dwordx4 v[228:229], off
	s_barrier
	s_waitcnt lgkmcnt(0)
	s_nop 0
	s_waitcnt lgkmcnt(0)
	v_mfma_f32_16x16x32_bf16 v[118:121], v[208:211], v[176:179], v[118:121]
	v_mfma_f32_16x16x32_bf16 v[114:117], v[216:219], v[176:179], v[114:117]
	v_mfma_f32_16x16x32_bf16 v[102:105], v[208:211], v[184:187], v[102:105]
	v_mfma_f32_16x16x32_bf16 v[98:101], v[216:219], v[184:187], v[98:101]
	v_mfma_f32_16x16x32_bf16 v[86:89], v[208:211], v[192:195], v[86:89]
	v_mfma_f32_16x16x32_bf16 v[82:85], v[216:219], v[192:195], v[82:85]
	v_mfma_f32_16x16x32_bf16 v[70:73], v[208:211], v[200:203], v[70:73]
	v_mfma_f32_16x16x32_bf16 v[66:69], v[216:219], v[200:203], v[66:69]
	v_mfma_f32_16x16x32_bf16 v[118:121], v[212:215], v[180:183], v[118:121]
	v_mfma_f32_16x16x32_bf16 v[114:117], v[220:223], v[180:183], v[114:117]
	v_mfma_f32_16x16x32_bf16 v[102:105], v[212:215], v[188:191], v[102:105]
	v_mfma_f32_16x16x32_bf16 v[98:101], v[220:223], v[188:191], v[98:101]
	v_mfma_f32_16x16x32_bf16 v[86:89], v[212:215], v[196:199], v[86:89]
	v_mfma_f32_16x16x32_bf16 v[82:85], v[220:223], v[196:199], v[82:85]
	v_mfma_f32_16x16x32_bf16 v[70:73], v[212:215], v[204:207], v[70:73]
	v_mfma_f32_16x16x32_bf16 v[66:69], v[220:223], v[204:207], v[66:69]
	s_nop 0
	s_mov_b32 m0, s46
	s_barrier
	ds_read_b128 v[176:179], v153 offset:16384
	ds_read_b128 v[180:183], v153 offset:17408
	ds_read_b128 v[184:187], v153 offset:18432
	ds_read_b128 v[188:191], v153 offset:19456
	ds_read_b128 v[192:195], v153 offset:20480
	ds_read_b128 v[196:199], v153 offset:21504
	ds_read_b128 v[200:203], v153 offset:22528
	ds_read_b128 v[204:207], v153 offset:23552
	global_load_lds_dwordx4 v134, s[38:39]
	s_mov_b32 m0, s47
	v_mov_b32_e32 v225, v135
	global_load_lds_dwordx4 v224, s[38:39]
	s_barrier
	s_waitcnt lgkmcnt(0)
	v_lshl_add_u64 v[230:231], s[38:39], 0, v[134:135]
	v_lshl_add_u64 v[224:225], s[38:39], 0, v[224:225]
	s_nop 0
	s_waitcnt lgkmcnt(0)
	v_mfma_f32_16x16x32_bf16 v[62:65], v[160:163], v[176:179], v[62:65]
	v_mfma_f32_16x16x32_bf16 v[58:61], v[168:171], v[176:179], v[58:61]
	v_mfma_f32_16x16x32_bf16 v[46:49], v[160:163], v[184:187], v[46:49]
	v_mfma_f32_16x16x32_bf16 v[42:45], v[168:171], v[184:187], v[42:45]
	v_mfma_f32_16x16x32_bf16 v[22:25], v[160:163], v[192:195], v[22:25]
	v_mfma_f32_16x16x32_bf16 v[18:21], v[168:171], v[192:195], v[18:21]
	v_mfma_f32_16x16x32_bf16 v[6:9], v[160:163], v[200:203], v[6:9]
	v_mfma_f32_16x16x32_bf16 v[2:5], v[168:171], v[200:203], v[2:5]
	v_mfma_f32_16x16x32_bf16 v[62:65], v[164:167], v[180:183], v[62:65]
	v_mfma_f32_16x16x32_bf16 v[58:61], v[172:175], v[180:183], v[58:61]
	v_mfma_f32_16x16x32_bf16 v[46:49], v[164:167], v[188:191], v[46:49]
	v_mfma_f32_16x16x32_bf16 v[42:45], v[172:175], v[188:191], v[42:45]
	v_mfma_f32_16x16x32_bf16 v[22:25], v[164:167], v[196:199], v[22:25]
	v_mfma_f32_16x16x32_bf16 v[18:21], v[172:175], v[196:199], v[18:21]
	v_mfma_f32_16x16x32_bf16 v[6:9], v[164:167], v[204:207], v[6:9]
	v_mfma_f32_16x16x32_bf16 v[2:5], v[172:175], v[204:207], v[2:5]
	s_nop 0
	s_barrier
	s_add_u32 s88, s36, 0x80000
	s_addc_u32 s89, s37, 0
	s_add_i32 s90, s76, s43
	v_lshl_add_u64 v[160:161], s[88:89], 0, v[132:133]
	s_mov_b32 m0, s90
	s_nop 0
	global_load_lds_dwordx4 v[160:161], off
	v_lshl_add_u64 v[160:161], s[88:89], 0, v[130:131]
	s_add_i32 m0, s90, 0x2000
	s_nop 0
	global_load_lds_dwordx4 v[160:161], off
	s_waitcnt vmcnt(6)
	s_barrier
	s_nop 0
	v_mfma_f32_16x16x32_bf16 v[54:57], v[208:211], v[176:179], v[54:57]
	v_mfma_f32_16x16x32_bf16 v[50:53], v[216:219], v[176:179], v[50:53]
	v_mfma_f32_16x16x32_bf16 v[30:33], v[208:211], v[184:187], v[30:33]
	v_mfma_f32_16x16x32_bf16 v[26:29], v[216:219], v[184:187], v[26:29]
	v_mfma_f32_16x16x32_bf16 v[34:37], v[208:211], v[192:195], v[34:37]
	v_mfma_f32_16x16x32_bf16 v[38:41], v[216:219], v[192:195], v[38:41]
	v_mfma_f32_16x16x32_bf16 v[10:13], v[208:211], v[200:203], v[10:13]
	v_mfma_f32_16x16x32_bf16 v[14:17], v[216:219], v[200:203], v[14:17]
	v_mfma_f32_16x16x32_bf16 v[54:57], v[212:215], v[180:183], v[54:57]
	v_mfma_f32_16x16x32_bf16 v[50:53], v[220:223], v[180:183], v[50:53]
	v_mfma_f32_16x16x32_bf16 v[30:33], v[212:215], v[188:191], v[30:33]
	v_mfma_f32_16x16x32_bf16 v[26:29], v[220:223], v[188:191], v[26:29]
	v_mfma_f32_16x16x32_bf16 v[34:37], v[212:215], v[196:199], v[34:37]
	v_mfma_f32_16x16x32_bf16 v[38:41], v[220:223], v[196:199], v[38:41]
	v_mfma_f32_16x16x32_bf16 v[10:13], v[212:215], v[204:207], v[10:13]
	v_mfma_f32_16x16x32_bf16 v[14:17], v[220:223], v[204:207], v[14:17]
	s_nop 0
	s_add_i32 s88, 0, 0x18000
	v_add_u32_e32 v134, s88, v150
	s_barrier
	ds_read_b128 v[160:163], v134
	ds_read_b128 v[164:167], v134 offset:1024
	ds_read_b128 v[168:171], v134 offset:2048
	ds_read_b128 v[172:175], v134 offset:3072
	s_mov_b32 m0, s48
	ds_read_b128 v[176:179], v153 offset:32768
	ds_read_b128 v[180:183], v153 offset:33792
	ds_read_b128 v[184:187], v153 offset:34816
	ds_read_b128 v[188:191], v153 offset:35840
	ds_read_b128 v[192:195], v153 offset:36864
	ds_read_b128 v[196:199], v153 offset:37888
	ds_read_b128 v[200:203], v153 offset:38912
	ds_read_b128 v[204:207], v153 offset:39936
	global_load_lds_dwordx4 v137, s[38:39]
	s_mov_b32 m0, s49
	s_nop 0
	global_load_lds_dwordx4 v141, s[38:39]
	s_waitcnt lgkmcnt(8)
	s_barrier
	s_waitcnt lgkmcnt(0)
	s_nop 0
	s_waitcnt lgkmcnt(0)
	v_mfma_f32_16x16x32_bf16 v[126:129], v[160:163], v[176:179], v[126:129]
	v_mfma_f32_16x16x32_bf16 v[122:125], v[168:171], v[176:179], v[122:125]
	v_mfma_f32_16x16x32_bf16 v[110:113], v[160:163], v[184:187], v[110:113]
	v_mfma_f32_16x16x32_bf16 v[106:109], v[168:171], v[184:187], v[106:109]
	v_mfma_f32_16x16x32_bf16 v[94:97], v[160:163], v[192:195], v[94:97]
	v_mfma_f32_16x16x32_bf16 v[90:93], v[168:171], v[192:195], v[90:93]
	v_mfma_f32_16x16x32_bf16 v[78:81], v[160:163], v[200:203], v[78:81]
	v_mfma_f32_16x16x32_bf16 v[74:77], v[168:171], v[200:203], v[74:77]
	v_mfma_f32_16x16x32_bf16 v[126:129], v[164:167], v[180:183], v[126:129]
	v_mfma_f32_16x16x32_bf16 v[122:125], v[172:175], v[180:183], v[122:125]
	v_mfma_f32_16x16x32_bf16 v[110:113], v[164:167], v[188:191], v[110:113]
	v_mfma_f32_16x16x32_bf16 v[106:109], v[172:175], v[188:191], v[106:109]
	v_mfma_f32_16x16x32_bf16 v[94:97], v[164:167], v[196:199], v[94:97]
	v_mfma_f32_16x16x32_bf16 v[90:93], v[172:175], v[196:199], v[90:93]
	v_mfma_f32_16x16x32_bf16 v[78:81], v[164:167], v[204:207], v[78:81]
	v_mfma_f32_16x16x32_bf16 v[74:77], v[172:175], v[204:207], v[74:77]
	s_nop 0
	s_barrier
	s_add_i32 s38, 0, 0x1c000
	s_add_i32 s39, s88, s43
	v_add_u32_e32 v134, s38, v150
	v_lshl_add_u64 v[226:227], v[226:227], 0, s[12:13]
	s_mov_b32 m0, s39
	ds_read_b128 v[208:211], v134
	ds_read_b128 v[212:215], v134 offset:1024
	ds_read_b128 v[216:219], v134 offset:2048
	ds_read_b128 v[220:223], v134 offset:3072
	global_load_lds_dwordx4 v[226:227], off
	v_lshl_add_u64 v[226:227], v[228:229], 0, s[12:13]
	s_add_i32 m0, s39, 0x2000
	s_nop 0
	global_load_lds_dwordx4 v[226:227], off
	s_barrier
	s_waitcnt lgkmcnt(0)
	s_nop 0
	s_waitcnt lgkmcnt(0)
	v_mfma_f32_16x16x32_bf16 v[118:121], v[208:211], v[176:179], v[118:121]
	v_mfma_f32_16x16x32_bf16 v[114:117], v[216:219], v[176:179], v[114:117]
	v_mfma_f32_16x16x32_bf16 v[102:105], v[208:211], v[184:187], v[102:105]
	v_mfma_f32_16x16x32_bf16 v[98:101], v[216:219], v[184:187], v[98:101]
	v_mfma_f32_16x16x32_bf16 v[86:89], v[208:211], v[192:195], v[86:89]
	v_mfma_f32_16x16x32_bf16 v[82:85], v[216:219], v[192:195], v[82:85]
	v_mfma_f32_16x16x32_bf16 v[70:73], v[208:211], v[200:203], v[70:73]
	v_mfma_f32_16x16x32_bf16 v[66:69], v[216:219], v[200:203], v[66:69]
	v_mfma_f32_16x16x32_bf16 v[118:121], v[212:215], v[180:183], v[118:121]
	v_mfma_f32_16x16x32_bf16 v[114:117], v[220:223], v[180:183], v[114:117]
	v_mfma_f32_16x16x32_bf16 v[102:105], v[212:215], v[188:191], v[102:105]
	v_mfma_f32_16x16x32_bf16 v[98:101], v[220:223], v[188:191], v[98:101]
	v_mfma_f32_16x16x32_bf16 v[86:89], v[212:215], v[196:199], v[86:89]
	v_mfma_f32_16x16x32_bf16 v[82:85], v[220:223], v[196:199], v[82:85]
	v_mfma_f32_16x16x32_bf16 v[70:73], v[212:215], v[204:207], v[70:73]
	v_mfma_f32_16x16x32_bf16 v[66:69], v[220:223], v[204:207], v[66:69]
	s_nop 0
	s_mov_b32 m0, s56
	v_lshl_add_u64 v[226:227], v[230:231], 0, s[12:13]
	s_barrier
	ds_read_b128 v[176:179], v153 offset:49152
	ds_read_b128 v[180:183], v153 offset:50176
	ds_read_b128 v[184:187], v153 offset:51200
	ds_read_b128 v[188:191], v153 offset:52224
	ds_read_b128 v[192:195], v153 offset:53248
	ds_read_b128 v[196:199], v153 offset:54272
	ds_read_b128 v[200:203], v153 offset:55296
	ds_read_b128 v[204:207], v153 offset:56320
	global_load_lds_dwordx4 v[226:227], off
	v_lshl_add_u64 v[224:225], v[224:225], 0, s[12:13]
	s_mov_b32 m0, s57
	s_nop 0
	global_load_lds_dwordx4 v[224:225], off
	s_barrier
	s_waitcnt lgkmcnt(0)
	s_nop 0
	s_waitcnt lgkmcnt(0)
	v_mfma_f32_16x16x32_bf16 v[62:65], v[160:163], v[176:179], v[62:65]
	v_mfma_f32_16x16x32_bf16 v[58:61], v[168:171], v[176:179], v[58:61]
	v_mfma_f32_16x16x32_bf16 v[46:49], v[160:163], v[184:187], v[46:49]
	v_mfma_f32_16x16x32_bf16 v[42:45], v[168:171], v[184:187], v[42:45]
	v_mfma_f32_16x16x32_bf16 v[22:25], v[160:163], v[192:195], v[22:25]
	v_mfma_f32_16x16x32_bf16 v[18:21], v[168:171], v[192:195], v[18:21]
	v_mfma_f32_16x16x32_bf16 v[6:9], v[160:163], v[200:203], v[6:9]
	v_mfma_f32_16x16x32_bf16 v[2:5], v[168:171], v[200:203], v[2:5]
	v_mfma_f32_16x16x32_bf16 v[62:65], v[164:167], v[180:183], v[62:65]
	v_mfma_f32_16x16x32_bf16 v[58:61], v[172:175], v[180:183], v[58:61]
	v_mfma_f32_16x16x32_bf16 v[46:49], v[164:167], v[188:191], v[46:49]
	v_mfma_f32_16x16x32_bf16 v[42:45], v[172:175], v[188:191], v[42:45]
	v_mfma_f32_16x16x32_bf16 v[22:25], v[164:167], v[196:199], v[22:25]
	v_mfma_f32_16x16x32_bf16 v[18:21], v[172:175], v[196:199], v[18:21]
	v_mfma_f32_16x16x32_bf16 v[6:9], v[164:167], v[204:207], v[6:9]
	v_mfma_f32_16x16x32_bf16 v[2:5], v[172:175], v[204:207], v[2:5]
	s_nop 0
	s_barrier
	s_add_u32 s36, s36, 0x80080
	s_addc_u32 s37, s37, 0
	s_add_i32 s38, s38, s43
	v_lshl_add_u64 v[160:161], s[36:37], 0, v[132:133]
	s_mov_b32 m0, s38
	s_nop 0
	global_load_lds_dwordx4 v[160:161], off
	v_lshl_add_u64 v[160:161], s[36:37], 0, v[130:131]
	s_add_i32 m0, s38, 0x2000
	s_nop 0
	global_load_lds_dwordx4 v[160:161], off
	s_waitcnt vmcnt(6)
	s_barrier
	s_nop 0
	v_mfma_f32_16x16x32_bf16 v[54:57], v[208:211], v[176:179], v[54:57]
	v_mfma_f32_16x16x32_bf16 v[50:53], v[216:219], v[176:179], v[50:53]
	v_mfma_f32_16x16x32_bf16 v[30:33], v[208:211], v[184:187], v[30:33]
	v_mfma_f32_16x16x32_bf16 v[26:29], v[216:219], v[184:187], v[26:29]
	v_mfma_f32_16x16x32_bf16 v[34:37], v[208:211], v[192:195], v[34:37]
	v_mfma_f32_16x16x32_bf16 v[38:41], v[216:219], v[192:195], v[38:41]
	v_mfma_f32_16x16x32_bf16 v[10:13], v[208:211], v[200:203], v[10:13]
	v_mfma_f32_16x16x32_bf16 v[14:17], v[216:219], v[200:203], v[14:17]
	v_mfma_f32_16x16x32_bf16 v[54:57], v[212:215], v[180:183], v[54:57]
	v_mfma_f32_16x16x32_bf16 v[50:53], v[220:223], v[180:183], v[50:53]
	v_mfma_f32_16x16x32_bf16 v[30:33], v[212:215], v[188:191], v[30:33]
	v_mfma_f32_16x16x32_bf16 v[26:29], v[220:223], v[188:191], v[26:29]
	v_mfma_f32_16x16x32_bf16 v[34:37], v[212:215], v[196:199], v[34:37]
	v_mfma_f32_16x16x32_bf16 v[38:41], v[220:223], v[196:199], v[38:41]
	v_mfma_f32_16x16x32_bf16 v[10:13], v[212:215], v[204:207], v[10:13]
	v_mfma_f32_16x16x32_bf16 v[14:17], v[220:223], v[204:207], v[14:17]
	s_nop 0
	s_add_i32 s87, s87, 2
	s_add_u32 s4, s4, 0x100
	s_addc_u32 s5, s5, 0
	s_cmp_gt_u32 s87, 29
	s_barrier
	s_cbranch_scc0 .LBB0_2150
	v_mul_f32_e32 v134, 0xbfb8aa3b, v126
	v_exp_f32_e32 v134, v134
	v_mul_f32_e32 v138, 0xbfb8aa3b, v127
	v_exp_f32_e32 v138, v138
	v_mul_f32_e32 v141, 0xbfb8aa3b, v129
	v_add_f32_e32 v134, 1.0, v134
	v_rcp_f32_e32 v140, v134
	v_add_f32_e32 v134, 1.0, v138
	v_mul_f32_e32 v138, 0xbfb8aa3b, v128
	v_exp_f32_e32 v138, v138
	v_exp_f32_e32 v143, v141
	v_rcp_f32_e32 v141, v134
	s_add_i32 s4, s82, s51
	v_add_f32_e32 v134, 1.0, v138
	v_rcp_f32_e32 v142, v134
	v_add_f32_e32 v134, 1.0, v143
	v_rcp_f32_e32 v143, v134
	s_lshr_b32 s5, s4, 31
	s_add_i32 s5, s4, s5
	v_pk_mul_f32 v[126:127], v[126:127], v[140:141]
	v_add_u32_e32 v136, s83, v139
	s_ashr_i32 s5, s5, 1
	v_pk_mul_f32 v[122:123], v[122:123], v[126:127]
	v_pk_mul_f32 v[126:127], v[128:129], v[142:143]
	v_ashrrev_i32_e32 v137, 31, v136
	v_pk_mul_f32 v[124:125], v[124:125], v[126:127]
	v_add_u32_e32 v126, s5, v151
	v_lshlrev_b64 v[136:137], 10, v[136:137]
	v_ashrrev_i32_e32 v127, 31, v126
	v_lshl_add_u64 v[136:137], s[10:11], 0, v[136:137]
	v_cvt_pk_bf16_f32 v128, v122, v123
	v_lshlrev_b64 v[122:123], 1, v[126:127]
	v_cvt_pk_bf16_f32 v129, v124, v125
	v_lshl_add_u64 v[124:125], v[136:137], 0, v[122:123]
	global_store_dwordx2 v[124:125], v[128:129], off
	v_mul_f32_e32 v124, 0xbfb8aa3b, v118
	v_mul_f32_e32 v125, 0xbfb8aa3b, v119
	v_exp_f32_e32 v124, v124
	v_exp_f32_e32 v125, v125
	v_mul_f32_e32 v126, 0xbfb8aa3b, v120
	v_mul_f32_e32 v127, 0xbfb8aa3b, v121
	v_exp_f32_e32 v126, v126
	v_exp_f32_e32 v127, v127
	v_add_f32_e32 v124, 1.0, v124
	v_add_f32_e32 v125, 1.0, v125
	v_rcp_f32_e32 v124, v124
	v_rcp_f32_e32 v125, v125
	v_add_f32_e32 v126, 1.0, v126
	v_add_f32_e32 v127, 1.0, v127
	v_rcp_f32_e32 v126, v126
	v_rcp_f32_e32 v127, v127
	s_addk_i32 s4, 0x80
	s_lshr_b32 s5, s4, 31
	s_add_i32 s4, s4, s5
	v_pk_mul_f32 v[118:119], v[118:119], v[124:125]
	s_ashr_i32 s4, s4, 1
	v_pk_mul_f32 v[114:115], v[114:115], v[118:119]
	v_pk_mul_f32 v[118:119], v[120:121], v[126:127]
	v_cvt_pk_bf16_f32 v120, v114, v115
	v_pk_mul_f32 v[116:117], v[116:117], v[118:119]
	v_add_u32_e32 v118, s4, v151
	v_ashrrev_i32_e32 v119, 31, v118
	v_lshlrev_b64 v[114:115], 1, v[118:119]
	v_mul_f32_e32 v118, 0xbfb8aa3b, v110
	v_mul_f32_e32 v119, 0xbfb8aa3b, v111
	v_exp_f32_e32 v118, v118
	v_exp_f32_e32 v119, v119
	v_cvt_pk_bf16_f32 v121, v116, v117
	v_lshl_add_u64 v[116:117], v[136:137], 0, v[114:115]
	global_store_dwordx2 v[116:117], v[120:121], off
	v_add_f32_e32 v116, 1.0, v118
	v_add_f32_e32 v117, 1.0, v119
	v_mul_f32_e32 v118, 0xbfb8aa3b, v112
	v_mul_f32_e32 v119, 0xbfb8aa3b, v113
	v_exp_f32_e32 v118, v118
	v_exp_f32_e32 v119, v119
	v_rcp_f32_e32 v116, v116
	v_rcp_f32_e32 v117, v117
	v_add_f32_e32 v118, 1.0, v118
	v_add_f32_e32 v119, 1.0, v119
	v_rcp_f32_e32 v118, v118
	v_rcp_f32_e32 v119, v119
	v_pk_mul_f32 v[110:111], v[110:111], v[116:117]
	v_lshl_add_u64 v[120:121], v[136:137], 0, s[16:17]
	v_pk_mul_f32 v[106:107], v[106:107], v[110:111]
	v_pk_mul_f32 v[110:111], v[112:113], v[118:119]
	v_cvt_pk_bf16_f32 v106, v106, v107
	v_pk_mul_f32 v[108:109], v[108:109], v[110:111]
	v_mul_f32_e32 v112, 0xbfb8aa3b, v104
	v_cvt_pk_bf16_f32 v107, v108, v109
	v_mul_f32_e32 v108, 0xbfb8aa3b, v102
	v_exp_f32_e32 v110, v108
	v_mul_f32_e32 v108, 0xbfb8aa3b, v103
	v_exp_f32_e32 v111, v108
	v_mul_f32_e32 v113, 0xbfb8aa3b, v105
	v_exp_f32_e32 v112, v112
	v_exp_f32_e32 v113, v113
	v_add_f32_e32 v110, 1.0, v110
	v_add_f32_e32 v111, 1.0, v111
	v_rcp_f32_e32 v110, v110
	v_rcp_f32_e32 v111, v111
	v_add_f32_e32 v112, 1.0, v112
	v_add_f32_e32 v113, 1.0, v113
	v_rcp_f32_e32 v112, v112
	v_rcp_f32_e32 v113, v113
	v_pk_mul_f32 v[102:103], v[102:103], v[110:111]
	v_lshl_add_u64 v[108:109], v[120:121], 0, v[122:123]
	v_pk_mul_f32 v[98:99], v[98:99], v[102:103]
	v_pk_mul_f32 v[102:103], v[104:105], v[112:113]
	v_cvt_pk_bf16_f32 v98, v98, v99
	v_pk_mul_f32 v[100:101], v[100:101], v[102:103]
	v_mul_f32_e32 v102, 0xbfb8aa3b, v94
	v_cvt_pk_bf16_f32 v99, v100, v101
	v_lshl_add_u64 v[100:101], v[120:121], 0, v[114:115]
	v_mul_f32_e32 v103, 0xbfb8aa3b, v95
	global_store_dwordx2 v[108:109], v[106:107], off
	v_exp_f32_e32 v102, v102
	v_exp_f32_e32 v103, v103
	global_store_dwordx2 v[100:101], v[98:99], off
	v_mul_f32_e32 v100, 0xbfb8aa3b, v96
	v_mul_f32_e32 v101, 0xbfb8aa3b, v97
	v_exp_f32_e32 v100, v100
	v_exp_f32_e32 v101, v101
	v_add_f32_e32 v98, 1.0, v102
	v_add_f32_e32 v99, 1.0, v103
	v_rcp_f32_e32 v98, v98
	v_rcp_f32_e32 v99, v99
	v_add_f32_e32 v100, 1.0, v100
	v_add_f32_e32 v101, 1.0, v101
	v_rcp_f32_e32 v100, v100
	v_rcp_f32_e32 v101, v101
	v_pk_mul_f32 v[94:95], v[94:95], v[98:99]
	v_lshl_add_u64 v[102:103], v[136:137], 0, s[18:19]
	v_pk_mul_f32 v[90:91], v[90:91], v[94:95]
	v_pk_mul_f32 v[94:95], v[96:97], v[100:101]
	v_cvt_pk_bf16_f32 v90, v90, v91
	v_pk_mul_f32 v[92:93], v[92:93], v[94:95]
	v_mul_f32_e32 v96, 0xbfb8aa3b, v88
	v_cvt_pk_bf16_f32 v91, v92, v93
	v_mul_f32_e32 v92, 0xbfb8aa3b, v86
	v_exp_f32_e32 v94, v92
	v_mul_f32_e32 v92, 0xbfb8aa3b, v87
	v_exp_f32_e32 v95, v92
	v_mul_f32_e32 v97, 0xbfb8aa3b, v89
	v_exp_f32_e32 v96, v96
	v_exp_f32_e32 v97, v97
	v_add_f32_e32 v94, 1.0, v94
	v_add_f32_e32 v95, 1.0, v95
	v_rcp_f32_e32 v94, v94
	v_rcp_f32_e32 v95, v95
	v_add_f32_e32 v96, 1.0, v96
	v_add_f32_e32 v97, 1.0, v97
	v_rcp_f32_e32 v96, v96
	v_rcp_f32_e32 v97, v97
	v_pk_mul_f32 v[86:87], v[86:87], v[94:95]
	v_lshl_add_u64 v[92:93], v[102:103], 0, v[122:123]
	v_pk_mul_f32 v[82:83], v[82:83], v[86:87]
	v_pk_mul_f32 v[86:87], v[88:89], v[96:97]
	v_cvt_pk_bf16_f32 v82, v82, v83
	v_pk_mul_f32 v[84:85], v[84:85], v[86:87]
	v_mul_f32_e32 v86, 0xbfb8aa3b, v78
	v_cvt_pk_bf16_f32 v83, v84, v85
	v_lshl_add_u64 v[84:85], v[102:103], 0, v[114:115]
	v_mul_f32_e32 v87, 0xbfb8aa3b, v79
	global_store_dwordx2 v[92:93], v[90:91], off
	v_exp_f32_e32 v86, v86
	v_exp_f32_e32 v87, v87
	global_store_dwordx2 v[84:85], v[82:83], off
	v_mul_f32_e32 v84, 0xbfb8aa3b, v80
	v_mul_f32_e32 v85, 0xbfb8aa3b, v81
	v_exp_f32_e32 v84, v84
	v_exp_f32_e32 v85, v85
	v_add_f32_e32 v82, 1.0, v86
	v_add_f32_e32 v83, 1.0, v87
	v_rcp_f32_e32 v82, v82
	v_rcp_f32_e32 v83, v83
	v_add_f32_e32 v84, 1.0, v84
	v_add_f32_e32 v85, 1.0, v85
	v_rcp_f32_e32 v84, v84
	v_rcp_f32_e32 v85, v85
	v_pk_mul_f32 v[78:79], v[78:79], v[82:83]
	v_lshl_add_u64 v[86:87], v[136:137], 0, s[20:21]
	v_pk_mul_f32 v[74:75], v[74:75], v[78:79]
	v_pk_mul_f32 v[78:79], v[80:81], v[84:85]
	v_cvt_pk_bf16_f32 v74, v74, v75
	v_pk_mul_f32 v[76:77], v[76:77], v[78:79]
	v_mul_f32_e32 v80, 0xbfb8aa3b, v72
	v_cvt_pk_bf16_f32 v75, v76, v77
	v_mul_f32_e32 v76, 0xbfb8aa3b, v70
	v_exp_f32_e32 v78, v76
	v_mul_f32_e32 v76, 0xbfb8aa3b, v71
	v_exp_f32_e32 v79, v76
	v_mul_f32_e32 v81, 0xbfb8aa3b, v73
	v_exp_f32_e32 v80, v80
	v_exp_f32_e32 v81, v81
	v_add_f32_e32 v78, 1.0, v78
	v_add_f32_e32 v79, 1.0, v79
	v_rcp_f32_e32 v78, v78
	v_rcp_f32_e32 v79, v79
	v_add_f32_e32 v80, 1.0, v80
	v_add_f32_e32 v81, 1.0, v81
	v_rcp_f32_e32 v80, v80
	v_rcp_f32_e32 v81, v81
	v_pk_mul_f32 v[70:71], v[70:71], v[78:79]
	v_lshl_add_u64 v[76:77], v[86:87], 0, v[122:123]
	v_pk_mul_f32 v[66:67], v[66:67], v[70:71]
	v_pk_mul_f32 v[70:71], v[72:73], v[80:81]
	v_cvt_pk_bf16_f32 v66, v66, v67
	v_pk_mul_f32 v[68:69], v[68:69], v[70:71]
	v_mul_f32_e32 v70, 0xbfb8aa3b, v62
	v_cvt_pk_bf16_f32 v67, v68, v69
	v_lshl_add_u64 v[68:69], v[86:87], 0, v[114:115]
	v_mul_f32_e32 v71, 0xbfb8aa3b, v63
	global_store_dwordx2 v[76:77], v[74:75], off
	v_exp_f32_e32 v70, v70
	v_exp_f32_e32 v71, v71
	global_store_dwordx2 v[68:69], v[66:67], off
	v_mul_f32_e32 v68, 0xbfb8aa3b, v64
	v_mul_f32_e32 v69, 0xbfb8aa3b, v65
	v_exp_f32_e32 v68, v68
	v_exp_f32_e32 v69, v69
	v_add_f32_e32 v66, 1.0, v70
	v_add_f32_e32 v67, 1.0, v71
	v_rcp_f32_e32 v66, v66
	v_rcp_f32_e32 v67, v67
	v_add_f32_e32 v68, 1.0, v68
	v_add_f32_e32 v69, 1.0, v69
	v_rcp_f32_e32 v68, v68
	v_rcp_f32_e32 v69, v69
	v_pk_mul_f32 v[62:63], v[62:63], v[66:67]
	v_lshl_add_u64 v[70:71], v[136:137], 0, s[22:23]
	v_pk_mul_f32 v[58:59], v[58:59], v[62:63]
	v_pk_mul_f32 v[62:63], v[64:65], v[68:69]
	v_cvt_pk_bf16_f32 v58, v58, v59
	v_pk_mul_f32 v[60:61], v[60:61], v[62:63]
	v_mul_f32_e32 v64, 0xbfb8aa3b, v56
	v_cvt_pk_bf16_f32 v59, v60, v61
	v_mul_f32_e32 v60, 0xbfb8aa3b, v54
	v_exp_f32_e32 v62, v60
	v_mul_f32_e32 v60, 0xbfb8aa3b, v55
	v_exp_f32_e32 v63, v60
	v_mul_f32_e32 v65, 0xbfb8aa3b, v57
	v_exp_f32_e32 v64, v64
	v_exp_f32_e32 v65, v65
	v_add_f32_e32 v62, 1.0, v62
	v_add_f32_e32 v63, 1.0, v63
	v_rcp_f32_e32 v62, v62
	v_rcp_f32_e32 v63, v63
	v_add_f32_e32 v64, 1.0, v64
	v_add_f32_e32 v65, 1.0, v65
	v_rcp_f32_e32 v64, v64
	v_rcp_f32_e32 v65, v65
	v_pk_mul_f32 v[54:55], v[54:55], v[62:63]
	v_lshl_add_u64 v[60:61], v[70:71], 0, v[122:123]
	v_pk_mul_f32 v[50:51], v[50:51], v[54:55]
	v_pk_mul_f32 v[54:55], v[56:57], v[64:65]
	v_cvt_pk_bf16_f32 v50, v50, v51
	v_pk_mul_f32 v[52:53], v[52:53], v[54:55]
	v_mul_f32_e32 v54, 0xbfb8aa3b, v46
	v_cvt_pk_bf16_f32 v51, v52, v53
	v_lshl_add_u64 v[52:53], v[70:71], 0, v[114:115]
	v_mul_f32_e32 v55, 0xbfb8aa3b, v47
	global_store_dwordx2 v[60:61], v[58:59], off
	v_exp_f32_e32 v54, v54
	v_exp_f32_e32 v55, v55
	global_store_dwordx2 v[52:53], v[50:51], off
	v_mul_f32_e32 v52, 0xbfb8aa3b, v48
	v_mul_f32_e32 v53, 0xbfb8aa3b, v49
	v_exp_f32_e32 v52, v52
	v_exp_f32_e32 v53, v53
	v_add_f32_e32 v50, 1.0, v54
	v_add_f32_e32 v51, 1.0, v55
	v_rcp_f32_e32 v50, v50
	v_rcp_f32_e32 v51, v51
	v_add_f32_e32 v52, 1.0, v52
	v_add_f32_e32 v53, 1.0, v53
	v_rcp_f32_e32 v52, v52
	v_rcp_f32_e32 v53, v53
	v_pk_mul_f32 v[46:47], v[46:47], v[50:51]
	v_lshl_add_u64 v[54:55], v[136:137], 0, s[24:25]
	v_pk_mul_f32 v[42:43], v[42:43], v[46:47]
	v_pk_mul_f32 v[46:47], v[48:49], v[52:53]
	v_cvt_pk_bf16_f32 v42, v42, v43
	v_pk_mul_f32 v[44:45], v[44:45], v[46:47]
	v_mul_f32_e32 v48, 0xbfb8aa3b, v32
	v_cvt_pk_bf16_f32 v43, v44, v45
	v_mul_f32_e32 v44, 0xbfb8aa3b, v30
	v_exp_f32_e32 v46, v44
	v_mul_f32_e32 v44, 0xbfb8aa3b, v31
	v_exp_f32_e32 v47, v44
	v_mul_f32_e32 v49, 0xbfb8aa3b, v33
	v_exp_f32_e32 v48, v48
	v_exp_f32_e32 v49, v49
	v_add_f32_e32 v46, 1.0, v46
	v_add_f32_e32 v47, 1.0, v47
	v_rcp_f32_e32 v46, v46
	v_rcp_f32_e32 v47, v47
	v_add_f32_e32 v48, 1.0, v48
	v_add_f32_e32 v49, 1.0, v49
	v_rcp_f32_e32 v48, v48
	v_rcp_f32_e32 v49, v49
	v_pk_mul_f32 v[30:31], v[30:31], v[46:47]
	v_lshl_add_u64 v[44:45], v[54:55], 0, v[122:123]
	v_pk_mul_f32 v[26:27], v[26:27], v[30:31]
	v_pk_mul_f32 v[30:31], v[32:33], v[48:49]
	v_cvt_pk_bf16_f32 v26, v26, v27
	v_pk_mul_f32 v[28:29], v[28:29], v[30:31]
	v_mul_f32_e32 v30, 0xbfb8aa3b, v22
	v_cvt_pk_bf16_f32 v27, v28, v29
	v_lshl_add_u64 v[28:29], v[54:55], 0, v[114:115]
	v_mul_f32_e32 v31, 0xbfb8aa3b, v23
	global_store_dwordx2 v[44:45], v[42:43], off
	v_exp_f32_e32 v30, v30
	v_exp_f32_e32 v31, v31
	global_store_dwordx2 v[28:29], v[26:27], off
	v_mul_f32_e32 v28, 0xbfb8aa3b, v24
	v_mul_f32_e32 v29, 0xbfb8aa3b, v25
	v_exp_f32_e32 v28, v28
	v_exp_f32_e32 v29, v29
	v_add_f32_e32 v26, 1.0, v30
	v_add_f32_e32 v27, 1.0, v31
	v_rcp_f32_e32 v26, v26
	v_rcp_f32_e32 v27, v27
	v_add_f32_e32 v28, 1.0, v28
	v_add_f32_e32 v29, 1.0, v29
	v_rcp_f32_e32 v28, v28
	v_rcp_f32_e32 v29, v29
	v_pk_mul_f32 v[22:23], v[22:23], v[26:27]
	v_lshl_add_u64 v[30:31], v[136:137], 0, s[26:27]
	v_pk_mul_f32 v[18:19], v[18:19], v[22:23]
	v_pk_mul_f32 v[22:23], v[24:25], v[28:29]
	v_cvt_pk_bf16_f32 v18, v18, v19
	v_pk_mul_f32 v[20:21], v[20:21], v[22:23]
	v_mul_f32_e32 v24, 0xbfb8aa3b, v36
	v_cvt_pk_bf16_f32 v19, v20, v21
	v_mul_f32_e32 v20, 0xbfb8aa3b, v34
	v_exp_f32_e32 v22, v20
	v_mul_f32_e32 v20, 0xbfb8aa3b, v35
	v_mul_f32_e32 v25, 0xbfb8aa3b, v37
	v_exp_f32_e32 v23, v20
	v_exp_f32_e32 v24, v24
	v_exp_f32_e32 v25, v25
	v_add_f32_e32 v22, 1.0, v22
	v_add_f32_e32 v23, 1.0, v23
	v_add_f32_e32 v24, 1.0, v24
	v_add_f32_e32 v25, 1.0, v25
	v_rcp_f32_e32 v22, v22
	v_rcp_f32_e32 v23, v23
	v_rcp_f32_e32 v24, v24
	v_rcp_f32_e32 v25, v25
	v_lshl_add_u64 v[20:21], v[30:31], 0, v[122:123]
	global_store_dwordx2 v[20:21], v[18:19], off
	v_pk_mul_f32 v[18:19], v[34:35], v[22:23]
	v_pk_mul_f32 v[20:21], v[36:37], v[24:25]
	v_pk_mul_f32 v[18:19], v[38:39], v[18:19]
	v_pk_mul_f32 v[20:21], v[40:41], v[20:21]
	v_cvt_pk_bf16_f32 v18, v18, v19
	v_cvt_pk_bf16_f32 v19, v20, v21
	v_lshl_add_u64 v[20:21], v[30:31], 0, v[114:115]
	v_mul_f32_e32 v22, 0xbfb8aa3b, v6
	v_mul_f32_e32 v23, 0xbfb8aa3b, v7
	v_exp_f32_e32 v22, v22
	v_exp_f32_e32 v23, v23
	global_store_dwordx2 v[20:21], v[18:19], off
	v_mul_f32_e32 v20, 0xbfb8aa3b, v8
	v_mul_f32_e32 v21, 0xbfb8aa3b, v9
	v_exp_f32_e32 v20, v20
	v_exp_f32_e32 v21, v21
	v_add_f32_e32 v18, 1.0, v22
	v_add_f32_e32 v19, 1.0, v23
	v_rcp_f32_e32 v18, v18
	v_rcp_f32_e32 v19, v19
	v_add_f32_e32 v20, 1.0, v20
	v_add_f32_e32 v21, 1.0, v21
	v_rcp_f32_e32 v20, v20
	v_rcp_f32_e32 v21, v21
	v_pk_mul_f32 v[6:7], v[6:7], v[18:19]
	v_lshl_add_u64 v[22:23], v[136:137], 0, s[28:29]
	v_pk_mul_f32 v[2:3], v[2:3], v[6:7]
	v_pk_mul_f32 v[6:7], v[8:9], v[20:21]
	v_cvt_pk_bf16_f32 v2, v2, v3
	v_pk_mul_f32 v[4:5], v[4:5], v[6:7]
	v_mul_f32_e32 v8, 0xbfb8aa3b, v12
	v_cvt_pk_bf16_f32 v3, v4, v5
	v_mul_f32_e32 v4, 0xbfb8aa3b, v10
	v_exp_f32_e32 v6, v4
	v_mul_f32_e32 v4, 0xbfb8aa3b, v11
	v_mul_f32_e32 v9, 0xbfb8aa3b, v13
	v_exp_f32_e32 v7, v4
	v_exp_f32_e32 v8, v8
	v_exp_f32_e32 v9, v9
	v_add_f32_e32 v6, 1.0, v6
	v_add_f32_e32 v7, 1.0, v7
	v_add_f32_e32 v8, 1.0, v8
	v_add_f32_e32 v9, 1.0, v9
	v_rcp_f32_e32 v6, v6
	v_rcp_f32_e32 v7, v7
	v_rcp_f32_e32 v8, v8
	v_rcp_f32_e32 v9, v9
	v_lshl_add_u64 v[4:5], v[22:23], 0, v[122:123]
	global_store_dwordx2 v[4:5], v[2:3], off
	v_pk_mul_f32 v[2:3], v[10:11], v[6:7]
	v_pk_mul_f32 v[4:5], v[12:13], v[8:9]
	v_pk_mul_f32 v[2:3], v[14:15], v[2:3]
	v_pk_mul_f32 v[4:5], v[16:17], v[4:5]
	v_cvt_pk_bf16_f32 v2, v2, v3
	v_cvt_pk_bf16_f32 v3, v4, v5
	v_lshl_add_u64 v[4:5], v[22:23], 0, v[114:115]
	s_and_b64 vcc, exec, s[0:1]
	v_mov_b32_e32 v138, v156
	v_mov_b32_e32 v158, v154
	v_mov_b32_e32 v140, v157
	v_mov_b32_e32 v136, v155
	s_mov_b32 s82, s80
	s_mov_b32 s83, s81
	s_mov_b64 s[36:37], s[34:35]
	global_store_dwordx2 v[4:5], v[2:3], off
	s_cbranch_vccz .LBB0_2145
	s_waitcnt vmcnt(0)
	v_readlane_b32 s72, v255, 2
	s_cmpk_gt_u32 s40, 0xff
	v_readlane_b32 s73, v255, 3
	v_readlane_b32 s71, v255, 4
	s_cbranch_scc1 .LBB0_2154
	s_barrier

.LBB0_2223:
	s_add_u32 s36, s54, s4
	s_addc_u32 s37, s55, s5
	s_add_u32 s38, s36, 0x29400100
	ds_read_b128 v[162:165], v153
	ds_read_b128 v[166:169], v153 offset:1024
	ds_read_b128 v[170:173], v153 offset:2048
	ds_read_b128 v[174:177], v153 offset:3072
	s_addc_u32 s39, s37, 0
	s_add_u32 s89, s86, s4
	s_addc_u32 s90, s87, s5
	s_cmpk_eq_i32 s4, 0x300
	s_cselect_b64 vcc, -1, 0
	s_and_b64 s[36:37], vcc, exec
	v_cndmask_b32_e32 v134, v156, v157, vcc
	s_cselect_b32 s39, s9, s39
	s_cselect_b32 s38, s8, s38
	v_cndmask_b32_e32 v139, v138, v158, vcc
	v_cndmask_b32_e32 v226, v136, v159, vcc
	v_cndmask_b32_e32 v141, v140, v160, vcc
	s_cselect_b32 s37, s31, s90
	s_cselect_b32 s36, s85, s89
	v_lshl_add_u64 v[210:211], v[144:145], 0, s[4:5]
	s_add_i32 m0, s44, 0xc000
	ds_read_b128 v[178:181], v154
	ds_read_b128 v[182:185], v154 offset:1024
	ds_read_b128 v[186:189], v154 offset:2048
	ds_read_b128 v[190:193], v154 offset:3072
	ds_read_b128 v[194:197], v154 offset:4096
	ds_read_b128 v[198:201], v154 offset:5120
	ds_read_b128 v[202:205], v154 offset:6144
	ds_read_b128 v[206:209], v154 offset:7168
	global_load_lds_dwordx4 v[210:211], off
	v_lshl_add_u64 v[210:211], v[142:143], 0, s[4:5]
	s_add_i32 m0, s44, 0xe000
	s_nop 0
	global_load_lds_dwordx4 v[210:211], off
	s_waitcnt lgkmcnt(8)
	s_barrier
	s_waitcnt lgkmcnt(0)
	s_nop 0
	s_waitcnt lgkmcnt(0)
	v_mfma_f32_16x16x32_bf16 v[126:129], v[162:165], v[178:181], v[126:129]
	v_mfma_f32_16x16x32_bf16 v[122:125], v[170:173], v[178:181], v[122:125]
	v_mfma_f32_16x16x32_bf16 v[118:121], v[162:165], v[186:189], v[118:121]
	v_mfma_f32_16x16x32_bf16 v[114:117], v[170:173], v[186:189], v[114:117]
	v_mfma_f32_16x16x32_bf16 v[110:113], v[162:165], v[194:197], v[110:113]
	v_mfma_f32_16x16x32_bf16 v[106:109], v[170:173], v[194:197], v[106:109]
	v_mfma_f32_16x16x32_bf16 v[102:105], v[162:165], v[202:205], v[102:105]
	v_mfma_f32_16x16x32_bf16 v[98:101], v[170:173], v[202:205], v[98:101]
	v_mfma_f32_16x16x32_bf16 v[126:129], v[166:169], v[182:185], v[126:129]
	v_mfma_f32_16x16x32_bf16 v[122:125], v[174:177], v[182:185], v[122:125]
	v_mfma_f32_16x16x32_bf16 v[118:121], v[166:169], v[190:193], v[118:121]
	v_mfma_f32_16x16x32_bf16 v[114:117], v[174:177], v[190:193], v[114:117]
	v_mfma_f32_16x16x32_bf16 v[110:113], v[166:169], v[198:201], v[110:113]
	v_mfma_f32_16x16x32_bf16 v[106:109], v[174:177], v[198:201], v[106:109]
	v_mfma_f32_16x16x32_bf16 v[102:105], v[166:169], v[206:209], v[102:105]
	v_mfma_f32_16x16x32_bf16 v[98:101], v[174:177], v[206:209], v[98:101]
	s_nop 0
	s_barrier
	s_add_i32 s89, s73, s41
	v_lshl_add_u64 v[228:229], s[36:37], 0, v[132:133]
	s_mov_b32 m0, s89
	ds_read_b128 v[210:213], v155
	ds_read_b128 v[214:217], v155 offset:1024
	ds_read_b128 v[218:221], v155 offset:2048
	ds_read_b128 v[222:225], v155 offset:3072
	global_load_lds_dwordx4 v[228:229], off
	v_lshl_add_u64 v[230:231], s[36:37], 0, v[130:131]
	s_add_i32 m0, s89, 0x2000
	s_nop 0
	global_load_lds_dwordx4 v[230:231], off
	s_barrier
	s_waitcnt lgkmcnt(0)
	s_nop 0
	s_waitcnt lgkmcnt(0)
	v_mfma_f32_16x16x32_bf16 v[86:89], v[210:213], v[178:181], v[86:89]
	v_mfma_f32_16x16x32_bf16 v[78:81], v[218:221], v[178:181], v[78:81]
	v_mfma_f32_16x16x32_bf16 v[70:73], v[210:213], v[186:189], v[70:73]
	v_mfma_f32_16x16x32_bf16 v[62:65], v[218:221], v[186:189], v[62:65]
	v_mfma_f32_16x16x32_bf16 v[38:41], v[210:213], v[194:197], v[38:41]
	v_mfma_f32_16x16x32_bf16 v[34:37], v[218:221], v[194:197], v[34:37]
	v_mfma_f32_16x16x32_bf16 v[26:29], v[210:213], v[202:205], v[26:29]
	v_mfma_f32_16x16x32_bf16 v[18:21], v[218:221], v[202:205], v[18:21]
	v_mfma_f32_16x16x32_bf16 v[86:89], v[214:217], v[182:185], v[86:89]
	v_mfma_f32_16x16x32_bf16 v[78:81], v[222:225], v[182:185], v[78:81]
	v_mfma_f32_16x16x32_bf16 v[70:73], v[214:217], v[190:193], v[70:73]
	v_mfma_f32_16x16x32_bf16 v[62:65], v[222:225], v[190:193], v[62:65]
	v_mfma_f32_16x16x32_bf16 v[38:41], v[214:217], v[198:201], v[38:41]
	v_mfma_f32_16x16x32_bf16 v[34:37], v[222:225], v[198:201], v[34:37]
	v_mfma_f32_16x16x32_bf16 v[26:29], v[214:217], v[206:209], v[26:29]
	v_mfma_f32_16x16x32_bf16 v[18:21], v[222:225], v[206:209], v[18:21]
	s_nop 0
	s_mov_b32 m0, s44
	s_barrier
	ds_read_b128 v[178:181], v154 offset:16384
	ds_read_b128 v[182:185], v154 offset:17408
	ds_read_b128 v[186:189], v154 offset:18432
	ds_read_b128 v[190:193], v154 offset:19456
	ds_read_b128 v[194:197], v154 offset:20480
	ds_read_b128 v[198:201], v154 offset:21504
	ds_read_b128 v[202:205], v154 offset:22528
	ds_read_b128 v[206:209], v154 offset:23552
	global_load_lds_dwordx4 v134, s[38:39]
	s_mov_b32 m0, s45
	v_mov_b32_e32 v227, v135
	global_load_lds_dwordx4 v226, s[38:39]
	s_barrier
	s_waitcnt lgkmcnt(0)
	v_lshl_add_u64 v[232:233], s[38:39], 0, v[134:135]
	v_lshl_add_u64 v[226:227], s[38:39], 0, v[226:227]
	s_nop 0
	s_waitcnt lgkmcnt(0)
	v_mfma_f32_16x16x32_bf16 v[94:97], v[162:165], v[178:181], v[94:97]
	v_mfma_f32_16x16x32_bf16 v[90:93], v[170:173], v[178:181], v[90:93]
	v_mfma_f32_16x16x32_bf16 v[82:85], v[162:165], v[186:189], v[82:85]
	v_mfma_f32_16x16x32_bf16 v[74:77], v[170:173], v[186:189], v[74:77]
	v_mfma_f32_16x16x32_bf16 v[46:49], v[162:165], v[194:197], v[46:49]
	v_mfma_f32_16x16x32_bf16 v[42:45], v[170:173], v[194:197], v[42:45]
	v_mfma_f32_16x16x32_bf16 v[30:33], v[162:165], v[202:205], v[30:33]
	v_mfma_f32_16x16x32_bf16 v[22:25], v[170:173], v[202:205], v[22:25]
	v_mfma_f32_16x16x32_bf16 v[94:97], v[166:169], v[182:185], v[94:97]
	v_mfma_f32_16x16x32_bf16 v[90:93], v[174:177], v[182:185], v[90:93]
	v_mfma_f32_16x16x32_bf16 v[82:85], v[166:169], v[190:193], v[82:85]
	v_mfma_f32_16x16x32_bf16 v[74:77], v[174:177], v[190:193], v[74:77]
	v_mfma_f32_16x16x32_bf16 v[46:49], v[166:169], v[198:201], v[46:49]
	v_mfma_f32_16x16x32_bf16 v[42:45], v[174:177], v[198:201], v[42:45]
	v_mfma_f32_16x16x32_bf16 v[30:33], v[166:169], v[206:209], v[30:33]
	v_mfma_f32_16x16x32_bf16 v[22:25], v[174:177], v[206:209], v[22:25]
	s_nop 0
	s_barrier
	s_add_u32 s90, s36, 0x20000
	s_addc_u32 s91, s37, 0
	s_add_i32 s89, s74, s41
	v_lshl_add_u64 v[162:163], s[90:91], 0, v[132:133]
	s_mov_b32 m0, s89
	s_nop 0
	global_load_lds_dwordx4 v[162:163], off
	v_lshl_add_u64 v[162:163], s[90:91], 0, v[130:131]
	s_add_i32 m0, s89, 0x2000
	s_nop 0
	global_load_lds_dwordx4 v[162:163], off
	s_waitcnt vmcnt(6)
	s_barrier
	s_nop 0
	v_mfma_f32_16x16x32_bf16 v[14:17], v[210:213], v[178:181], v[14:17]
	v_mfma_f32_16x16x32_bf16 v[10:13], v[218:221], v[178:181], v[10:13]
	v_mfma_f32_16x16x32_bf16 v[6:9], v[210:213], v[186:189], v[6:9]
	v_mfma_f32_16x16x32_bf16 v[2:5], v[218:221], v[186:189], v[2:5]
	v_mfma_f32_16x16x32_bf16 v[54:57], v[210:213], v[194:197], v[54:57]
	v_mfma_f32_16x16x32_bf16 v[66:69], v[218:221], v[194:197], v[66:69]
	v_mfma_f32_16x16x32_bf16 v[50:53], v[210:213], v[202:205], v[50:53]
	v_mfma_f32_16x16x32_bf16 v[58:61], v[218:221], v[202:205], v[58:61]
	v_mfma_f32_16x16x32_bf16 v[14:17], v[214:217], v[182:185], v[14:17]
	v_mfma_f32_16x16x32_bf16 v[10:13], v[222:225], v[182:185], v[10:13]
	v_mfma_f32_16x16x32_bf16 v[6:9], v[214:217], v[190:193], v[6:9]
	v_mfma_f32_16x16x32_bf16 v[2:5], v[222:225], v[190:193], v[2:5]
	v_mfma_f32_16x16x32_bf16 v[54:57], v[214:217], v[198:201], v[54:57]
	v_mfma_f32_16x16x32_bf16 v[66:69], v[222:225], v[198:201], v[66:69]
	v_mfma_f32_16x16x32_bf16 v[50:53], v[214:217], v[206:209], v[50:53]
	v_mfma_f32_16x16x32_bf16 v[58:61], v[222:225], v[206:209], v[58:61]
	s_nop 0
	s_add_i32 s89, 0, 0x18000
	v_add_u32_e32 v134, s89, v150
	s_barrier
	ds_read_b128 v[162:165], v134
	ds_read_b128 v[166:169], v134 offset:1024
	ds_read_b128 v[170:173], v134 offset:2048
	ds_read_b128 v[174:177], v134 offset:3072
	s_mov_b32 m0, s46
	ds_read_b128 v[178:181], v154 offset:32768
	ds_read_b128 v[182:185], v154 offset:33792
	ds_read_b128 v[186:189], v154 offset:34816
	ds_read_b128 v[190:193], v154 offset:35840
	ds_read_b128 v[194:197], v154 offset:36864
	ds_read_b128 v[198:201], v154 offset:37888
	ds_read_b128 v[202:205], v154 offset:38912
	ds_read_b128 v[206:209], v154 offset:39936
	global_load_lds_dwordx4 v139, s[38:39]
	s_mov_b32 m0, s47
	s_nop 0
	global_load_lds_dwordx4 v141, s[38:39]
	s_waitcnt lgkmcnt(8)
	s_barrier
	s_waitcnt lgkmcnt(0)
	s_nop 0
	s_waitcnt lgkmcnt(0)
	v_mfma_f32_16x16x32_bf16 v[126:129], v[162:165], v[178:181], v[126:129]
	v_mfma_f32_16x16x32_bf16 v[122:125], v[170:173], v[178:181], v[122:125]
	v_mfma_f32_16x16x32_bf16 v[118:121], v[162:165], v[186:189], v[118:121]
	v_mfma_f32_16x16x32_bf16 v[114:117], v[170:173], v[186:189], v[114:117]
	v_mfma_f32_16x16x32_bf16 v[110:113], v[162:165], v[194:197], v[110:113]
	v_mfma_f32_16x16x32_bf16 v[106:109], v[170:173], v[194:197], v[106:109]
	v_mfma_f32_16x16x32_bf16 v[102:105], v[162:165], v[202:205], v[102:105]
	v_mfma_f32_16x16x32_bf16 v[98:101], v[170:173], v[202:205], v[98:101]
	v_mfma_f32_16x16x32_bf16 v[126:129], v[166:169], v[182:185], v[126:129]
	v_mfma_f32_16x16x32_bf16 v[122:125], v[174:177], v[182:185], v[122:125]
	v_mfma_f32_16x16x32_bf16 v[118:121], v[166:169], v[190:193], v[118:121]
	v_mfma_f32_16x16x32_bf16 v[114:117], v[174:177], v[190:193], v[114:117]
	v_mfma_f32_16x16x32_bf16 v[110:113], v[166:169], v[198:201], v[110:113]
	v_mfma_f32_16x16x32_bf16 v[106:109], v[174:177], v[198:201], v[106:109]
	v_mfma_f32_16x16x32_bf16 v[102:105], v[166:169], v[206:209], v[102:105]
	v_mfma_f32_16x16x32_bf16 v[98:101], v[174:177], v[206:209], v[98:101]
	s_nop 0
	s_barrier
	s_add_i32 s38, 0, 0x1c000
	s_add_i32 s39, s89, s41
	v_add_u32_e32 v134, s38, v150
	v_lshl_add_u64 v[228:229], v[228:229], 0, s[14:15]
	s_mov_b32 m0, s39
	ds_read_b128 v[210:213], v134
	ds_read_b128 v[214:217], v134 offset:1024
	ds_read_b128 v[218:221], v134 offset:2048
	ds_read_b128 v[222:225], v134 offset:3072
	global_load_lds_dwordx4 v[228:229], off
	v_lshl_add_u64 v[228:229], v[230:231], 0, s[14:15]
	s_add_i32 m0, s39, 0x2000
	s_nop 0
	global_load_lds_dwordx4 v[228:229], off
	s_barrier
	s_waitcnt lgkmcnt(0)
	s_nop 0
	s_waitcnt lgkmcnt(0)
	v_mfma_f32_16x16x32_bf16 v[86:89], v[210:213], v[178:181], v[86:89]
	v_mfma_f32_16x16x32_bf16 v[78:81], v[218:221], v[178:181], v[78:81]
	v_mfma_f32_16x16x32_bf16 v[70:73], v[210:213], v[186:189], v[70:73]
	v_mfma_f32_16x16x32_bf16 v[62:65], v[218:221], v[186:189], v[62:65]
	v_mfma_f32_16x16x32_bf16 v[38:41], v[210:213], v[194:197], v[38:41]
	v_mfma_f32_16x16x32_bf16 v[34:37], v[218:221], v[194:197], v[34:37]
	v_mfma_f32_16x16x32_bf16 v[26:29], v[210:213], v[202:205], v[26:29]
	v_mfma_f32_16x16x32_bf16 v[18:21], v[218:221], v[202:205], v[18:21]
	v_mfma_f32_16x16x32_bf16 v[86:89], v[214:217], v[182:185], v[86:89]
	v_mfma_f32_16x16x32_bf16 v[78:81], v[222:225], v[182:185], v[78:81]
	v_mfma_f32_16x16x32_bf16 v[70:73], v[214:217], v[190:193], v[70:73]
	v_mfma_f32_16x16x32_bf16 v[62:65], v[222:225], v[190:193], v[62:65]
	v_mfma_f32_16x16x32_bf16 v[38:41], v[214:217], v[198:201], v[38:41]
	v_mfma_f32_16x16x32_bf16 v[34:37], v[222:225], v[198:201], v[34:37]
	v_mfma_f32_16x16x32_bf16 v[26:29], v[214:217], v[206:209], v[26:29]
	v_mfma_f32_16x16x32_bf16 v[18:21], v[222:225], v[206:209], v[18:21]
	s_nop 0
	s_mov_b32 m0, s49
	v_lshl_add_u64 v[228:229], v[232:233], 0, s[14:15]
	s_barrier
	ds_read_b128 v[178:181], v154 offset:49152
	ds_read_b128 v[182:185], v154 offset:50176
	ds_read_b128 v[186:189], v154 offset:51200
	ds_read_b128 v[190:193], v154 offset:52224
	ds_read_b128 v[194:197], v154 offset:53248
	ds_read_b128 v[198:201], v154 offset:54272
	ds_read_b128 v[202:205], v154 offset:55296
	ds_read_b128 v[206:209], v154 offset:56320
	global_load_lds_dwordx4 v[228:229], off
	v_lshl_add_u64 v[226:227], v[226:227], 0, s[14:15]
	s_mov_b32 m0, s50
	s_nop 0
	global_load_lds_dwordx4 v[226:227], off
	s_barrier
	s_waitcnt lgkmcnt(0)
	s_nop 0
	s_waitcnt lgkmcnt(0)
	v_mfma_f32_16x16x32_bf16 v[94:97], v[162:165], v[178:181], v[94:97]
	v_mfma_f32_16x16x32_bf16 v[90:93], v[170:173], v[178:181], v[90:93]
	v_mfma_f32_16x16x32_bf16 v[82:85], v[162:165], v[186:189], v[82:85]
	v_mfma_f32_16x16x32_bf16 v[74:77], v[170:173], v[186:189], v[74:77]
	v_mfma_f32_16x16x32_bf16 v[46:49], v[162:165], v[194:197], v[46:49]
	v_mfma_f32_16x16x32_bf16 v[42:45], v[170:173], v[194:197], v[42:45]
	v_mfma_f32_16x16x32_bf16 v[30:33], v[162:165], v[202:205], v[30:33]
	v_mfma_f32_16x16x32_bf16 v[22:25], v[170:173], v[202:205], v[22:25]
	v_mfma_f32_16x16x32_bf16 v[94:97], v[166:169], v[182:185], v[94:97]
	v_mfma_f32_16x16x32_bf16 v[90:93], v[174:177], v[182:185], v[90:93]
	v_mfma_f32_16x16x32_bf16 v[82:85], v[166:169], v[190:193], v[82:85]
	v_mfma_f32_16x16x32_bf16 v[74:77], v[174:177], v[190:193], v[74:77]
	v_mfma_f32_16x16x32_bf16 v[46:49], v[166:169], v[198:201], v[46:49]
	v_mfma_f32_16x16x32_bf16 v[42:45], v[174:177], v[198:201], v[42:45]
	v_mfma_f32_16x16x32_bf16 v[30:33], v[166:169], v[206:209], v[30:33]
	v_mfma_f32_16x16x32_bf16 v[22:25], v[174:177], v[206:209], v[22:25]
	s_nop 0
	s_barrier
	s_add_u32 s36, s36, 0x20080
	s_addc_u32 s37, s37, 0
	s_add_i32 s38, s38, s41
	v_lshl_add_u64 v[162:163], s[36:37], 0, v[132:133]
	s_mov_b32 m0, s38
	s_nop 0
	global_load_lds_dwordx4 v[162:163], off
	v_lshl_add_u64 v[162:163], s[36:37], 0, v[130:131]
	s_add_i32 m0, s38, 0x2000
	s_nop 0
	global_load_lds_dwordx4 v[162:163], off
	s_waitcnt vmcnt(6)
	s_barrier
	s_nop 0
	v_mfma_f32_16x16x32_bf16 v[14:17], v[210:213], v[178:181], v[14:17]
	v_mfma_f32_16x16x32_bf16 v[10:13], v[218:221], v[178:181], v[10:13]
	v_mfma_f32_16x16x32_bf16 v[6:9], v[210:213], v[186:189], v[6:9]
	v_mfma_f32_16x16x32_bf16 v[2:5], v[218:221], v[186:189], v[2:5]
	v_mfma_f32_16x16x32_bf16 v[54:57], v[210:213], v[194:197], v[54:57]
	v_mfma_f32_16x16x32_bf16 v[66:69], v[218:221], v[194:197], v[66:69]
	v_mfma_f32_16x16x32_bf16 v[50:53], v[210:213], v[202:205], v[50:53]
	v_mfma_f32_16x16x32_bf16 v[58:61], v[218:221], v[202:205], v[58:61]
	v_mfma_f32_16x16x32_bf16 v[14:17], v[214:217], v[182:185], v[14:17]
	v_mfma_f32_16x16x32_bf16 v[10:13], v[222:225], v[182:185], v[10:13]
	v_mfma_f32_16x16x32_bf16 v[6:9], v[214:217], v[190:193], v[6:9]
	v_mfma_f32_16x16x32_bf16 v[2:5], v[222:225], v[190:193], v[2:5]
	v_mfma_f32_16x16x32_bf16 v[54:57], v[214:217], v[198:201], v[54:57]
	v_mfma_f32_16x16x32_bf16 v[66:69], v[222:225], v[198:201], v[66:69]
	v_mfma_f32_16x16x32_bf16 v[50:53], v[214:217], v[206:209], v[50:53]
	v_mfma_f32_16x16x32_bf16 v[58:61], v[222:225], v[206:209], v[58:61]
	s_nop 0
	s_add_i32 s88, s88, 2
	s_add_u32 s4, s4, 0x100
	s_addc_u32 s5, s5, 0
	s_cmp_gt_u32 s88, 5
	s_barrier
	s_cbranch_scc0 .LBB0_2223
	v_add_u32_e32 v138, s82, v137
	v_add_u32_e32 v140, s81, v151
	v_ashrrev_i32_e32 v141, 31, v140
	v_ashrrev_i32_e32 v139, 31, v138
	v_lshl_add_u64 v[140:141], v[140:141], 1, s[12:13]
	v_cvt_pk_bf16_f32 v126, v126, v127
	v_cvt_pk_bf16_f32 v127, v128, v129
	v_cvt_pk_bf16_f32 v128, v122, v123
	v_lshlrev_b64 v[122:123], 12, v[138:139]
	v_lshl_add_u64 v[122:123], v[140:141], 0, v[122:123]
	v_cvt_pk_bf16_f32 v118, v118, v119
	v_cvt_pk_bf16_f32 v119, v120, v121
	v_cvt_pk_bf16_f32 v121, v116, v117
	v_add_co_u32_e32 v116, vcc, s48, v122
	v_cvt_pk_bf16_f32 v110, v110, v111
	s_nop 0
	v_addc_co_u32_e32 v117, vcc, 0, v123, vcc
	v_cvt_pk_bf16_f32 v111, v112, v113
	v_cvt_pk_bf16_f32 v113, v108, v109
	v_add_co_u32_e32 v108, vcc, s75, v122
	v_cvt_pk_bf16_f32 v102, v102, v103
	s_nop 0
	v_addc_co_u32_e32 v109, vcc, 0, v123, vcc
	v_cvt_pk_bf16_f32 v103, v104, v105
	v_cvt_pk_bf16_f32 v105, v100, v101
	v_add_co_u32_e32 v100, vcc, s76, v122
	v_cvt_pk_bf16_f32 v94, v94, v95
	s_nop 0
	v_addc_co_u32_e32 v101, vcc, 0, v123, vcc
	v_cvt_pk_bf16_f32 v95, v96, v97
	v_cvt_pk_bf16_f32 v97, v92, v93
	v_add_co_u32_e32 v92, vcc, s77, v122
	v_cvt_pk_bf16_f32 v82, v82, v83
	s_nop 0
	v_addc_co_u32_e32 v93, vcc, 0, v123, vcc
	v_cvt_pk_bf16_f32 v83, v84, v85
	v_cvt_pk_bf16_f32 v85, v76, v77
	v_add_co_u32_e32 v76, vcc, s78, v122
	v_cvt_pk_bf16_f32 v46, v46, v47
	s_nop 0
	v_addc_co_u32_e32 v77, vcc, 0, v123, vcc
	v_cvt_pk_bf16_f32 v47, v48, v49
	v_cvt_pk_bf16_f32 v49, v44, v45
	v_add_co_u32_e32 v44, vcc, s79, v122
	v_cvt_pk_bf16_f32 v30, v30, v31
	s_nop 0
	v_addc_co_u32_e32 v45, vcc, 0, v123, vcc
	v_cvt_pk_bf16_f32 v31, v32, v33
	v_cvt_pk_bf16_f32 v32, v22, v23
	v_add_co_u32_e32 v22, vcc, s80, v122
	v_cvt_pk_bf16_f32 v33, v24, v25
	s_nop 0
	v_addc_co_u32_e32 v23, vcc, 0, v123, vcc
	global_store_dwordx4 v[22:23], v[30:33], off
	v_cvt_pk_bf16_f32 v22, v86, v87
	v_cvt_pk_bf16_f32 v23, v88, v89
	v_cvt_pk_bf16_f32 v24, v78, v79
	v_cvt_pk_bf16_f32 v25, v80, v81
	v_cvt_pk_bf16_f32 v120, v114, v115
	v_lshl_add_u64 v[114:115], v[122:123], 0, s[18:19]
	global_store_dwordx4 v[122:123], v[22:25], off offset:256
	v_cvt_pk_bf16_f32 v112, v106, v107
	v_lshl_add_u64 v[106:107], v[122:123], 0, s[10:11]
	v_cvt_pk_bf16_f32 v22, v70, v71
	v_cvt_pk_bf16_f32 v23, v72, v73
	v_cvt_pk_bf16_f32 v24, v62, v63
	v_cvt_pk_bf16_f32 v25, v64, v65
	v_cvt_pk_bf16_f32 v48, v42, v43
	v_lshl_add_u64 v[42:43], v[122:123], 0, s[26:27]
	global_store_dwordx4 v[114:115], v[22:25], off offset:256
	v_cvt_pk_bf16_f32 v6, v6, v7
	v_cvt_pk_bf16_f32 v7, v8, v9
	v_cvt_pk_bf16_f32 v22, v38, v39
	v_cvt_pk_bf16_f32 v23, v40, v41
	v_cvt_pk_bf16_f32 v24, v34, v35
	v_cvt_pk_bf16_f32 v25, v36, v37
	v_cvt_pk_bf16_f32 v8, v2, v3
	v_cvt_pk_bf16_f32 v9, v4, v5
	v_cvt_pk_bf16_f32 v2, v54, v55
	v_cvt_pk_bf16_f32 v3, v56, v57
	v_cvt_pk_bf16_f32 v4, v66, v67
	v_cvt_pk_bf16_f32 v5, v68, v69
	v_cvt_pk_bf16_f32 v129, v124, v125
	v_cvt_pk_bf16_f32 v104, v98, v99
	v_lshl_add_u64 v[98:99], v[122:123], 0, s[20:21]
	v_cvt_pk_bf16_f32 v96, v90, v91
	v_lshl_add_u64 v[90:91], v[122:123], 0, s[22:23]
	v_cvt_pk_bf16_f32 v84, v74, v75
	v_lshl_add_u64 v[74:75], v[122:123], 0, s[24:25]
	global_store_dwordx4 v[44:45], v[46:49], off
	v_lshl_add_u64 v[44:45], v[122:123], 0, s[28:29]
	global_store_dwordx4 v[106:107], v[22:25], off offset:256
	v_cvt_pk_bf16_f32 v14, v14, v15
	v_cvt_pk_bf16_f32 v15, v16, v17
	v_cvt_pk_bf16_f32 v22, v26, v27
	v_cvt_pk_bf16_f32 v23, v28, v29
	v_cvt_pk_bf16_f32 v24, v18, v19
	v_cvt_pk_bf16_f32 v25, v20, v21
	v_cvt_pk_bf16_f32 v16, v10, v11
	v_cvt_pk_bf16_f32 v17, v12, v13
	global_store_dwordx4 v[42:43], v[2:5], off offset:256
	s_and_b64 vcc, exec, s[0:1]
	v_mov_b32_e32 v136, v159
	v_cvt_pk_bf16_f32 v2, v50, v51
	v_cvt_pk_bf16_f32 v3, v52, v53
	v_cvt_pk_bf16_f32 v4, v58, v59
	v_cvt_pk_bf16_f32 v5, v60, v61
	v_mov_b32_e32 v156, v157
	v_mov_b32_e32 v140, v160
	v_mov_b32_e32 v138, v158
	s_mov_b32 s81, s83
	s_mov_b32 s82, s84
	s_mov_b64 s[36:37], s[34:35]
	global_store_dwordx4 v[122:123], v[126:129], off
	global_store_dwordx4 v[116:117], v[118:121], off
	global_store_dwordx4 v[108:109], v[110:113], off
	global_store_dwordx4 v[100:101], v[102:105], off
	global_store_dwordx4 v[92:93], v[94:97], off
	global_store_dwordx4 v[76:77], v[82:85], off
	global_store_dwordx4 v[98:99], v[22:25], off offset:256
	global_store_dwordx4 v[90:91], v[14:17], off offset:256
	global_store_dwordx4 v[74:75], v[6:9], off offset:256
	global_store_dwordx4 v[44:45], v[2:5], off offset:256
	s_cbranch_vccz .LBB0_2218
	s_waitcnt vmcnt(0)
	v_readlane_b32 s72, v255, 2
	s_cmpk_gt_u32 s40, 0xff
	v_readlane_b32 s73, v255, 3
	v_readlane_b32 s71, v255, 4
	s_cbranch_scc1 .LBB0_2227
	s_barrier
